# GEMM K-loops: s_setprio roles inverted (the loading wave half gets priority 1, the computing half 0)
# speedup vs baseline: 1.0094x; 1.0031x over previous
.LBB0_378:
	s_add_u32 s28, s36, 0xfff80080
	s_addc_u32 s29, s37, -1
	s_add_i32 s42, 0, 0x10000
	s_cmp_eq_u32 vcc_hi, 28
	s_cselect_b32 s53, s11, s29
	s_cselect_b32 s52, s21, s28
	s_cselect_b32 s51, s41, s79
	s_cselect_b32 s50, vcc_lo, s78
	s_add_i32 s43, 0, 0x14000
	v_add_u32_e32 v140, s42, v169
	v_add_u32_e32 v173, s43, v169
	ds_read_b128 v[128:131], v140
	ds_read_b128 v[132:135], v140 offset:1024
	ds_read_b128 v[136:139], v140 offset:2048
	ds_read_b128 v[140:143], v140 offset:3072
	ds_read_b128 v[156:159], v173
	ds_read_b128 v[160:163], v173 offset:1024
	ds_read_b128 v[164:167], v173 offset:2048
	ds_read_b128 v[174:177], v173 offset:3072
	v_lshl_add_u64 v[182:183], s[36:37], 0, v[152:153]
	s_add_i32 m0, s88, 0xc000
	ds_read_b128 v[178:181], v172
	ds_read_b128 v[194:197], v172 offset:1024
	ds_read_b128 v[198:201], v172 offset:2048
	ds_read_b128 v[202:205], v172 offset:3072
	ds_read_b128 v[206:209], v172 offset:4096
	ds_read_b128 v[224:227], v172 offset:5120
	ds_read_b128 v[228:231], v172 offset:6144
	ds_read_b128 v[232:235], v172 offset:7168
	global_load_lds_dwordx4 v[182:183], off
	v_lshl_add_u64 v[182:183], s[36:37], 0, v[154:155]
	s_add_i32 m0, s88, 0xe000
	s_nop 0
	global_load_lds_dwordx4 v[182:183], off
	s_waitcnt vmcnt(8)
	s_waitcnt lgkmcnt(0)
	s_barrier
	s_setprio 0
	s_waitcnt lgkmcnt(0)
	v_mfma_f32_16x16x32_bf16 v[124:127], v[128:131], v[178:181], v[124:127]
	v_mfma_f32_16x16x32_bf16 v[120:123], v[136:139], v[178:181], v[120:123]
	v_mfma_f32_16x16x32_bf16 v[116:119], v[128:131], v[198:201], v[116:119]
	v_mfma_f32_16x16x32_bf16 v[108:111], v[136:139], v[198:201], v[108:111]
	v_mfma_f32_16x16x32_bf16 v[100:103], v[128:131], v[206:209], v[100:103]
	v_mfma_f32_16x16x32_bf16 v[92:95], v[136:139], v[206:209], v[92:95]
	v_mfma_f32_16x16x32_bf16 v[84:87], v[128:131], v[228:231], v[84:87]
	v_mfma_f32_16x16x32_bf16 v[76:79], v[136:139], v[228:231], v[76:79]
	v_mfma_f32_16x16x32_bf16 v[124:127], v[132:135], v[194:197], v[124:127]
	v_mfma_f32_16x16x32_bf16 v[120:123], v[140:143], v[194:197], v[120:123]
	v_mfma_f32_16x16x32_bf16 v[116:119], v[132:135], v[202:205], v[116:119]
	v_mfma_f32_16x16x32_bf16 v[108:111], v[140:143], v[202:205], v[108:111]
	v_mfma_f32_16x16x32_bf16 v[100:103], v[132:135], v[224:227], v[100:103]
	v_mfma_f32_16x16x32_bf16 v[92:95], v[140:143], v[224:227], v[92:95]
	v_mfma_f32_16x16x32_bf16 v[84:87], v[132:135], v[232:235], v[84:87]
	v_mfma_f32_16x16x32_bf16 v[76:79], v[140:143], v[232:235], v[76:79]
	s_setprio 1
	s_setprio 0
	v_mfma_f32_16x16x32_bf16 v[112:115], v[156:159], v[178:181], v[112:115]
	v_mfma_f32_16x16x32_bf16 v[104:107], v[164:167], v[178:181], v[104:107]
	v_mfma_f32_16x16x32_bf16 v[96:99], v[156:159], v[198:201], v[96:99]
	v_mfma_f32_16x16x32_bf16 v[88:91], v[164:167], v[198:201], v[88:91]
	v_mfma_f32_16x16x32_bf16 v[80:83], v[156:159], v[206:209], v[80:83]
	v_mfma_f32_16x16x32_bf16 v[72:75], v[164:167], v[206:209], v[72:75]
	v_mfma_f32_16x16x32_bf16 v[68:71], v[156:159], v[228:231], v[68:71]
	v_mfma_f32_16x16x32_bf16 v[64:67], v[164:167], v[228:231], v[64:67]
	v_mfma_f32_16x16x32_bf16 v[112:115], v[160:163], v[194:197], v[112:115]
	v_mfma_f32_16x16x32_bf16 v[104:107], v[174:177], v[194:197], v[104:107]
	v_mfma_f32_16x16x32_bf16 v[96:99], v[160:163], v[202:205], v[96:99]
	v_mfma_f32_16x16x32_bf16 v[88:91], v[174:177], v[202:205], v[88:91]
	v_mfma_f32_16x16x32_bf16 v[80:83], v[160:163], v[224:227], v[80:83]
	v_mfma_f32_16x16x32_bf16 v[72:75], v[174:177], v[224:227], v[72:75]
	v_mfma_f32_16x16x32_bf16 v[68:71], v[160:163], v[232:235], v[68:71]
	v_mfma_f32_16x16x32_bf16 v[64:67], v[174:177], v[232:235], v[64:67]
	s_setprio 1
	s_barrier
	s_add_i32 s28, s42, s62
	v_lshl_add_u64 v[182:183], s[50:51], 0, v[146:147]
	s_mov_b32 m0, s28
	ds_read_b128 v[178:181], v172 offset:16384
	ds_read_b128 v[194:197], v172 offset:17408
	ds_read_b128 v[198:201], v172 offset:18432
	ds_read_b128 v[202:205], v172 offset:19456
	ds_read_b128 v[206:209], v172 offset:20480
	ds_read_b128 v[224:227], v172 offset:21504
	ds_read_b128 v[228:231], v172 offset:22528
	ds_read_b128 v[232:235], v172 offset:23552
	global_load_lds_dwordx4 v[182:183], off
	s_add_i32 m0, s28, 0x2000
	s_add_u32 s28, s50, 0x80000
	v_lshl_add_u64 v[210:211], s[50:51], 0, v[150:151]
	s_addc_u32 s29, s51, 0
	s_add_i32 s42, s43, s62
	global_load_lds_dwordx4 v[210:211], off
	v_lshl_add_u64 v[236:237], s[28:29], 0, v[146:147]
	s_mov_b32 m0, s42
	v_lshl_add_u64 v[238:239], s[52:53], 0, v[148:149]
	global_load_lds_dwordx4 v[236:237], off
	v_lshl_add_u64 v[236:237], s[28:29], 0, v[150:151]
	s_add_i32 m0, s42, 0x2000
	s_nop 0
	global_load_lds_dwordx4 v[236:237], off
	v_lshl_add_u64 v[236:237], s[52:53], 0, v[144:145]
	s_mov_b32 m0, s88
	s_nop 0
	global_load_lds_dwordx4 v[236:237], off
	s_mov_b32 m0, s89
	s_nop 0
	global_load_lds_dwordx4 v[238:239], off
	s_waitcnt vmcnt(8)
	s_waitcnt lgkmcnt(0)
	s_barrier
	s_setprio 0
	s_waitcnt lgkmcnt(0)
	v_mfma_f32_16x16x32_bf16 v[60:63], v[128:131], v[178:181], v[60:63]
	v_mfma_f32_16x16x32_bf16 v[56:59], v[136:139], v[178:181], v[56:59]
	v_mfma_f32_16x16x32_bf16 v[52:55], v[128:131], v[198:201], v[52:55]
	v_mfma_f32_16x16x32_bf16 v[44:47], v[136:139], v[198:201], v[44:47]
	v_mfma_f32_16x16x32_bf16 v[36:39], v[128:131], v[206:209], v[36:39]
	v_mfma_f32_16x16x32_bf16 v[28:31], v[136:139], v[206:209], v[28:31]
	v_mfma_f32_16x16x32_bf16 v[20:23], v[128:131], v[228:231], v[20:23]
	v_mfma_f32_16x16x32_bf16 v[12:15], v[136:139], v[228:231], v[12:15]
	v_mfma_f32_16x16x32_bf16 v[60:63], v[132:135], v[194:197], v[60:63]
	v_mfma_f32_16x16x32_bf16 v[56:59], v[140:143], v[194:197], v[56:59]
	v_mfma_f32_16x16x32_bf16 v[52:55], v[132:135], v[202:205], v[52:55]
	v_mfma_f32_16x16x32_bf16 v[44:47], v[140:143], v[202:205], v[44:47]
	v_mfma_f32_16x16x32_bf16 v[36:39], v[132:135], v[224:227], v[36:39]
	v_mfma_f32_16x16x32_bf16 v[28:31], v[140:143], v[224:227], v[28:31]
	v_mfma_f32_16x16x32_bf16 v[20:23], v[132:135], v[232:235], v[20:23]
	v_mfma_f32_16x16x32_bf16 v[12:15], v[140:143], v[232:235], v[12:15]
	s_setprio 1
	s_setprio 0
	v_mfma_f32_16x16x32_bf16 v[48:51], v[156:159], v[178:181], v[48:51]
	v_mfma_f32_16x16x32_bf16 v[40:43], v[164:167], v[178:181], v[40:43]
	v_mfma_f32_16x16x32_bf16 v[32:35], v[156:159], v[198:201], v[32:35]
	v_mfma_f32_16x16x32_bf16 v[24:27], v[164:167], v[198:201], v[24:27]
	v_mfma_f32_16x16x32_bf16 v[16:19], v[156:159], v[206:209], v[16:19]
	v_mfma_f32_16x16x32_bf16 v[8:11], v[164:167], v[206:209], v[8:11]
	v_mfma_f32_16x16x32_bf16 v[4:7], v[156:159], v[228:231], v[4:7]
	v_mfma_f32_16x16x32_bf16 v[0:3], v[164:167], v[228:231], v[0:3]
	v_mfma_f32_16x16x32_bf16 v[48:51], v[160:163], v[194:197], v[48:51]
	v_mfma_f32_16x16x32_bf16 v[40:43], v[174:177], v[194:197], v[40:43]
	v_mfma_f32_16x16x32_bf16 v[32:35], v[160:163], v[202:205], v[32:35]
	v_mfma_f32_16x16x32_bf16 v[24:27], v[174:177], v[202:205], v[24:27]
	v_mfma_f32_16x16x32_bf16 v[16:19], v[160:163], v[224:227], v[16:19]
	v_mfma_f32_16x16x32_bf16 v[8:11], v[174:177], v[224:227], v[8:11]
	v_mfma_f32_16x16x32_bf16 v[4:7], v[160:163], v[232:235], v[4:7]
	v_mfma_f32_16x16x32_bf16 v[0:3], v[174:177], v[232:235], v[0:3]
	s_setprio 1
	s_barrier
	s_add_i32 s42, 0, 0x18000
	s_add_i32 s43, 0, 0x1c000
	v_add_u32_e32 v140, s42, v169
	v_add_u32_e32 v173, s43, v169
	ds_read_b128 v[128:131], v140
	ds_read_b128 v[132:135], v140 offset:1024
	ds_read_b128 v[136:139], v140 offset:2048
	ds_read_b128 v[140:143], v140 offset:3072
	ds_read_b128 v[156:159], v173
	ds_read_b128 v[160:163], v173 offset:1024
	ds_read_b128 v[164:167], v173 offset:2048
	ds_read_b128 v[174:177], v173 offset:3072
	s_add_u32 s28, s52, 0x80000
	s_addc_u32 s29, s53, 0
	s_mov_b32 m0, s26
	v_lshl_add_u64 v[240:241], s[28:29], 0, v[144:145]
	ds_read_b128 v[178:181], v172 offset:32768
	ds_read_b128 v[194:197], v172 offset:33792
	ds_read_b128 v[198:201], v172 offset:34816
	ds_read_b128 v[202:205], v172 offset:35840
	ds_read_b128 v[206:209], v172 offset:36864
	ds_read_b128 v[224:227], v172 offset:37888
	ds_read_b128 v[228:231], v172 offset:38912
	ds_read_b128 v[232:235], v172 offset:39936
	global_load_lds_dwordx4 v[240:241], off
	v_lshl_add_u64 v[240:241], s[28:29], 0, v[148:149]
	s_mov_b32 m0, s27
	s_nop 0
	global_load_lds_dwordx4 v[240:241], off
	s_waitcnt vmcnt(8)
	s_waitcnt lgkmcnt(0)
	s_barrier
	s_setprio 0
	s_waitcnt lgkmcnt(0)
	v_mfma_f32_16x16x32_bf16 v[124:127], v[128:131], v[178:181], v[124:127]
	v_mfma_f32_16x16x32_bf16 v[120:123], v[136:139], v[178:181], v[120:123]
	v_mfma_f32_16x16x32_bf16 v[116:119], v[128:131], v[198:201], v[116:119]
	v_mfma_f32_16x16x32_bf16 v[108:111], v[136:139], v[198:201], v[108:111]
	v_mfma_f32_16x16x32_bf16 v[100:103], v[128:131], v[206:209], v[100:103]
	v_mfma_f32_16x16x32_bf16 v[92:95], v[136:139], v[206:209], v[92:95]
	v_mfma_f32_16x16x32_bf16 v[84:87], v[128:131], v[228:231], v[84:87]
	v_mfma_f32_16x16x32_bf16 v[76:79], v[136:139], v[228:231], v[76:79]
	v_mfma_f32_16x16x32_bf16 v[124:127], v[132:135], v[194:197], v[124:127]
	v_mfma_f32_16x16x32_bf16 v[120:123], v[140:143], v[194:197], v[120:123]
	v_mfma_f32_16x16x32_bf16 v[116:119], v[132:135], v[202:205], v[116:119]
	v_mfma_f32_16x16x32_bf16 v[108:111], v[140:143], v[202:205], v[108:111]
	v_mfma_f32_16x16x32_bf16 v[100:103], v[132:135], v[224:227], v[100:103]
	v_mfma_f32_16x16x32_bf16 v[92:95], v[140:143], v[224:227], v[92:95]
	v_mfma_f32_16x16x32_bf16 v[84:87], v[132:135], v[232:235], v[84:87]
	v_mfma_f32_16x16x32_bf16 v[76:79], v[140:143], v[232:235], v[76:79]
	s_setprio 1
	s_setprio 0
	v_mfma_f32_16x16x32_bf16 v[112:115], v[156:159], v[178:181], v[112:115]
	v_mfma_f32_16x16x32_bf16 v[104:107], v[164:167], v[178:181], v[104:107]
	v_mfma_f32_16x16x32_bf16 v[96:99], v[156:159], v[198:201], v[96:99]
	v_mfma_f32_16x16x32_bf16 v[88:91], v[164:167], v[198:201], v[88:91]
	v_mfma_f32_16x16x32_bf16 v[80:83], v[156:159], v[206:209], v[80:83]
	v_mfma_f32_16x16x32_bf16 v[72:75], v[164:167], v[206:209], v[72:75]
	v_mfma_f32_16x16x32_bf16 v[68:71], v[156:159], v[228:231], v[68:71]
	v_mfma_f32_16x16x32_bf16 v[64:67], v[164:167], v[228:231], v[64:67]
	v_mfma_f32_16x16x32_bf16 v[112:115], v[160:163], v[194:197], v[112:115]
	v_mfma_f32_16x16x32_bf16 v[104:107], v[174:177], v[194:197], v[104:107]
	v_mfma_f32_16x16x32_bf16 v[96:99], v[160:163], v[202:205], v[96:99]
	v_mfma_f32_16x16x32_bf16 v[88:91], v[174:177], v[202:205], v[88:91]
	v_mfma_f32_16x16x32_bf16 v[80:83], v[160:163], v[224:227], v[80:83]
	v_mfma_f32_16x16x32_bf16 v[72:75], v[174:177], v[224:227], v[72:75]
	v_mfma_f32_16x16x32_bf16 v[68:71], v[160:163], v[232:235], v[68:71]
	v_mfma_f32_16x16x32_bf16 v[64:67], v[174:177], v[232:235], v[64:67]
	s_setprio 1
	s_barrier
	s_add_i32 s28, s42, s62
	v_lshl_add_u64 v[182:183], v[182:183], 0, s[68:69]
	s_mov_b32 m0, s28
	ds_read_b128 v[178:181], v172 offset:49152
	ds_read_b128 v[194:197], v172 offset:50176
	ds_read_b128 v[198:201], v172 offset:51200
	ds_read_b128 v[202:205], v172 offset:52224
	ds_read_b128 v[206:209], v172 offset:53248
	ds_read_b128 v[224:227], v172 offset:54272
	ds_read_b128 v[228:231], v172 offset:55296
	ds_read_b128 v[232:235], v172 offset:56320
	global_load_lds_dwordx4 v[182:183], off
	s_add_i32 m0, s28, 0x2000
	s_add_u32 s28, s50, 0x80080
	v_lshl_add_u64 v[182:183], v[210:211], 0, s[68:69]
	s_addc_u32 s29, s51, 0
	s_add_i32 s42, s43, s62
	global_load_lds_dwordx4 v[182:183], off
	v_lshl_add_u64 v[182:183], s[28:29], 0, v[146:147]
	s_mov_b32 m0, s42
	s_nop 0
	global_load_lds_dwordx4 v[182:183], off
	v_lshl_add_u64 v[182:183], s[28:29], 0, v[150:151]
	s_add_i32 m0, s42, 0x2000
	s_nop 0
	global_load_lds_dwordx4 v[182:183], off
	v_lshl_add_u64 v[182:183], v[236:237], 0, s[68:69]
	s_mov_b32 m0, s94
	s_nop 0
	global_load_lds_dwordx4 v[182:183], off
	v_lshl_add_u64 v[182:183], v[238:239], 0, s[68:69]
	s_mov_b32 m0, s95
	s_nop 0
	global_load_lds_dwordx4 v[182:183], off
	s_waitcnt vmcnt(8)
	s_waitcnt lgkmcnt(0)
	s_barrier
	s_setprio 0
	s_waitcnt lgkmcnt(0)
	v_mfma_f32_16x16x32_bf16 v[60:63], v[128:131], v[178:181], v[60:63]
	v_mfma_f32_16x16x32_bf16 v[56:59], v[136:139], v[178:181], v[56:59]
	v_mfma_f32_16x16x32_bf16 v[52:55], v[128:131], v[198:201], v[52:55]
	v_mfma_f32_16x16x32_bf16 v[44:47], v[136:139], v[198:201], v[44:47]
	v_mfma_f32_16x16x32_bf16 v[36:39], v[128:131], v[206:209], v[36:39]
	v_mfma_f32_16x16x32_bf16 v[28:31], v[136:139], v[206:209], v[28:31]
	v_mfma_f32_16x16x32_bf16 v[20:23], v[128:131], v[228:231], v[20:23]
	v_mfma_f32_16x16x32_bf16 v[12:15], v[136:139], v[228:231], v[12:15]
	v_mfma_f32_16x16x32_bf16 v[60:63], v[132:135], v[194:197], v[60:63]
	v_mfma_f32_16x16x32_bf16 v[56:59], v[140:143], v[194:197], v[56:59]
	v_mfma_f32_16x16x32_bf16 v[52:55], v[132:135], v[202:205], v[52:55]
	v_mfma_f32_16x16x32_bf16 v[44:47], v[140:143], v[202:205], v[44:47]
	v_mfma_f32_16x16x32_bf16 v[36:39], v[132:135], v[224:227], v[36:39]
	v_mfma_f32_16x16x32_bf16 v[28:31], v[140:143], v[224:227], v[28:31]
	v_mfma_f32_16x16x32_bf16 v[20:23], v[132:135], v[232:235], v[20:23]
	v_mfma_f32_16x16x32_bf16 v[12:15], v[140:143], v[232:235], v[12:15]
	s_setprio 1
	s_setprio 0
	v_mfma_f32_16x16x32_bf16 v[48:51], v[156:159], v[178:181], v[48:51]
	v_mfma_f32_16x16x32_bf16 v[40:43], v[164:167], v[178:181], v[40:43]
	v_mfma_f32_16x16x32_bf16 v[32:35], v[156:159], v[198:201], v[32:35]
	v_mfma_f32_16x16x32_bf16 v[24:27], v[164:167], v[198:201], v[24:27]
	v_mfma_f32_16x16x32_bf16 v[16:19], v[156:159], v[206:209], v[16:19]
	v_mfma_f32_16x16x32_bf16 v[8:11], v[164:167], v[206:209], v[8:11]
	v_mfma_f32_16x16x32_bf16 v[4:7], v[156:159], v[228:231], v[4:7]
	v_mfma_f32_16x16x32_bf16 v[0:3], v[164:167], v[228:231], v[0:3]
	v_mfma_f32_16x16x32_bf16 v[48:51], v[160:163], v[194:197], v[48:51]
	v_mfma_f32_16x16x32_bf16 v[40:43], v[174:177], v[194:197], v[40:43]
	v_mfma_f32_16x16x32_bf16 v[32:35], v[160:163], v[202:205], v[32:35]
	v_mfma_f32_16x16x32_bf16 v[24:27], v[174:177], v[202:205], v[24:27]
	v_mfma_f32_16x16x32_bf16 v[16:19], v[160:163], v[224:227], v[16:19]
	v_mfma_f32_16x16x32_bf16 v[8:11], v[174:177], v[224:227], v[8:11]
	v_mfma_f32_16x16x32_bf16 v[4:7], v[160:163], v[232:235], v[4:7]
	v_mfma_f32_16x16x32_bf16 v[0:3], v[174:177], v[232:235], v[0:3]
	s_setprio 1
	s_barrier
	s_add_i32 vcc_hi, vcc_hi, 2
	s_add_u32 s36, s36, 0x100
	s_addc_u32 s37, s37, 0
	s_add_u32 s78, s78, 0x100
	s_addc_u32 s79, s79, 0
	s_cmp_gt_u32 vcc_hi, 29
	s_cbranch_scc0 .LBB0_378
	s_and_b64 vcc, exec, s[14:15]
	s_cbranch_vccz .LBB0_381
	s_barrier

.LBB0_514:
	s_add_u32 s42, s30, s44
	s_addc_u32 s43, s31, 0
	s_add_u32 s40, s42, 0x100
	s_addc_u32 s41, s43, 0
	s_and_b64 s[28:29], s[38:39], exec
	s_cselect_b32 s41, s9, s41
	s_cselect_b32 s40, s63, s40
	s_add_u32 s28, s18, s44
	s_addc_u32 s29, s19, 0
	s_add_u32 s44, s28, 0x100
	s_addc_u32 s45, s29, 0
	s_add_i32 s76, 0, 0x10000
	s_and_b64 s[28:29], s[38:39], exec
	s_cselect_b32 s44, s79, s44
	s_cselect_b32 s45, s78, s45
	s_add_i32 s85, 0, 0x14000
	v_add_u32_e32 v158, s76, v136
	v_add_u32_e32 v174, s85, v136
	ds_read_b128 v[146:149], v158
	ds_read_b128 v[150:153], v158 offset:1024
	ds_read_b128 v[154:157], v158 offset:2048
	ds_read_b128 v[158:161], v158 offset:3072
	ds_read_b128 v[162:165], v174
	ds_read_b128 v[166:169], v174 offset:1024
	ds_read_b128 v[170:173], v174 offset:2048
	ds_read_b128 v[174:177], v174 offset:3072
	s_add_u32 s46, s42, 0x10080
	s_addc_u32 s47, s43, 0
	s_add_i32 s29, s76, s4
	s_add_i32 s43, s85, s4
	s_add_i32 m0, s20, 0xc000
	s_add_i32 s90, s20, 0xe000
	s_add_i32 s49, s29, 0x2000
	s_add_i32 s42, s43, 0x2000
	s_add_i32 s48, 0, 0x18000
	s_add_i32 s28, 0, 0x1c000
	s_add_u32 s38, s40, 0x10000
	s_addc_u32 s39, s41, 0
	s_add_i32 s88, s48, s4
	s_add_i32 s76, s28, s4
	s_add_i32 s89, s88, 0x2000
	s_add_i32 s85, s76, 0x2000
	v_lshl_add_u64 v[182:183], s[46:47], 0, v[134:135]
	ds_read_b128 v[178:181], v145
	ds_read_b128 v[194:197], v145 offset:1024
	ds_read_b128 v[198:201], v145 offset:2048
	ds_read_b128 v[202:205], v145 offset:3072
	ds_read_b128 v[206:209], v145 offset:4096
	ds_read_b128 v[224:227], v145 offset:5120
	ds_read_b128 v[228:231], v145 offset:6144
	ds_read_b128 v[232:235], v145 offset:7168
	global_load_lds_dwordx4 v[182:183], off
	v_lshl_add_u64 v[182:183], s[46:47], 0, v[130:131]
	s_mov_b32 m0, s90
	s_nop 0
	global_load_lds_dwordx4 v[182:183], off
	s_waitcnt vmcnt(8)
	s_waitcnt lgkmcnt(0)
	s_barrier
	s_setprio 0
	s_waitcnt lgkmcnt(0)
	v_mfma_f32_16x16x32_bf16 v[124:127], v[146:149], v[178:181], v[124:127]
	v_mfma_f32_16x16x32_bf16 v[120:123], v[154:157], v[178:181], v[120:123]
	v_mfma_f32_16x16x32_bf16 v[112:115], v[146:149], v[198:201], v[112:115]
	v_mfma_f32_16x16x32_bf16 v[104:107], v[154:157], v[198:201], v[104:107]
	v_mfma_f32_16x16x32_bf16 v[96:99], v[146:149], v[206:209], v[96:99]
	v_mfma_f32_16x16x32_bf16 v[88:91], v[154:157], v[206:209], v[88:91]
	v_mfma_f32_16x16x32_bf16 v[80:83], v[146:149], v[228:231], v[80:83]
	v_mfma_f32_16x16x32_bf16 v[72:75], v[154:157], v[228:231], v[72:75]
	v_mfma_f32_16x16x32_bf16 v[124:127], v[150:153], v[194:197], v[124:127]
	v_mfma_f32_16x16x32_bf16 v[120:123], v[158:161], v[194:197], v[120:123]
	v_mfma_f32_16x16x32_bf16 v[112:115], v[150:153], v[202:205], v[112:115]
	v_mfma_f32_16x16x32_bf16 v[104:107], v[158:161], v[202:205], v[104:107]
	v_mfma_f32_16x16x32_bf16 v[96:99], v[150:153], v[224:227], v[96:99]
	v_mfma_f32_16x16x32_bf16 v[88:91], v[158:161], v[224:227], v[88:91]
	v_mfma_f32_16x16x32_bf16 v[80:83], v[150:153], v[232:235], v[80:83]
	v_mfma_f32_16x16x32_bf16 v[72:75], v[158:161], v[232:235], v[72:75]
	s_setprio 1
	s_setprio 0
	v_mfma_f32_16x16x32_bf16 v[116:119], v[162:165], v[178:181], v[116:119]
	v_mfma_f32_16x16x32_bf16 v[108:111], v[170:173], v[178:181], v[108:111]
	v_mfma_f32_16x16x32_bf16 v[100:103], v[162:165], v[198:201], v[100:103]
	v_mfma_f32_16x16x32_bf16 v[92:95], v[170:173], v[198:201], v[92:95]
	v_mfma_f32_16x16x32_bf16 v[84:87], v[162:165], v[206:209], v[84:87]
	v_mfma_f32_16x16x32_bf16 v[76:79], v[170:173], v[206:209], v[76:79]
	v_mfma_f32_16x16x32_bf16 v[68:71], v[162:165], v[228:231], v[68:71]
	v_mfma_f32_16x16x32_bf16 v[64:67], v[170:173], v[228:231], v[64:67]
	v_mfma_f32_16x16x32_bf16 v[116:119], v[166:169], v[194:197], v[116:119]
	v_mfma_f32_16x16x32_bf16 v[108:111], v[174:177], v[194:197], v[108:111]
	v_mfma_f32_16x16x32_bf16 v[100:103], v[166:169], v[202:205], v[100:103]
	v_mfma_f32_16x16x32_bf16 v[92:95], v[174:177], v[202:205], v[92:95]
	v_mfma_f32_16x16x32_bf16 v[84:87], v[166:169], v[224:227], v[84:87]
	v_mfma_f32_16x16x32_bf16 v[76:79], v[174:177], v[224:227], v[76:79]
	v_mfma_f32_16x16x32_bf16 v[68:71], v[166:169], v[232:235], v[68:71]
	v_mfma_f32_16x16x32_bf16 v[64:67], v[174:177], v[232:235], v[64:67]
	s_setprio 1
	s_barrier
	s_mov_b32 m0, s29
	v_lshl_add_u64 v[182:183], s[44:45], 0, v[132:133]
	ds_read_b128 v[178:181], v145 offset:16384
	ds_read_b128 v[194:197], v145 offset:17408
	ds_read_b128 v[198:201], v145 offset:18432
	ds_read_b128 v[202:205], v145 offset:19456
	ds_read_b128 v[206:209], v145 offset:20480
	ds_read_b128 v[224:227], v145 offset:21504
	ds_read_b128 v[228:231], v145 offset:22528
	ds_read_b128 v[232:235], v145 offset:23552
	global_load_lds_dwordx4 v[182:183], off
	v_lshl_add_u64 v[210:211], s[44:45], 0, v[128:129]
	s_mov_b32 m0, s49
	v_lshl_add_u64 v[236:237], v[182:183], 0, s[70:71]
	global_load_lds_dwordx4 v[210:211], off
	s_mov_b32 m0, s43
	v_lshl_add_u64 v[238:239], s[40:41], 0, v[130:131]
	global_load_lds_dwordx4 v[236:237], off
	v_lshl_add_u64 v[236:237], v[210:211], 0, s[70:71]
	s_mov_b32 m0, s42
	s_nop 0
	global_load_lds_dwordx4 v[236:237], off
	v_lshl_add_u64 v[236:237], s[40:41], 0, v[134:135]
	s_mov_b32 m0, s20
	s_nop 0
	global_load_lds_dwordx4 v[236:237], off
	s_mov_b32 m0, s21
	s_nop 0
	global_load_lds_dwordx4 v[238:239], off
	s_waitcnt vmcnt(8)
	s_waitcnt lgkmcnt(0)
	s_barrier
	s_setprio 0
	s_waitcnt lgkmcnt(0)
	v_mfma_f32_16x16x32_bf16 v[60:63], v[146:149], v[178:181], v[60:63]
	v_mfma_f32_16x16x32_bf16 v[56:59], v[154:157], v[178:181], v[56:59]
	v_mfma_f32_16x16x32_bf16 v[48:51], v[146:149], v[198:201], v[48:51]
	v_mfma_f32_16x16x32_bf16 v[40:43], v[154:157], v[198:201], v[40:43]
	v_mfma_f32_16x16x32_bf16 v[32:35], v[146:149], v[206:209], v[32:35]
	v_mfma_f32_16x16x32_bf16 v[24:27], v[154:157], v[206:209], v[24:27]
	v_mfma_f32_16x16x32_bf16 v[16:19], v[146:149], v[228:231], v[16:19]
	v_mfma_f32_16x16x32_bf16 v[8:11], v[154:157], v[228:231], v[8:11]
	v_mfma_f32_16x16x32_bf16 v[60:63], v[150:153], v[194:197], v[60:63]
	v_mfma_f32_16x16x32_bf16 v[56:59], v[158:161], v[194:197], v[56:59]
	v_mfma_f32_16x16x32_bf16 v[48:51], v[150:153], v[202:205], v[48:51]
	v_mfma_f32_16x16x32_bf16 v[40:43], v[158:161], v[202:205], v[40:43]
	v_mfma_f32_16x16x32_bf16 v[32:35], v[150:153], v[224:227], v[32:35]
	v_mfma_f32_16x16x32_bf16 v[24:27], v[158:161], v[224:227], v[24:27]
	v_mfma_f32_16x16x32_bf16 v[16:19], v[150:153], v[232:235], v[16:19]
	v_mfma_f32_16x16x32_bf16 v[8:11], v[158:161], v[232:235], v[8:11]
	s_setprio 1
	s_setprio 0
	v_mfma_f32_16x16x32_bf16 v[52:55], v[162:165], v[178:181], v[52:55]
	v_mfma_f32_16x16x32_bf16 v[44:47], v[170:173], v[178:181], v[44:47]
	v_mfma_f32_16x16x32_bf16 v[36:39], v[162:165], v[198:201], v[36:39]
	v_mfma_f32_16x16x32_bf16 v[28:31], v[170:173], v[198:201], v[28:31]
	v_mfma_f32_16x16x32_bf16 v[20:23], v[162:165], v[206:209], v[20:23]
	v_mfma_f32_16x16x32_bf16 v[12:15], v[170:173], v[206:209], v[12:15]
	v_mfma_f32_16x16x32_bf16 v[4:7], v[162:165], v[228:231], v[4:7]
	v_mfma_f32_16x16x32_bf16 v[0:3], v[170:173], v[228:231], v[0:3]
	v_mfma_f32_16x16x32_bf16 v[52:55], v[166:169], v[194:197], v[52:55]
	v_mfma_f32_16x16x32_bf16 v[44:47], v[174:177], v[194:197], v[44:47]
	v_mfma_f32_16x16x32_bf16 v[36:39], v[166:169], v[202:205], v[36:39]
	v_mfma_f32_16x16x32_bf16 v[28:31], v[174:177], v[202:205], v[28:31]
	v_mfma_f32_16x16x32_bf16 v[20:23], v[166:169], v[224:227], v[20:23]
	v_mfma_f32_16x16x32_bf16 v[12:15], v[174:177], v[224:227], v[12:15]
	v_mfma_f32_16x16x32_bf16 v[4:7], v[166:169], v[232:235], v[4:7]
	v_mfma_f32_16x16x32_bf16 v[0:3], v[174:177], v[232:235], v[0:3]
	s_setprio 1
	s_barrier
	v_add_u32_e32 v158, s48, v136
	v_add_u32_e32 v174, s28, v136
	ds_read_b128 v[146:149], v158
	ds_read_b128 v[150:153], v158 offset:1024
	ds_read_b128 v[154:157], v158 offset:2048
	ds_read_b128 v[158:161], v158 offset:3072
	ds_read_b128 v[162:165], v174
	ds_read_b128 v[166:169], v174 offset:1024
	ds_read_b128 v[170:173], v174 offset:2048
	ds_read_b128 v[174:177], v174 offset:3072
	s_mov_b32 m0, s26
	v_lshl_add_u64 v[240:241], s[38:39], 0, v[134:135]
	ds_read_b128 v[178:181], v145 offset:32768
	ds_read_b128 v[194:197], v145 offset:33792
	ds_read_b128 v[198:201], v145 offset:34816
	ds_read_b128 v[202:205], v145 offset:35840
	ds_read_b128 v[206:209], v145 offset:36864
	ds_read_b128 v[224:227], v145 offset:37888
	ds_read_b128 v[228:231], v145 offset:38912
	ds_read_b128 v[232:235], v145 offset:39936
	global_load_lds_dwordx4 v[240:241], off
	v_lshl_add_u64 v[240:241], s[38:39], 0, v[130:131]
	s_mov_b32 m0, s27
	s_nop 0
	global_load_lds_dwordx4 v[240:241], off
	s_waitcnt vmcnt(8)
	s_waitcnt lgkmcnt(0)
	s_barrier
	s_setprio 0
	s_waitcnt lgkmcnt(0)
	v_mfma_f32_16x16x32_bf16 v[124:127], v[146:149], v[178:181], v[124:127]
	v_mfma_f32_16x16x32_bf16 v[120:123], v[154:157], v[178:181], v[120:123]
	v_mfma_f32_16x16x32_bf16 v[112:115], v[146:149], v[198:201], v[112:115]
	v_mfma_f32_16x16x32_bf16 v[104:107], v[154:157], v[198:201], v[104:107]
	v_mfma_f32_16x16x32_bf16 v[96:99], v[146:149], v[206:209], v[96:99]
	v_mfma_f32_16x16x32_bf16 v[88:91], v[154:157], v[206:209], v[88:91]
	v_mfma_f32_16x16x32_bf16 v[80:83], v[146:149], v[228:231], v[80:83]
	v_mfma_f32_16x16x32_bf16 v[72:75], v[154:157], v[228:231], v[72:75]
	v_mfma_f32_16x16x32_bf16 v[124:127], v[150:153], v[194:197], v[124:127]
	v_mfma_f32_16x16x32_bf16 v[120:123], v[158:161], v[194:197], v[120:123]
	v_mfma_f32_16x16x32_bf16 v[112:115], v[150:153], v[202:205], v[112:115]
	v_mfma_f32_16x16x32_bf16 v[104:107], v[158:161], v[202:205], v[104:107]
	v_mfma_f32_16x16x32_bf16 v[96:99], v[150:153], v[224:227], v[96:99]
	v_mfma_f32_16x16x32_bf16 v[88:91], v[158:161], v[224:227], v[88:91]
	v_mfma_f32_16x16x32_bf16 v[80:83], v[150:153], v[232:235], v[80:83]
	v_mfma_f32_16x16x32_bf16 v[72:75], v[158:161], v[232:235], v[72:75]
	s_setprio 1
	s_setprio 0
	v_mfma_f32_16x16x32_bf16 v[116:119], v[162:165], v[178:181], v[116:119]
	v_mfma_f32_16x16x32_bf16 v[108:111], v[170:173], v[178:181], v[108:111]
	v_mfma_f32_16x16x32_bf16 v[100:103], v[162:165], v[198:201], v[100:103]
	v_mfma_f32_16x16x32_bf16 v[92:95], v[170:173], v[198:201], v[92:95]
	v_mfma_f32_16x16x32_bf16 v[84:87], v[162:165], v[206:209], v[84:87]
	v_mfma_f32_16x16x32_bf16 v[76:79], v[170:173], v[206:209], v[76:79]
	v_mfma_f32_16x16x32_bf16 v[68:71], v[162:165], v[228:231], v[68:71]
	v_mfma_f32_16x16x32_bf16 v[64:67], v[170:173], v[228:231], v[64:67]
	v_mfma_f32_16x16x32_bf16 v[116:119], v[166:169], v[194:197], v[116:119]
	v_mfma_f32_16x16x32_bf16 v[108:111], v[174:177], v[194:197], v[108:111]
	v_mfma_f32_16x16x32_bf16 v[100:103], v[166:169], v[202:205], v[100:103]
	v_mfma_f32_16x16x32_bf16 v[92:95], v[174:177], v[202:205], v[92:95]
	v_mfma_f32_16x16x32_bf16 v[84:87], v[166:169], v[224:227], v[84:87]
	v_mfma_f32_16x16x32_bf16 v[76:79], v[174:177], v[224:227], v[76:79]
	v_mfma_f32_16x16x32_bf16 v[68:71], v[166:169], v[232:235], v[68:71]
	v_mfma_f32_16x16x32_bf16 v[64:67], v[174:177], v[232:235], v[64:67]
	s_setprio 1
	s_barrier
	s_mov_b32 m0, s88
	v_lshl_add_u64 v[240:241], v[182:183], 0, s[68:69]
	ds_read_b128 v[178:181], v145 offset:49152
	ds_read_b128 v[194:197], v145 offset:50176
	ds_read_b128 v[198:201], v145 offset:51200
	ds_read_b128 v[202:205], v145 offset:52224
	ds_read_b128 v[206:209], v145 offset:53248
	ds_read_b128 v[224:227], v145 offset:54272
	ds_read_b128 v[228:231], v145 offset:55296
	ds_read_b128 v[232:235], v145 offset:56320
	global_load_lds_dwordx4 v[240:241], off
	v_lshl_add_u64 v[240:241], v[210:211], 0, s[68:69]
	s_mov_b32 m0, s89
	v_lshl_add_u64 v[182:183], v[182:183], 0, s[54:55]
	global_load_lds_dwordx4 v[240:241], off
	s_mov_b32 m0, s76
	s_nop 0
	global_load_lds_dwordx4 v[182:183], off
	v_lshl_add_u64 v[182:183], v[210:211], 0, s[54:55]
	s_mov_b32 m0, s85
	s_nop 0
	global_load_lds_dwordx4 v[182:183], off
	v_lshl_add_u64 v[182:183], v[236:237], 0, s[68:69]
	s_mov_b32 m0, s50
	s_nop 0
	global_load_lds_dwordx4 v[182:183], off
	v_lshl_add_u64 v[182:183], v[238:239], 0, s[68:69]
	s_mov_b32 m0, s51
	s_nop 0
	global_load_lds_dwordx4 v[182:183], off
	s_waitcnt vmcnt(8)
	s_waitcnt lgkmcnt(0)
	s_barrier
	s_setprio 0
	s_waitcnt lgkmcnt(0)
	v_mfma_f32_16x16x32_bf16 v[60:63], v[146:149], v[178:181], v[60:63]
	v_mfma_f32_16x16x32_bf16 v[56:59], v[154:157], v[178:181], v[56:59]
	v_mfma_f32_16x16x32_bf16 v[48:51], v[146:149], v[198:201], v[48:51]
	v_mfma_f32_16x16x32_bf16 v[40:43], v[154:157], v[198:201], v[40:43]
	v_mfma_f32_16x16x32_bf16 v[32:35], v[146:149], v[206:209], v[32:35]
	v_mfma_f32_16x16x32_bf16 v[24:27], v[154:157], v[206:209], v[24:27]
	v_mfma_f32_16x16x32_bf16 v[16:19], v[146:149], v[228:231], v[16:19]
	v_mfma_f32_16x16x32_bf16 v[8:11], v[154:157], v[228:231], v[8:11]
	v_mfma_f32_16x16x32_bf16 v[60:63], v[150:153], v[194:197], v[60:63]
	v_mfma_f32_16x16x32_bf16 v[56:59], v[158:161], v[194:197], v[56:59]
	v_mfma_f32_16x16x32_bf16 v[48:51], v[150:153], v[202:205], v[48:51]
	v_mfma_f32_16x16x32_bf16 v[40:43], v[158:161], v[202:205], v[40:43]
	v_mfma_f32_16x16x32_bf16 v[32:35], v[150:153], v[224:227], v[32:35]
	v_mfma_f32_16x16x32_bf16 v[24:27], v[158:161], v[224:227], v[24:27]
	v_mfma_f32_16x16x32_bf16 v[16:19], v[150:153], v[232:235], v[16:19]
	v_mfma_f32_16x16x32_bf16 v[8:11], v[158:161], v[232:235], v[8:11]
	s_setprio 1
	s_setprio 0
	v_mfma_f32_16x16x32_bf16 v[52:55], v[162:165], v[178:181], v[52:55]
	v_mfma_f32_16x16x32_bf16 v[44:47], v[170:173], v[178:181], v[44:47]
	v_mfma_f32_16x16x32_bf16 v[36:39], v[162:165], v[198:201], v[36:39]
	v_mfma_f32_16x16x32_bf16 v[28:31], v[170:173], v[198:201], v[28:31]
	v_mfma_f32_16x16x32_bf16 v[20:23], v[162:165], v[206:209], v[20:23]
	v_mfma_f32_16x16x32_bf16 v[12:15], v[170:173], v[206:209], v[12:15]
	v_mfma_f32_16x16x32_bf16 v[4:7], v[162:165], v[228:231], v[4:7]
	v_mfma_f32_16x16x32_bf16 v[0:3], v[170:173], v[228:231], v[0:3]
	v_mfma_f32_16x16x32_bf16 v[52:55], v[166:169], v[194:197], v[52:55]
	v_mfma_f32_16x16x32_bf16 v[44:47], v[174:177], v[194:197], v[44:47]
	v_mfma_f32_16x16x32_bf16 v[36:39], v[166:169], v[202:205], v[36:39]
	v_mfma_f32_16x16x32_bf16 v[28:31], v[174:177], v[202:205], v[28:31]
	v_mfma_f32_16x16x32_bf16 v[20:23], v[166:169], v[224:227], v[20:23]
	v_mfma_f32_16x16x32_bf16 v[12:15], v[174:177], v[224:227], v[12:15]
	v_mfma_f32_16x16x32_bf16 v[4:7], v[166:169], v[232:235], v[4:7]
	v_mfma_f32_16x16x32_bf16 v[0:3], v[174:177], v[232:235], v[0:3]
	s_setprio 1
	s_barrier
	s_movk_i32 s44, 0x100
	s_andn2_b64 vcc, exec, s[36:37]
	s_mov_b64 s[38:39], -1
	s_mov_b64 s[36:37], 0
	s_cbranch_vccz .LBB0_514
	s_and_b64 vcc, exec, s[6:7]
	s_cbranch_vccz .LBB0_517
	s_barrier

.LBB0_531:
	s_add_u32 s39, s18, s38
	s_addc_u32 s42, s19, 0
	s_add_u32 s40, s39, 0x100
	s_addc_u32 s41, s42, 0
	s_and_b64 s[28:29], s[36:37], exec
	s_cselect_b32 s41, s78, s41
	s_cselect_b32 s40, s79, s40
	s_add_u32 s28, s16, s38
	s_addc_u32 s29, s17, 0
	s_add_u32 s38, s28, 0x100
	s_addc_u32 s43, s29, 0
	s_add_i32 s76, 0, 0x10000
	s_and_b64 s[28:29], s[36:37], exec
	s_cselect_b32 s45, s88, s43
	s_cselect_b32 s44, s89, s38
	s_add_i32 s29, 0, 0x14000
	s_add_u32 s50, s39, 0x10080
	s_addc_u32 s51, s42, 0
	s_add_i32 s43, s76, s4
	s_add_i32 m0, s20, 0xc000
	s_add_i32 s85, s20, 0xe000
	s_add_i32 s48, s43, 0x2000
	v_add_u32_e32 v136, s76, v139
	s_add_u32 s46, s44, 0x40000
	ds_read_b128 v[142:145], v136
	ds_read_b128 v[146:149], v136 offset:1024
	ds_read_b128 v[150:153], v136 offset:2048
	ds_read_b128 v[154:157], v136 offset:3072
	v_add_u32_e32 v136, s29, v139
	s_addc_u32 s47, s45, 0
	s_add_i32 s42, s29, s4
	ds_read_b128 v[158:161], v136
	ds_read_b128 v[162:165], v136 offset:1024
	ds_read_b128 v[166:169], v136 offset:2048
	ds_read_b128 v[170:173], v136 offset:3072
	s_add_i32 s49, s42, 0x2000
	s_add_i32 s28, 0, 0x18000
	s_add_i32 s94, 0, 0x1c000
	s_add_u32 s38, s40, 0x10000
	s_addc_u32 s39, s41, 0
	s_add_i32 s93, s28, s4
	s_add_i32 s92, s93, 0x2000
	s_add_u32 s36, s44, 0x40080
	s_addc_u32 s37, s45, 0
	s_add_i32 s76, s94, s4
	s_add_i32 s29, s76, 0x2000
	v_lshl_add_u64 v[136:137], s[50:51], 0, v[134:135]
	ds_read_b128 v[174:177], v140
	ds_read_b128 v[178:181], v140 offset:1024
	ds_read_b128 v[194:197], v140 offset:2048
	ds_read_b128 v[198:201], v140 offset:3072
	ds_read_b128 v[202:205], v140 offset:4096
	ds_read_b128 v[206:209], v140 offset:5120
	ds_read_b128 v[224:227], v140 offset:6144
	ds_read_b128 v[228:231], v140 offset:7168
	global_load_lds_dwordx4 v[136:137], off
	v_lshl_add_u64 v[136:137], s[50:51], 0, v[130:131]
	s_mov_b32 m0, s85
	s_nop 0
	global_load_lds_dwordx4 v[136:137], off
	s_waitcnt vmcnt(8)
	s_waitcnt lgkmcnt(0)
	s_barrier
	s_setprio 0
	s_waitcnt lgkmcnt(0)
	v_mfma_f32_16x16x32_bf16 v[124:127], v[142:145], v[174:177], v[124:127]
	v_mfma_f32_16x16x32_bf16 v[120:123], v[150:153], v[174:177], v[120:123]
	v_mfma_f32_16x16x32_bf16 v[116:119], v[142:145], v[194:197], v[116:119]
	v_mfma_f32_16x16x32_bf16 v[108:111], v[150:153], v[194:197], v[108:111]
	v_mfma_f32_16x16x32_bf16 v[100:103], v[142:145], v[202:205], v[100:103]
	v_mfma_f32_16x16x32_bf16 v[92:95], v[150:153], v[202:205], v[92:95]
	v_mfma_f32_16x16x32_bf16 v[84:87], v[142:145], v[224:227], v[84:87]
	v_mfma_f32_16x16x32_bf16 v[76:79], v[150:153], v[224:227], v[76:79]
	v_mfma_f32_16x16x32_bf16 v[124:127], v[146:149], v[178:181], v[124:127]
	v_mfma_f32_16x16x32_bf16 v[120:123], v[154:157], v[178:181], v[120:123]
	v_mfma_f32_16x16x32_bf16 v[116:119], v[146:149], v[198:201], v[116:119]
	v_mfma_f32_16x16x32_bf16 v[108:111], v[154:157], v[198:201], v[108:111]
	v_mfma_f32_16x16x32_bf16 v[100:103], v[146:149], v[206:209], v[100:103]
	v_mfma_f32_16x16x32_bf16 v[92:95], v[154:157], v[206:209], v[92:95]
	v_mfma_f32_16x16x32_bf16 v[84:87], v[146:149], v[228:231], v[84:87]
	v_mfma_f32_16x16x32_bf16 v[76:79], v[154:157], v[228:231], v[76:79]
	s_setprio 1
	s_setprio 0
	v_mfma_f32_16x16x32_bf16 v[112:115], v[158:161], v[174:177], v[112:115]
	v_mfma_f32_16x16x32_bf16 v[104:107], v[166:169], v[174:177], v[104:107]
	v_mfma_f32_16x16x32_bf16 v[96:99], v[158:161], v[194:197], v[96:99]
	v_mfma_f32_16x16x32_bf16 v[88:91], v[166:169], v[194:197], v[88:91]
	v_mfma_f32_16x16x32_bf16 v[80:83], v[158:161], v[202:205], v[80:83]
	v_mfma_f32_16x16x32_bf16 v[72:75], v[166:169], v[202:205], v[72:75]
	v_mfma_f32_16x16x32_bf16 v[68:71], v[158:161], v[224:227], v[68:71]
	v_mfma_f32_16x16x32_bf16 v[64:67], v[166:169], v[224:227], v[64:67]
	v_mfma_f32_16x16x32_bf16 v[112:115], v[162:165], v[178:181], v[112:115]
	v_mfma_f32_16x16x32_bf16 v[104:107], v[170:173], v[178:181], v[104:107]
	v_mfma_f32_16x16x32_bf16 v[96:99], v[162:165], v[198:201], v[96:99]
	v_mfma_f32_16x16x32_bf16 v[88:91], v[170:173], v[198:201], v[88:91]
	v_mfma_f32_16x16x32_bf16 v[80:83], v[162:165], v[206:209], v[80:83]
	v_mfma_f32_16x16x32_bf16 v[72:75], v[170:173], v[206:209], v[72:75]
	v_mfma_f32_16x16x32_bf16 v[68:71], v[162:165], v[228:231], v[68:71]
	v_mfma_f32_16x16x32_bf16 v[64:67], v[170:173], v[228:231], v[64:67]
	s_setprio 1
	s_barrier
	s_mov_b32 m0, s43
	v_lshl_add_u64 v[136:137], s[44:45], 0, v[132:133]
	ds_read_b128 v[174:177], v140 offset:16384
	ds_read_b128 v[178:181], v140 offset:17408
	ds_read_b128 v[194:197], v140 offset:18432
	ds_read_b128 v[198:201], v140 offset:19456
	ds_read_b128 v[202:205], v140 offset:20480
	ds_read_b128 v[206:209], v140 offset:21504
	ds_read_b128 v[224:227], v140 offset:22528
	ds_read_b128 v[228:231], v140 offset:23552
	global_load_lds_dwordx4 v[136:137], off
	v_lshl_add_u64 v[182:183], s[44:45], 0, v[128:129]
	s_mov_b32 m0, s48
	v_lshl_add_u64 v[210:211], s[46:47], 0, v[132:133]
	global_load_lds_dwordx4 v[182:183], off
	s_mov_b32 m0, s42
	v_lshl_add_u64 v[232:233], s[40:41], 0, v[130:131]
	global_load_lds_dwordx4 v[210:211], off
	v_lshl_add_u64 v[210:211], s[46:47], 0, v[128:129]
	s_mov_b32 m0, s49
	s_nop 0
	global_load_lds_dwordx4 v[210:211], off
	v_lshl_add_u64 v[210:211], s[40:41], 0, v[134:135]
	s_mov_b32 m0, s20
	s_nop 0
	global_load_lds_dwordx4 v[210:211], off
	s_mov_b32 m0, s21
	s_nop 0
	global_load_lds_dwordx4 v[232:233], off
	s_waitcnt vmcnt(8)
	s_waitcnt lgkmcnt(0)
	s_barrier
	s_setprio 0
	s_waitcnt lgkmcnt(0)
	v_mfma_f32_16x16x32_bf16 v[60:63], v[142:145], v[174:177], v[60:63]
	v_mfma_f32_16x16x32_bf16 v[56:59], v[150:153], v[174:177], v[56:59]
	v_mfma_f32_16x16x32_bf16 v[52:55], v[142:145], v[194:197], v[52:55]
	v_mfma_f32_16x16x32_bf16 v[44:47], v[150:153], v[194:197], v[44:47]
	v_mfma_f32_16x16x32_bf16 v[36:39], v[142:145], v[202:205], v[36:39]
	v_mfma_f32_16x16x32_bf16 v[28:31], v[150:153], v[202:205], v[28:31]
	v_mfma_f32_16x16x32_bf16 v[20:23], v[142:145], v[224:227], v[20:23]
	v_mfma_f32_16x16x32_bf16 v[12:15], v[150:153], v[224:227], v[12:15]
	v_mfma_f32_16x16x32_bf16 v[60:63], v[146:149], v[178:181], v[60:63]
	v_mfma_f32_16x16x32_bf16 v[56:59], v[154:157], v[178:181], v[56:59]
	v_mfma_f32_16x16x32_bf16 v[52:55], v[146:149], v[198:201], v[52:55]
	v_mfma_f32_16x16x32_bf16 v[44:47], v[154:157], v[198:201], v[44:47]
	v_mfma_f32_16x16x32_bf16 v[36:39], v[146:149], v[206:209], v[36:39]
	v_mfma_f32_16x16x32_bf16 v[28:31], v[154:157], v[206:209], v[28:31]
	v_mfma_f32_16x16x32_bf16 v[20:23], v[146:149], v[228:231], v[20:23]
	v_mfma_f32_16x16x32_bf16 v[12:15], v[154:157], v[228:231], v[12:15]
	s_setprio 1
	s_setprio 0
	v_mfma_f32_16x16x32_bf16 v[48:51], v[158:161], v[174:177], v[48:51]
	v_mfma_f32_16x16x32_bf16 v[40:43], v[166:169], v[174:177], v[40:43]
	v_mfma_f32_16x16x32_bf16 v[32:35], v[158:161], v[194:197], v[32:35]
	v_mfma_f32_16x16x32_bf16 v[24:27], v[166:169], v[194:197], v[24:27]
	v_mfma_f32_16x16x32_bf16 v[16:19], v[158:161], v[202:205], v[16:19]
	v_mfma_f32_16x16x32_bf16 v[8:11], v[166:169], v[202:205], v[8:11]
	v_mfma_f32_16x16x32_bf16 v[4:7], v[158:161], v[224:227], v[4:7]
	v_mfma_f32_16x16x32_bf16 v[0:3], v[166:169], v[224:227], v[0:3]
	v_mfma_f32_16x16x32_bf16 v[48:51], v[162:165], v[178:181], v[48:51]
	v_mfma_f32_16x16x32_bf16 v[40:43], v[170:173], v[178:181], v[40:43]
	v_mfma_f32_16x16x32_bf16 v[32:35], v[162:165], v[198:201], v[32:35]
	v_mfma_f32_16x16x32_bf16 v[24:27], v[170:173], v[198:201], v[24:27]
	v_mfma_f32_16x16x32_bf16 v[16:19], v[162:165], v[206:209], v[16:19]
	v_mfma_f32_16x16x32_bf16 v[8:11], v[170:173], v[206:209], v[8:11]
	v_mfma_f32_16x16x32_bf16 v[4:7], v[162:165], v[228:231], v[4:7]
	v_mfma_f32_16x16x32_bf16 v[0:3], v[170:173], v[228:231], v[0:3]
	s_setprio 1
	s_barrier
	v_add_u32_e32 v141, s28, v139
	ds_read_b128 v[142:145], v141
	ds_read_b128 v[146:149], v141 offset:1024
	ds_read_b128 v[150:153], v141 offset:2048
	ds_read_b128 v[154:157], v141 offset:3072
	v_add_u32_e32 v141, s94, v139
	ds_read_b128 v[158:161], v141
	ds_read_b128 v[162:165], v141 offset:1024
	ds_read_b128 v[166:169], v141 offset:2048
	ds_read_b128 v[170:173], v141 offset:3072
	s_mov_b32 m0, s26
	v_lshl_add_u64 v[234:235], s[38:39], 0, v[134:135]
	ds_read_b128 v[174:177], v140 offset:32768
	ds_read_b128 v[178:181], v140 offset:33792
	ds_read_b128 v[194:197], v140 offset:34816
	ds_read_b128 v[198:201], v140 offset:35840
	ds_read_b128 v[202:205], v140 offset:36864
	ds_read_b128 v[206:209], v140 offset:37888
	ds_read_b128 v[224:227], v140 offset:38912
	ds_read_b128 v[228:231], v140 offset:39936
	global_load_lds_dwordx4 v[234:235], off
	v_lshl_add_u64 v[234:235], s[38:39], 0, v[130:131]
	s_mov_b32 m0, s27
	s_nop 0
	global_load_lds_dwordx4 v[234:235], off
	s_waitcnt vmcnt(8)
	s_waitcnt lgkmcnt(0)
	s_barrier
	s_setprio 0
	s_waitcnt lgkmcnt(0)
	v_mfma_f32_16x16x32_bf16 v[124:127], v[142:145], v[174:177], v[124:127]
	v_mfma_f32_16x16x32_bf16 v[120:123], v[150:153], v[174:177], v[120:123]
	v_mfma_f32_16x16x32_bf16 v[116:119], v[142:145], v[194:197], v[116:119]
	v_mfma_f32_16x16x32_bf16 v[108:111], v[150:153], v[194:197], v[108:111]
	v_mfma_f32_16x16x32_bf16 v[100:103], v[142:145], v[202:205], v[100:103]
	v_mfma_f32_16x16x32_bf16 v[92:95], v[150:153], v[202:205], v[92:95]
	v_mfma_f32_16x16x32_bf16 v[84:87], v[142:145], v[224:227], v[84:87]
	v_mfma_f32_16x16x32_bf16 v[76:79], v[150:153], v[224:227], v[76:79]
	v_mfma_f32_16x16x32_bf16 v[124:127], v[146:149], v[178:181], v[124:127]
	v_mfma_f32_16x16x32_bf16 v[120:123], v[154:157], v[178:181], v[120:123]
	v_mfma_f32_16x16x32_bf16 v[116:119], v[146:149], v[198:201], v[116:119]
	v_mfma_f32_16x16x32_bf16 v[108:111], v[154:157], v[198:201], v[108:111]
	v_mfma_f32_16x16x32_bf16 v[100:103], v[146:149], v[206:209], v[100:103]
	v_mfma_f32_16x16x32_bf16 v[92:95], v[154:157], v[206:209], v[92:95]
	v_mfma_f32_16x16x32_bf16 v[84:87], v[146:149], v[228:231], v[84:87]
	v_mfma_f32_16x16x32_bf16 v[76:79], v[154:157], v[228:231], v[76:79]
	s_setprio 1
	s_setprio 0
	v_mfma_f32_16x16x32_bf16 v[112:115], v[158:161], v[174:177], v[112:115]
	v_mfma_f32_16x16x32_bf16 v[104:107], v[166:169], v[174:177], v[104:107]
	v_mfma_f32_16x16x32_bf16 v[96:99], v[158:161], v[194:197], v[96:99]
	v_mfma_f32_16x16x32_bf16 v[88:91], v[166:169], v[194:197], v[88:91]
	v_mfma_f32_16x16x32_bf16 v[80:83], v[158:161], v[202:205], v[80:83]
	v_mfma_f32_16x16x32_bf16 v[72:75], v[166:169], v[202:205], v[72:75]
	v_mfma_f32_16x16x32_bf16 v[68:71], v[158:161], v[224:227], v[68:71]
	v_mfma_f32_16x16x32_bf16 v[64:67], v[166:169], v[224:227], v[64:67]
	v_mfma_f32_16x16x32_bf16 v[112:115], v[162:165], v[178:181], v[112:115]
	v_mfma_f32_16x16x32_bf16 v[104:107], v[170:173], v[178:181], v[104:107]
	v_mfma_f32_16x16x32_bf16 v[96:99], v[162:165], v[198:201], v[96:99]
	v_mfma_f32_16x16x32_bf16 v[88:91], v[170:173], v[198:201], v[88:91]
	v_mfma_f32_16x16x32_bf16 v[80:83], v[162:165], v[206:209], v[80:83]
	v_mfma_f32_16x16x32_bf16 v[72:75], v[170:173], v[206:209], v[72:75]
	v_mfma_f32_16x16x32_bf16 v[68:71], v[162:165], v[228:231], v[68:71]
	v_mfma_f32_16x16x32_bf16 v[64:67], v[170:173], v[228:231], v[64:67]
	s_setprio 1
	s_barrier
	s_mov_b32 m0, s93
	v_lshl_add_u64 v[136:137], v[136:137], 0, s[68:69]
	ds_read_b128 v[174:177], v140 offset:49152
	ds_read_b128 v[178:181], v140 offset:50176
	ds_read_b128 v[194:197], v140 offset:51200
	ds_read_b128 v[198:201], v140 offset:52224
	ds_read_b128 v[202:205], v140 offset:53248
	ds_read_b128 v[206:209], v140 offset:54272
	ds_read_b128 v[224:227], v140 offset:55296
	ds_read_b128 v[228:231], v140 offset:56320
	global_load_lds_dwordx4 v[136:137], off
	v_lshl_add_u64 v[136:137], v[182:183], 0, s[68:69]
	s_mov_b32 m0, s92
	s_nop 0
	global_load_lds_dwordx4 v[136:137], off
	v_lshl_add_u64 v[136:137], s[36:37], 0, v[132:133]
	s_mov_b32 m0, s76
	s_nop 0
	global_load_lds_dwordx4 v[136:137], off
	v_lshl_add_u64 v[136:137], s[36:37], 0, v[128:129]
	s_mov_b32 m0, s29
	s_nop 0
	global_load_lds_dwordx4 v[136:137], off
	v_lshl_add_u64 v[136:137], v[210:211], 0, s[68:69]
	s_mov_b32 m0, s52
	s_nop 0
	global_load_lds_dwordx4 v[136:137], off
	v_lshl_add_u64 v[136:137], v[232:233], 0, s[68:69]
	s_mov_b32 m0, s53
	s_nop 0
	global_load_lds_dwordx4 v[136:137], off
	s_waitcnt vmcnt(8)
	s_waitcnt lgkmcnt(0)
	s_barrier
	s_setprio 0
	s_waitcnt lgkmcnt(0)
	v_mfma_f32_16x16x32_bf16 v[60:63], v[142:145], v[174:177], v[60:63]
	v_mfma_f32_16x16x32_bf16 v[56:59], v[150:153], v[174:177], v[56:59]
	v_mfma_f32_16x16x32_bf16 v[52:55], v[142:145], v[194:197], v[52:55]
	v_mfma_f32_16x16x32_bf16 v[44:47], v[150:153], v[194:197], v[44:47]
	v_mfma_f32_16x16x32_bf16 v[36:39], v[142:145], v[202:205], v[36:39]
	v_mfma_f32_16x16x32_bf16 v[28:31], v[150:153], v[202:205], v[28:31]
	v_mfma_f32_16x16x32_bf16 v[20:23], v[142:145], v[224:227], v[20:23]
	v_mfma_f32_16x16x32_bf16 v[12:15], v[150:153], v[224:227], v[12:15]
	v_mfma_f32_16x16x32_bf16 v[60:63], v[146:149], v[178:181], v[60:63]
	v_mfma_f32_16x16x32_bf16 v[56:59], v[154:157], v[178:181], v[56:59]
	v_mfma_f32_16x16x32_bf16 v[52:55], v[146:149], v[198:201], v[52:55]
	v_mfma_f32_16x16x32_bf16 v[44:47], v[154:157], v[198:201], v[44:47]
	v_mfma_f32_16x16x32_bf16 v[36:39], v[146:149], v[206:209], v[36:39]
	v_mfma_f32_16x16x32_bf16 v[28:31], v[154:157], v[206:209], v[28:31]
	v_mfma_f32_16x16x32_bf16 v[20:23], v[146:149], v[228:231], v[20:23]
	v_mfma_f32_16x16x32_bf16 v[12:15], v[154:157], v[228:231], v[12:15]
	s_setprio 1
	s_setprio 0
	v_mfma_f32_16x16x32_bf16 v[48:51], v[158:161], v[174:177], v[48:51]
	v_mfma_f32_16x16x32_bf16 v[40:43], v[166:169], v[174:177], v[40:43]
	v_mfma_f32_16x16x32_bf16 v[32:35], v[158:161], v[194:197], v[32:35]
	v_mfma_f32_16x16x32_bf16 v[24:27], v[166:169], v[194:197], v[24:27]
	v_mfma_f32_16x16x32_bf16 v[16:19], v[158:161], v[202:205], v[16:19]
	v_mfma_f32_16x16x32_bf16 v[8:11], v[166:169], v[202:205], v[8:11]
	v_mfma_f32_16x16x32_bf16 v[4:7], v[158:161], v[224:227], v[4:7]
	v_mfma_f32_16x16x32_bf16 v[0:3], v[166:169], v[224:227], v[0:3]
	v_mfma_f32_16x16x32_bf16 v[48:51], v[162:165], v[178:181], v[48:51]
	v_mfma_f32_16x16x32_bf16 v[40:43], v[170:173], v[178:181], v[40:43]
	v_mfma_f32_16x16x32_bf16 v[32:35], v[162:165], v[198:201], v[32:35]
	v_mfma_f32_16x16x32_bf16 v[24:27], v[170:173], v[198:201], v[24:27]
	v_mfma_f32_16x16x32_bf16 v[16:19], v[162:165], v[206:209], v[16:19]
	v_mfma_f32_16x16x32_bf16 v[8:11], v[170:173], v[206:209], v[8:11]
	v_mfma_f32_16x16x32_bf16 v[4:7], v[162:165], v[228:231], v[4:7]
	v_mfma_f32_16x16x32_bf16 v[0:3], v[170:173], v[228:231], v[0:3]
	s_setprio 1
	s_barrier
	s_movk_i32 s38, 0x100
	s_andn2_b64 vcc, exec, s[30:31]
	s_mov_b64 s[36:37], -1
	s_mov_b64 s[30:31], 0
	s_cbranch_vccz .LBB0_531
	s_and_b64 vcc, exec, s[6:7]
	s_cbranch_vccz .LBB0_534
	s_barrier

.LBB0_599:
	s_add_i32 s37, s36, 0x100
	s_and_b64 s[28:29], s[30:31], exec
	s_cselect_b32 s29, 0, s37
	s_cselect_b32 s28, 0, 0
	s_add_u32 s38, s34, s29
	s_addc_u32 s39, s35, s28
	s_add_u32 s28, s16, s36
	s_addc_u32 s29, s17, 0
	s_add_u32 s37, s28, 0x100
	s_addc_u32 s40, s29, 0
	s_add_i32 s43, 0, 0x10000
	s_and_b64 s[28:29], s[30:31], exec
	s_cselect_b32 s41, s9, s40
	s_cselect_b32 s40, s58, s37
	s_add_i32 s29, 0, 0x14000
	s_add_u32 s46, s56, s36
	s_addc_u32 s47, s57, 0
	s_add_i32 s42, s43, s4
	s_add_i32 m0, s20, 0xc000
	s_add_i32 s63, s20, 0xe000
	s_add_i32 s48, s42, 0x2000
	s_add_u32 s44, s40, 0x10000
	v_add_u32_e32 v156, s43, v145
	v_add_u32_e32 v172, s29, v145
	s_addc_u32 s45, s41, 0
	s_add_i32 s62, s29, s4
	ds_read_b128 v[136:139], v156
	ds_read_b128 v[140:143], v156 offset:1024
	ds_read_b128 v[152:155], v156 offset:2048
	ds_read_b128 v[156:159], v156 offset:3072
	ds_read_b128 v[160:163], v172
	ds_read_b128 v[164:167], v172 offset:1024
	ds_read_b128 v[168:171], v172 offset:2048
	ds_read_b128 v[172:175], v172 offset:3072
	s_add_i32 s49, s62, 0x2000
	s_add_i32 s28, 0, 0x18000
	s_add_i32 s61, 0, 0x1c000
	s_add_u32 s36, s38, 0x10000
	s_addc_u32 s37, s39, 0
	s_add_i32 s60, s28, s4
	s_add_i32 s59, s60, 0x2000
	s_add_u32 s30, s40, 0x10080
	s_addc_u32 s31, s41, 0
	s_add_i32 s43, s61, s4
	s_add_i32 s29, s43, 0x2000
	v_lshl_add_u64 v[210:211], s[46:47], 0, v[132:133]
	v_lshl_add_u64 v[210:211], v[210:211], 0, s[68:69]
	ds_read_b128 v[176:179], v151
	ds_read_b128 v[180:183], v151 offset:1024
	ds_read_b128 v[194:197], v151 offset:2048
	ds_read_b128 v[198:201], v151 offset:3072
	ds_read_b128 v[202:205], v151 offset:4096
	ds_read_b128 v[206:209], v151 offset:5120
	ds_read_b128 v[224:227], v151 offset:6144
	ds_read_b128 v[228:231], v151 offset:7168
	global_load_lds_dwordx4 v[210:211], off
	v_lshl_add_u64 v[210:211], s[46:47], 0, v[130:131]
	v_lshl_add_u64 v[210:211], v[210:211], 0, s[68:69]
	s_mov_b32 m0, s63
	s_nop 0
	global_load_lds_dwordx4 v[210:211], off
	s_waitcnt vmcnt(8)
	s_waitcnt lgkmcnt(0)
	s_barrier
	s_setprio 0
	s_waitcnt lgkmcnt(0)
	v_mfma_f32_16x16x32_bf16 v[124:127], v[136:139], v[176:179], v[124:127]
	v_mfma_f32_16x16x32_bf16 v[116:119], v[152:155], v[176:179], v[116:119]
	v_mfma_f32_16x16x32_bf16 v[92:95], v[136:139], v[194:197], v[92:95]
	v_mfma_f32_16x16x32_bf16 v[84:87], v[152:155], v[194:197], v[84:87]
	v_mfma_f32_16x16x32_bf16 v[60:63], v[136:139], v[202:205], v[60:63]
	v_mfma_f32_16x16x32_bf16 v[52:55], v[152:155], v[202:205], v[52:55]
	v_mfma_f32_16x16x32_bf16 v[28:31], v[136:139], v[224:227], v[28:31]
	v_mfma_f32_16x16x32_bf16 v[20:23], v[152:155], v[224:227], v[20:23]
	v_mfma_f32_16x16x32_bf16 v[124:127], v[140:143], v[180:183], v[124:127]
	v_mfma_f32_16x16x32_bf16 v[116:119], v[156:159], v[180:183], v[116:119]
	v_mfma_f32_16x16x32_bf16 v[92:95], v[140:143], v[198:201], v[92:95]
	v_mfma_f32_16x16x32_bf16 v[84:87], v[156:159], v[198:201], v[84:87]
	v_mfma_f32_16x16x32_bf16 v[60:63], v[140:143], v[206:209], v[60:63]
	v_mfma_f32_16x16x32_bf16 v[52:55], v[156:159], v[206:209], v[52:55]
	v_mfma_f32_16x16x32_bf16 v[28:31], v[140:143], v[228:231], v[28:31]
	v_mfma_f32_16x16x32_bf16 v[20:23], v[156:159], v[228:231], v[20:23]
	s_setprio 1
	s_setprio 0
	v_mfma_f32_16x16x32_bf16 v[108:111], v[160:163], v[176:179], v[108:111]
	v_mfma_f32_16x16x32_bf16 v[104:107], v[168:171], v[176:179], v[104:107]
	v_mfma_f32_16x16x32_bf16 v[76:79], v[160:163], v[194:197], v[76:79]
	v_mfma_f32_16x16x32_bf16 v[72:75], v[168:171], v[194:197], v[72:75]
	v_mfma_f32_16x16x32_bf16 v[44:47], v[160:163], v[202:205], v[44:47]
	v_mfma_f32_16x16x32_bf16 v[40:43], v[168:171], v[202:205], v[40:43]
	v_mfma_f32_16x16x32_bf16 v[12:15], v[160:163], v[224:227], v[12:15]
	v_mfma_f32_16x16x32_bf16 v[8:11], v[168:171], v[224:227], v[8:11]
	v_mfma_f32_16x16x32_bf16 v[108:111], v[164:167], v[180:183], v[108:111]
	v_mfma_f32_16x16x32_bf16 v[104:107], v[172:175], v[180:183], v[104:107]
	v_mfma_f32_16x16x32_bf16 v[76:79], v[164:167], v[198:201], v[76:79]
	v_mfma_f32_16x16x32_bf16 v[72:75], v[172:175], v[198:201], v[72:75]
	v_mfma_f32_16x16x32_bf16 v[44:47], v[164:167], v[206:209], v[44:47]
	v_mfma_f32_16x16x32_bf16 v[40:43], v[172:175], v[206:209], v[40:43]
	v_mfma_f32_16x16x32_bf16 v[12:15], v[164:167], v[228:231], v[12:15]
	v_mfma_f32_16x16x32_bf16 v[8:11], v[172:175], v[228:231], v[8:11]
	s_setprio 1
	s_barrier
	s_mov_b32 m0, s42
	v_lshl_add_u64 v[210:211], s[40:41], 0, v[184:185]
	ds_read_b128 v[176:179], v151 offset:16384
	ds_read_b128 v[180:183], v151 offset:17408
	ds_read_b128 v[194:197], v151 offset:18432
	ds_read_b128 v[198:201], v151 offset:19456
	ds_read_b128 v[202:205], v151 offset:20480
	ds_read_b128 v[206:209], v151 offset:21504
	ds_read_b128 v[224:227], v151 offset:22528
	ds_read_b128 v[228:231], v151 offset:23552
	global_load_lds_dwordx4 v[210:211], off
	v_lshl_add_u64 v[232:233], s[40:41], 0, v[128:129]
	s_mov_b32 m0, s48
	v_lshl_add_u64 v[234:235], s[44:45], 0, v[184:185]
	global_load_lds_dwordx4 v[232:233], off
	s_mov_b32 m0, s62
	v_lshl_add_u64 v[236:237], s[38:39], 0, v[130:131]
	global_load_lds_dwordx4 v[234:235], off
	v_lshl_add_u64 v[234:235], s[44:45], 0, v[128:129]
	s_mov_b32 m0, s49
	s_nop 0
	global_load_lds_dwordx4 v[234:235], off
	v_lshl_add_u64 v[234:235], s[38:39], 0, v[132:133]
	s_mov_b32 m0, s20
	s_nop 0
	global_load_lds_dwordx4 v[234:235], off
	s_mov_b32 m0, s21
	s_nop 0
	global_load_lds_dwordx4 v[236:237], off
	s_waitcnt vmcnt(8)
	s_waitcnt lgkmcnt(0)
	s_barrier
	s_setprio 0
	s_waitcnt lgkmcnt(0)
	v_mfma_f32_16x16x32_bf16 v[120:123], v[136:139], v[176:179], v[120:123]
	v_mfma_f32_16x16x32_bf16 v[112:115], v[152:155], v[176:179], v[112:115]
	v_mfma_f32_16x16x32_bf16 v[88:91], v[136:139], v[194:197], v[88:91]
	v_mfma_f32_16x16x32_bf16 v[80:83], v[152:155], v[194:197], v[80:83]
	v_mfma_f32_16x16x32_bf16 v[56:59], v[136:139], v[202:205], v[56:59]
	v_mfma_f32_16x16x32_bf16 v[48:51], v[152:155], v[202:205], v[48:51]
	v_mfma_f32_16x16x32_bf16 v[24:27], v[136:139], v[224:227], v[24:27]
	v_mfma_f32_16x16x32_bf16 v[16:19], v[152:155], v[224:227], v[16:19]
	v_mfma_f32_16x16x32_bf16 v[120:123], v[140:143], v[180:183], v[120:123]
	v_mfma_f32_16x16x32_bf16 v[112:115], v[156:159], v[180:183], v[112:115]
	v_mfma_f32_16x16x32_bf16 v[88:91], v[140:143], v[198:201], v[88:91]
	v_mfma_f32_16x16x32_bf16 v[80:83], v[156:159], v[198:201], v[80:83]
	v_mfma_f32_16x16x32_bf16 v[56:59], v[140:143], v[206:209], v[56:59]
	v_mfma_f32_16x16x32_bf16 v[48:51], v[156:159], v[206:209], v[48:51]
	v_mfma_f32_16x16x32_bf16 v[24:27], v[140:143], v[228:231], v[24:27]
	v_mfma_f32_16x16x32_bf16 v[16:19], v[156:159], v[228:231], v[16:19]
	s_setprio 1
	s_setprio 0
	v_mfma_f32_16x16x32_bf16 v[100:103], v[160:163], v[176:179], v[100:103]
	v_mfma_f32_16x16x32_bf16 v[96:99], v[168:171], v[176:179], v[96:99]
	v_mfma_f32_16x16x32_bf16 v[68:71], v[160:163], v[194:197], v[68:71]
	v_mfma_f32_16x16x32_bf16 v[64:67], v[168:171], v[194:197], v[64:67]
	v_mfma_f32_16x16x32_bf16 v[36:39], v[160:163], v[202:205], v[36:39]
	v_mfma_f32_16x16x32_bf16 v[32:35], v[168:171], v[202:205], v[32:35]
	v_mfma_f32_16x16x32_bf16 v[4:7], v[160:163], v[224:227], v[4:7]
	v_mfma_f32_16x16x32_bf16 v[0:3], v[168:171], v[224:227], v[0:3]
	v_mfma_f32_16x16x32_bf16 v[100:103], v[164:167], v[180:183], v[100:103]
	v_mfma_f32_16x16x32_bf16 v[96:99], v[172:175], v[180:183], v[96:99]
	v_mfma_f32_16x16x32_bf16 v[68:71], v[164:167], v[198:201], v[68:71]
	v_mfma_f32_16x16x32_bf16 v[64:67], v[172:175], v[198:201], v[64:67]
	v_mfma_f32_16x16x32_bf16 v[36:39], v[164:167], v[206:209], v[36:39]
	v_mfma_f32_16x16x32_bf16 v[32:35], v[172:175], v[206:209], v[32:35]
	v_mfma_f32_16x16x32_bf16 v[4:7], v[164:167], v[228:231], v[4:7]
	v_mfma_f32_16x16x32_bf16 v[0:3], v[172:175], v[228:231], v[0:3]
	s_setprio 1
	s_barrier
	v_add_u32_e32 v156, s28, v145
	v_add_u32_e32 v172, s61, v145
	ds_read_b128 v[136:139], v156
	ds_read_b128 v[140:143], v156 offset:1024
	ds_read_b128 v[152:155], v156 offset:2048
	ds_read_b128 v[156:159], v156 offset:3072
	ds_read_b128 v[160:163], v172
	ds_read_b128 v[164:167], v172 offset:1024
	ds_read_b128 v[168:171], v172 offset:2048
	ds_read_b128 v[172:175], v172 offset:3072
	s_mov_b32 m0, s26
	v_lshl_add_u64 v[238:239], s[36:37], 0, v[132:133]
	ds_read_b128 v[176:179], v151 offset:32768
	ds_read_b128 v[180:183], v151 offset:33792
	ds_read_b128 v[194:197], v151 offset:34816
	ds_read_b128 v[198:201], v151 offset:35840
	ds_read_b128 v[202:205], v151 offset:36864
	ds_read_b128 v[206:209], v151 offset:37888
	ds_read_b128 v[224:227], v151 offset:38912
	ds_read_b128 v[228:231], v151 offset:39936
	global_load_lds_dwordx4 v[238:239], off
	v_lshl_add_u64 v[238:239], s[36:37], 0, v[130:131]
	s_mov_b32 m0, s27
	s_nop 0
	global_load_lds_dwordx4 v[238:239], off
	s_waitcnt vmcnt(8)
	s_waitcnt lgkmcnt(0)
	s_barrier
	s_setprio 0
	s_waitcnt lgkmcnt(0)
	v_mfma_f32_16x16x32_bf16 v[124:127], v[136:139], v[176:179], v[124:127]
	v_mfma_f32_16x16x32_bf16 v[116:119], v[152:155], v[176:179], v[116:119]
	v_mfma_f32_16x16x32_bf16 v[92:95], v[136:139], v[194:197], v[92:95]
	v_mfma_f32_16x16x32_bf16 v[84:87], v[152:155], v[194:197], v[84:87]
	v_mfma_f32_16x16x32_bf16 v[60:63], v[136:139], v[202:205], v[60:63]
	v_mfma_f32_16x16x32_bf16 v[52:55], v[152:155], v[202:205], v[52:55]
	v_mfma_f32_16x16x32_bf16 v[28:31], v[136:139], v[224:227], v[28:31]
	v_mfma_f32_16x16x32_bf16 v[20:23], v[152:155], v[224:227], v[20:23]
	v_mfma_f32_16x16x32_bf16 v[124:127], v[140:143], v[180:183], v[124:127]
	v_mfma_f32_16x16x32_bf16 v[116:119], v[156:159], v[180:183], v[116:119]
	v_mfma_f32_16x16x32_bf16 v[92:95], v[140:143], v[198:201], v[92:95]
	v_mfma_f32_16x16x32_bf16 v[84:87], v[156:159], v[198:201], v[84:87]
	v_mfma_f32_16x16x32_bf16 v[60:63], v[140:143], v[206:209], v[60:63]
	v_mfma_f32_16x16x32_bf16 v[52:55], v[156:159], v[206:209], v[52:55]
	v_mfma_f32_16x16x32_bf16 v[28:31], v[140:143], v[228:231], v[28:31]
	v_mfma_f32_16x16x32_bf16 v[20:23], v[156:159], v[228:231], v[20:23]
	s_setprio 1
	s_setprio 0
	v_mfma_f32_16x16x32_bf16 v[108:111], v[160:163], v[176:179], v[108:111]
	v_mfma_f32_16x16x32_bf16 v[104:107], v[168:171], v[176:179], v[104:107]
	v_mfma_f32_16x16x32_bf16 v[76:79], v[160:163], v[194:197], v[76:79]
	v_mfma_f32_16x16x32_bf16 v[72:75], v[168:171], v[194:197], v[72:75]
	v_mfma_f32_16x16x32_bf16 v[44:47], v[160:163], v[202:205], v[44:47]
	v_mfma_f32_16x16x32_bf16 v[40:43], v[168:171], v[202:205], v[40:43]
	v_mfma_f32_16x16x32_bf16 v[12:15], v[160:163], v[224:227], v[12:15]
	v_mfma_f32_16x16x32_bf16 v[8:11], v[168:171], v[224:227], v[8:11]
	v_mfma_f32_16x16x32_bf16 v[108:111], v[164:167], v[180:183], v[108:111]
	v_mfma_f32_16x16x32_bf16 v[104:107], v[172:175], v[180:183], v[104:107]
	v_mfma_f32_16x16x32_bf16 v[76:79], v[164:167], v[198:201], v[76:79]
	v_mfma_f32_16x16x32_bf16 v[72:75], v[172:175], v[198:201], v[72:75]
	v_mfma_f32_16x16x32_bf16 v[44:47], v[164:167], v[206:209], v[44:47]
	v_mfma_f32_16x16x32_bf16 v[40:43], v[172:175], v[206:209], v[40:43]
	v_mfma_f32_16x16x32_bf16 v[12:15], v[164:167], v[228:231], v[12:15]
	v_mfma_f32_16x16x32_bf16 v[8:11], v[172:175], v[228:231], v[8:11]
	s_setprio 1
	s_barrier
	s_mov_b32 m0, s60
	v_lshl_add_u64 v[210:211], v[210:211], 0, s[68:69]
	ds_read_b128 v[176:179], v151 offset:49152
	ds_read_b128 v[180:183], v151 offset:50176
	ds_read_b128 v[194:197], v151 offset:51200
	ds_read_b128 v[198:201], v151 offset:52224
	ds_read_b128 v[202:205], v151 offset:53248
	ds_read_b128 v[206:209], v151 offset:54272
	ds_read_b128 v[224:227], v151 offset:55296
	ds_read_b128 v[228:231], v151 offset:56320
	global_load_lds_dwordx4 v[210:211], off
	v_lshl_add_u64 v[210:211], v[232:233], 0, s[68:69]
	s_mov_b32 m0, s59
	s_nop 0
	global_load_lds_dwordx4 v[210:211], off
	v_lshl_add_u64 v[210:211], s[30:31], 0, v[184:185]
	s_mov_b32 m0, s43
	s_nop 0
	global_load_lds_dwordx4 v[210:211], off
	v_lshl_add_u64 v[210:211], s[30:31], 0, v[128:129]
	s_mov_b32 m0, s29
	s_nop 0
	global_load_lds_dwordx4 v[210:211], off
	v_lshl_add_u64 v[210:211], v[234:235], 0, s[68:69]
	s_mov_b32 m0, s50
	s_nop 0
	global_load_lds_dwordx4 v[210:211], off
	v_lshl_add_u64 v[210:211], v[236:237], 0, s[68:69]
	s_mov_b32 m0, s51
	s_nop 0
	global_load_lds_dwordx4 v[210:211], off
	s_waitcnt vmcnt(8)
	s_waitcnt lgkmcnt(0)
	s_barrier
	s_setprio 0
	s_waitcnt lgkmcnt(0)
	v_mfma_f32_16x16x32_bf16 v[120:123], v[136:139], v[176:179], v[120:123]
	v_mfma_f32_16x16x32_bf16 v[112:115], v[152:155], v[176:179], v[112:115]
	v_mfma_f32_16x16x32_bf16 v[88:91], v[136:139], v[194:197], v[88:91]
	v_mfma_f32_16x16x32_bf16 v[80:83], v[152:155], v[194:197], v[80:83]
	v_mfma_f32_16x16x32_bf16 v[56:59], v[136:139], v[202:205], v[56:59]
	v_mfma_f32_16x16x32_bf16 v[48:51], v[152:155], v[202:205], v[48:51]
	v_mfma_f32_16x16x32_bf16 v[24:27], v[136:139], v[224:227], v[24:27]
	v_mfma_f32_16x16x32_bf16 v[16:19], v[152:155], v[224:227], v[16:19]
	v_mfma_f32_16x16x32_bf16 v[120:123], v[140:143], v[180:183], v[120:123]
	v_mfma_f32_16x16x32_bf16 v[112:115], v[156:159], v[180:183], v[112:115]
	v_mfma_f32_16x16x32_bf16 v[88:91], v[140:143], v[198:201], v[88:91]
	v_mfma_f32_16x16x32_bf16 v[80:83], v[156:159], v[198:201], v[80:83]
	v_mfma_f32_16x16x32_bf16 v[56:59], v[140:143], v[206:209], v[56:59]
	v_mfma_f32_16x16x32_bf16 v[48:51], v[156:159], v[206:209], v[48:51]
	v_mfma_f32_16x16x32_bf16 v[24:27], v[140:143], v[228:231], v[24:27]
	v_mfma_f32_16x16x32_bf16 v[16:19], v[156:159], v[228:231], v[16:19]
	s_setprio 1
	s_setprio 0
	v_mfma_f32_16x16x32_bf16 v[100:103], v[160:163], v[176:179], v[100:103]
	v_mfma_f32_16x16x32_bf16 v[96:99], v[168:171], v[176:179], v[96:99]
	v_mfma_f32_16x16x32_bf16 v[68:71], v[160:163], v[194:197], v[68:71]
	v_mfma_f32_16x16x32_bf16 v[64:67], v[168:171], v[194:197], v[64:67]
	v_mfma_f32_16x16x32_bf16 v[36:39], v[160:163], v[202:205], v[36:39]
	v_mfma_f32_16x16x32_bf16 v[32:35], v[168:171], v[202:205], v[32:35]
	v_mfma_f32_16x16x32_bf16 v[4:7], v[160:163], v[224:227], v[4:7]
	v_mfma_f32_16x16x32_bf16 v[0:3], v[168:171], v[224:227], v[0:3]
	v_mfma_f32_16x16x32_bf16 v[100:103], v[164:167], v[180:183], v[100:103]
	v_mfma_f32_16x16x32_bf16 v[96:99], v[172:175], v[180:183], v[96:99]
	v_mfma_f32_16x16x32_bf16 v[68:71], v[164:167], v[198:201], v[68:71]
	v_mfma_f32_16x16x32_bf16 v[64:67], v[172:175], v[198:201], v[64:67]
	v_mfma_f32_16x16x32_bf16 v[36:39], v[164:167], v[206:209], v[36:39]
	v_mfma_f32_16x16x32_bf16 v[32:35], v[172:175], v[206:209], v[32:35]
	v_mfma_f32_16x16x32_bf16 v[4:7], v[164:167], v[228:231], v[4:7]
	v_mfma_f32_16x16x32_bf16 v[0:3], v[172:175], v[228:231], v[0:3]
	s_setprio 1
	s_barrier
	s_andn2_b64 vcc, exec, s[18:19]
	s_mov_b64 s[30:31], -1
	s_mov_b64 s[18:19], 0
	s_movk_i32 s36, 0x100
	s_cbranch_vccz .LBB0_599
	s_and_b64 vcc, exec, s[6:7]
	s_cbranch_vccz .LBB0_602
	s_barrier

.LBB0_667:
	s_add_i32 s29, s28, 0x100
	s_and_b64 s[36:37], s[30:31], exec
	s_cselect_b32 s29, 0, s29
	s_cselect_b32 s36, 0, 0
	s_add_u32 s38, s34, s29
	s_addc_u32 s39, s35, s36
	s_add_u32 s29, s16, s28
	s_addc_u32 s36, s17, 0
	s_add_u32 s29, s29, 0x100
	s_addc_u32 s36, s36, 0
	s_add_i32 s42, 0, 0x10000
	s_and_b64 s[30:31], s[30:31], exec
	s_cselect_b32 s41, s9, s36
	s_cselect_b32 s40, s58, s29
	s_add_i32 s29, 0, 0x14000
	s_add_u32 s46, s56, s28
	s_addc_u32 s47, s57, 0
	s_add_i32 s49, s42, s4
	s_add_i32 m0, s20, 0xc000
	s_add_i32 s43, s20, 0xe000
	s_add_i32 s59, s49, 0x2000
	v_add_u32_e32 v75, s42, v72
	s_add_u32 s44, s40, 0x10000
	ds_read_b128 v[76:79], v75
	ds_read_b128 v[80:83], v75 offset:1024
	ds_read_b128 v[84:87], v75 offset:2048
	ds_read_b128 v[88:91], v75 offset:3072
	v_add_u32_e32 v75, s29, v72
	s_addc_u32 s45, s41, 0
	s_add_i32 s60, s29, s4
	ds_read_b128 v[92:95], v75
	ds_read_b128 v[96:99], v75 offset:1024
	ds_read_b128 v[100:103], v75 offset:2048
	ds_read_b128 v[104:107], v75 offset:3072
	s_add_i32 s61, s60, 0x2000
	s_add_i32 s62, 0, 0x18000
	s_add_i32 s63, 0, 0x1c000
	s_add_u32 s36, s38, 0x10000
	s_addc_u32 s37, s39, 0
	s_add_i32 s48, s62, s4
	s_add_i32 s28, s48, 0x2000
	s_add_u32 s30, s40, 0x10080
	s_addc_u32 s31, s41, 0
	s_add_i32 s29, s63, s4
	s_add_i32 s42, s29, 0x2000
	v_lshl_add_u64 v[140:141], s[46:47], 0, v[70:71]
	v_lshl_add_u64 v[140:141], v[140:141], 0, s[68:69]
	ds_read_b128 v[108:111], v74
	ds_read_b128 v[112:115], v74 offset:1024
	ds_read_b128 v[116:119], v74 offset:2048
	ds_read_b128 v[120:123], v74 offset:3072
	ds_read_b128 v[124:127], v74 offset:4096
	ds_read_b128 v[128:131], v74 offset:5120
	ds_read_b128 v[132:135], v74 offset:6144
	ds_read_b128 v[136:139], v74 offset:7168
	global_load_lds_dwordx4 v[140:141], off
	v_lshl_add_u64 v[140:141], s[46:47], 0, v[66:67]
	v_lshl_add_u64 v[140:141], v[140:141], 0, s[68:69]
	s_mov_b32 m0, s43
	s_nop 0
	global_load_lds_dwordx4 v[140:141], off
	s_waitcnt vmcnt(8)
	s_waitcnt lgkmcnt(0)
	s_barrier
	s_setprio 0
	s_waitcnt lgkmcnt(0)
	v_mfma_f32_16x16x32_bf16 v[60:63], v[76:79], v[108:111], v[60:63]
	v_mfma_f32_16x16x32_bf16 v[56:59], v[84:87], v[108:111], v[56:59]
	v_mfma_f32_16x16x32_bf16 v[52:55], v[76:79], v[116:119], v[52:55]
	v_mfma_f32_16x16x32_bf16 v[44:47], v[84:87], v[116:119], v[44:47]
	v_mfma_f32_16x16x32_bf16 v[36:39], v[76:79], v[124:127], v[36:39]
	v_mfma_f32_16x16x32_bf16 v[28:31], v[84:87], v[124:127], v[28:31]
	v_mfma_f32_16x16x32_bf16 v[20:23], v[76:79], v[132:135], v[20:23]
	v_mfma_f32_16x16x32_bf16 v[12:15], v[84:87], v[132:135], v[12:15]
	v_mfma_f32_16x16x32_bf16 v[60:63], v[80:83], v[112:115], v[60:63]
	v_mfma_f32_16x16x32_bf16 v[56:59], v[88:91], v[112:115], v[56:59]
	v_mfma_f32_16x16x32_bf16 v[52:55], v[80:83], v[120:123], v[52:55]
	v_mfma_f32_16x16x32_bf16 v[44:47], v[88:91], v[120:123], v[44:47]
	v_mfma_f32_16x16x32_bf16 v[36:39], v[80:83], v[128:131], v[36:39]
	v_mfma_f32_16x16x32_bf16 v[28:31], v[88:91], v[128:131], v[28:31]
	v_mfma_f32_16x16x32_bf16 v[20:23], v[80:83], v[136:139], v[20:23]
	v_mfma_f32_16x16x32_bf16 v[12:15], v[88:91], v[136:139], v[12:15]
	s_setprio 1
	s_setprio 0
	v_mfma_f32_16x16x32_bf16 v[48:51], v[92:95], v[108:111], v[48:51]
	v_mfma_f32_16x16x32_bf16 v[40:43], v[100:103], v[108:111], v[40:43]
	v_mfma_f32_16x16x32_bf16 v[32:35], v[92:95], v[116:119], v[32:35]
	v_mfma_f32_16x16x32_bf16 v[24:27], v[100:103], v[116:119], v[24:27]
	v_mfma_f32_16x16x32_bf16 v[16:19], v[92:95], v[124:127], v[16:19]
	v_mfma_f32_16x16x32_bf16 v[8:11], v[100:103], v[124:127], v[8:11]
	v_mfma_f32_16x16x32_bf16 v[4:7], v[92:95], v[132:135], v[4:7]
	v_mfma_f32_16x16x32_bf16 v[0:3], v[100:103], v[132:135], v[0:3]
	v_mfma_f32_16x16x32_bf16 v[48:51], v[96:99], v[112:115], v[48:51]
	v_mfma_f32_16x16x32_bf16 v[40:43], v[104:107], v[112:115], v[40:43]
	v_mfma_f32_16x16x32_bf16 v[32:35], v[96:99], v[120:123], v[32:35]
	v_mfma_f32_16x16x32_bf16 v[24:27], v[104:107], v[120:123], v[24:27]
	v_mfma_f32_16x16x32_bf16 v[16:19], v[96:99], v[128:131], v[16:19]
	v_mfma_f32_16x16x32_bf16 v[8:11], v[104:107], v[128:131], v[8:11]
	v_mfma_f32_16x16x32_bf16 v[4:7], v[96:99], v[136:139], v[4:7]
	v_mfma_f32_16x16x32_bf16 v[0:3], v[104:107], v[136:139], v[0:3]
	s_setprio 1
	s_barrier
	s_mov_b32 m0, s49
	v_lshl_add_u64 v[140:141], s[40:41], 0, v[68:69]
	global_load_lds_dwordx4 v[140:141], off
	v_lshl_add_u64 v[142:143], s[40:41], 0, v[64:65]
	s_mov_b32 m0, s59
	v_lshl_add_u64 v[76:77], s[44:45], 0, v[68:69]
	global_load_lds_dwordx4 v[142:143], off
	s_mov_b32 m0, s60
	v_lshl_add_u64 v[144:145], s[38:39], 0, v[70:71]
	global_load_lds_dwordx4 v[76:77], off
	v_lshl_add_u64 v[76:77], s[44:45], 0, v[64:65]
	s_mov_b32 m0, s61
	v_lshl_add_u64 v[146:147], s[38:39], 0, v[66:67]
	global_load_lds_dwordx4 v[76:77], off
	s_mov_b32 m0, s20
	s_nop 0
	global_load_lds_dwordx4 v[144:145], off
	s_mov_b32 m0, s21
	s_nop 0
	global_load_lds_dwordx4 v[146:147], off
	s_waitcnt vmcnt(8)
	s_waitcnt lgkmcnt(0)
	s_barrier
	s_setprio 0
	s_setprio 1
	s_setprio 0
	s_setprio 1
	s_barrier
	v_add_u32_e32 v75, s62, v72
	ds_read_b128 v[76:79], v75
	ds_read_b128 v[80:83], v75 offset:1024
	ds_read_b128 v[84:87], v75 offset:2048
	ds_read_b128 v[88:91], v75 offset:3072
	v_add_u32_e32 v75, s63, v72
	ds_read_b128 v[92:95], v75
	ds_read_b128 v[96:99], v75 offset:1024
	ds_read_b128 v[100:103], v75 offset:2048
	ds_read_b128 v[104:107], v75 offset:3072
	s_mov_b32 m0, s26
	v_lshl_add_u64 v[148:149], s[36:37], 0, v[70:71]
	ds_read_b128 v[108:111], v74 offset:32768
	ds_read_b128 v[112:115], v74 offset:33792
	ds_read_b128 v[116:119], v74 offset:34816
	ds_read_b128 v[120:123], v74 offset:35840
	ds_read_b128 v[124:127], v74 offset:36864
	ds_read_b128 v[128:131], v74 offset:37888
	ds_read_b128 v[132:135], v74 offset:38912
	ds_read_b128 v[136:139], v74 offset:39936
	global_load_lds_dwordx4 v[148:149], off
	v_lshl_add_u64 v[148:149], s[36:37], 0, v[66:67]
	s_mov_b32 m0, s27
	s_nop 0
	global_load_lds_dwordx4 v[148:149], off
	s_waitcnt vmcnt(8)
	s_waitcnt lgkmcnt(0)
	s_barrier
	s_setprio 0
	s_waitcnt lgkmcnt(0)
	v_mfma_f32_16x16x32_bf16 v[60:63], v[76:79], v[108:111], v[60:63]
	v_mfma_f32_16x16x32_bf16 v[56:59], v[84:87], v[108:111], v[56:59]
	v_mfma_f32_16x16x32_bf16 v[52:55], v[76:79], v[116:119], v[52:55]
	v_mfma_f32_16x16x32_bf16 v[44:47], v[84:87], v[116:119], v[44:47]
	v_mfma_f32_16x16x32_bf16 v[36:39], v[76:79], v[124:127], v[36:39]
	v_mfma_f32_16x16x32_bf16 v[28:31], v[84:87], v[124:127], v[28:31]
	v_mfma_f32_16x16x32_bf16 v[20:23], v[76:79], v[132:135], v[20:23]
	v_mfma_f32_16x16x32_bf16 v[12:15], v[84:87], v[132:135], v[12:15]
	v_mfma_f32_16x16x32_bf16 v[60:63], v[80:83], v[112:115], v[60:63]
	v_mfma_f32_16x16x32_bf16 v[56:59], v[88:91], v[112:115], v[56:59]
	v_mfma_f32_16x16x32_bf16 v[52:55], v[80:83], v[120:123], v[52:55]
	v_mfma_f32_16x16x32_bf16 v[44:47], v[88:91], v[120:123], v[44:47]
	v_mfma_f32_16x16x32_bf16 v[36:39], v[80:83], v[128:131], v[36:39]
	v_mfma_f32_16x16x32_bf16 v[28:31], v[88:91], v[128:131], v[28:31]
	v_mfma_f32_16x16x32_bf16 v[20:23], v[80:83], v[136:139], v[20:23]
	v_mfma_f32_16x16x32_bf16 v[12:15], v[88:91], v[136:139], v[12:15]
	s_setprio 1
	s_setprio 0
	v_mfma_f32_16x16x32_bf16 v[48:51], v[92:95], v[108:111], v[48:51]
	v_mfma_f32_16x16x32_bf16 v[40:43], v[100:103], v[108:111], v[40:43]
	v_mfma_f32_16x16x32_bf16 v[32:35], v[92:95], v[116:119], v[32:35]
	v_mfma_f32_16x16x32_bf16 v[24:27], v[100:103], v[116:119], v[24:27]
	v_mfma_f32_16x16x32_bf16 v[16:19], v[92:95], v[124:127], v[16:19]
	v_mfma_f32_16x16x32_bf16 v[8:11], v[100:103], v[124:127], v[8:11]
	v_mfma_f32_16x16x32_bf16 v[4:7], v[92:95], v[132:135], v[4:7]
	v_mfma_f32_16x16x32_bf16 v[0:3], v[100:103], v[132:135], v[0:3]
	v_mfma_f32_16x16x32_bf16 v[48:51], v[96:99], v[112:115], v[48:51]
	v_mfma_f32_16x16x32_bf16 v[40:43], v[104:107], v[112:115], v[40:43]
	v_mfma_f32_16x16x32_bf16 v[32:35], v[96:99], v[120:123], v[32:35]
	v_mfma_f32_16x16x32_bf16 v[24:27], v[104:107], v[120:123], v[24:27]
	v_mfma_f32_16x16x32_bf16 v[16:19], v[96:99], v[128:131], v[16:19]
	v_mfma_f32_16x16x32_bf16 v[8:11], v[104:107], v[128:131], v[8:11]
	v_mfma_f32_16x16x32_bf16 v[4:7], v[96:99], v[136:139], v[4:7]
	v_mfma_f32_16x16x32_bf16 v[0:3], v[104:107], v[136:139], v[0:3]
	s_setprio 1
	s_barrier
	s_mov_b32 m0, s48
	v_lshl_add_u64 v[76:77], v[140:141], 0, s[68:69]
	global_load_lds_dwordx4 v[76:77], off
	v_lshl_add_u64 v[76:77], v[142:143], 0, s[68:69]
	s_mov_b32 m0, s28
	s_nop 0
	global_load_lds_dwordx4 v[76:77], off
	v_lshl_add_u64 v[76:77], s[30:31], 0, v[68:69]
	s_mov_b32 m0, s29
	s_nop 0
	global_load_lds_dwordx4 v[76:77], off
	v_lshl_add_u64 v[76:77], s[30:31], 0, v[64:65]
	s_mov_b32 m0, s42
	s_nop 0
	global_load_lds_dwordx4 v[76:77], off
	v_lshl_add_u64 v[76:77], v[144:145], 0, s[68:69]
	s_mov_b32 m0, s50
	s_nop 0
	global_load_lds_dwordx4 v[76:77], off
	v_lshl_add_u64 v[76:77], v[146:147], 0, s[68:69]
	s_mov_b32 m0, s51
	s_nop 0
	global_load_lds_dwordx4 v[76:77], off
	s_waitcnt vmcnt(8)
	s_waitcnt lgkmcnt(0)
	s_barrier
	s_setprio 0
	s_setprio 1
	s_setprio 0
	s_setprio 1
	s_barrier
	s_andn2_b64 vcc, exec, s[18:19]
	s_mov_b64 s[30:31], -1
	s_mov_b64 s[18:19], 0
	s_movk_i32 s28, 0x100
	s_cbranch_vccz .LBB0_667
	s_and_b64 vcc, exec, s[6:7]
	s_cbranch_vccz .LBB0_670
	s_barrier

.LBB0_682:
	s_add_u32 s18, s16, 0x100
	s_addc_u32 s19, s17, 0
	s_add_u32 s28, s45, s16
	s_addc_u32 s29, s46, s17
	s_cmp_eq_u32 s47, 4
	s_cselect_b32 s36, 0, s18
	s_cselect_b32 s37, 0, s19
	s_cselect_b32 s30, s44, s28
	s_cselect_b32 s31, s9, s29
	s_add_u32 s36, s64, s36
	s_addc_u32 s37, s65, s37
	s_add_i32 s28, 0, 0x10000
	s_add_i32 s29, 0, 0x14000
	v_add_u32_e32 v168, s28, v154
	v_add_u32_e32 v194, s29, v154
	ds_read_b128 v[156:159], v168
	ds_read_b128 v[160:163], v168 offset:1024
	ds_read_b128 v[164:167], v168 offset:2048
	ds_read_b128 v[168:171], v168 offset:3072
	ds_read_b128 v[172:175], v194
	ds_read_b128 v[176:179], v194 offset:1024
	ds_read_b128 v[180:183], v194 offset:2048
	ds_read_b128 v[194:197], v194 offset:3072
	v_lshl_add_u64 v[210:211], v[150:151], 0, s[16:17]
	s_add_i32 m0, s20, 0xc000
	ds_read_b128 v[198:201], v155
	ds_read_b128 v[202:205], v155 offset:1024
	ds_read_b128 v[206:209], v155 offset:2048
	ds_read_b128 v[224:227], v155 offset:3072
	ds_read_b128 v[228:231], v155 offset:4096
	ds_read_b128 v[232:235], v155 offset:5120
	ds_read_b128 v[236:239], v155 offset:6144
	ds_read_b128 v[240:243], v155 offset:7168
	global_load_lds_dwordx4 v[210:211], off
	v_lshl_add_u64 v[210:211], v[152:153], 0, s[16:17]
	s_add_i32 m0, s20, 0xe000
	s_nop 0
	global_load_lds_dwordx4 v[210:211], off
	s_waitcnt vmcnt(8)
	s_waitcnt lgkmcnt(0)
	s_barrier
	s_setprio 0
	s_waitcnt lgkmcnt(0)
	v_mfma_f32_16x16x32_bf16 v[124:127], v[156:159], v[198:201], v[124:127]
	v_mfma_f32_16x16x32_bf16 v[120:123], v[164:167], v[198:201], v[120:123]
	v_mfma_f32_16x16x32_bf16 v[116:119], v[156:159], v[206:209], v[116:119]
	v_mfma_f32_16x16x32_bf16 v[108:111], v[164:167], v[206:209], v[108:111]
	v_mfma_f32_16x16x32_bf16 v[100:103], v[156:159], v[228:231], v[100:103]
	v_mfma_f32_16x16x32_bf16 v[92:95], v[164:167], v[228:231], v[92:95]
	v_mfma_f32_16x16x32_bf16 v[84:87], v[156:159], v[236:239], v[84:87]
	v_mfma_f32_16x16x32_bf16 v[76:79], v[164:167], v[236:239], v[76:79]
	v_mfma_f32_16x16x32_bf16 v[124:127], v[160:163], v[202:205], v[124:127]
	v_mfma_f32_16x16x32_bf16 v[120:123], v[168:171], v[202:205], v[120:123]
	v_mfma_f32_16x16x32_bf16 v[116:119], v[160:163], v[224:227], v[116:119]
	v_mfma_f32_16x16x32_bf16 v[108:111], v[168:171], v[224:227], v[108:111]
	v_mfma_f32_16x16x32_bf16 v[100:103], v[160:163], v[232:235], v[100:103]
	v_mfma_f32_16x16x32_bf16 v[92:95], v[168:171], v[232:235], v[92:95]
	v_mfma_f32_16x16x32_bf16 v[84:87], v[160:163], v[240:243], v[84:87]
	v_mfma_f32_16x16x32_bf16 v[76:79], v[168:171], v[240:243], v[76:79]
	s_setprio 1
	s_setprio 0
	v_mfma_f32_16x16x32_bf16 v[112:115], v[172:175], v[198:201], v[112:115]
	v_mfma_f32_16x16x32_bf16 v[104:107], v[180:183], v[198:201], v[104:107]
	v_mfma_f32_16x16x32_bf16 v[96:99], v[172:175], v[206:209], v[96:99]
	v_mfma_f32_16x16x32_bf16 v[88:91], v[180:183], v[206:209], v[88:91]
	v_mfma_f32_16x16x32_bf16 v[80:83], v[172:175], v[228:231], v[80:83]
	v_mfma_f32_16x16x32_bf16 v[72:75], v[180:183], v[228:231], v[72:75]
	v_mfma_f32_16x16x32_bf16 v[68:71], v[172:175], v[236:239], v[68:71]
	v_mfma_f32_16x16x32_bf16 v[64:67], v[180:183], v[236:239], v[64:67]
	v_mfma_f32_16x16x32_bf16 v[112:115], v[176:179], v[202:205], v[112:115]
	v_mfma_f32_16x16x32_bf16 v[104:107], v[194:197], v[202:205], v[104:107]
	v_mfma_f32_16x16x32_bf16 v[96:99], v[176:179], v[224:227], v[96:99]
	v_mfma_f32_16x16x32_bf16 v[88:91], v[194:197], v[224:227], v[88:91]
	v_mfma_f32_16x16x32_bf16 v[80:83], v[176:179], v[232:235], v[80:83]
	v_mfma_f32_16x16x32_bf16 v[72:75], v[194:197], v[232:235], v[72:75]
	v_mfma_f32_16x16x32_bf16 v[68:71], v[176:179], v[240:243], v[68:71]
	v_mfma_f32_16x16x32_bf16 v[64:67], v[194:197], v[240:243], v[64:67]
	s_setprio 1
	s_barrier
	s_add_i32 s16, s28, s4
	v_lshl_add_u64 v[210:211], s[30:31], 0, v[184:185]
	s_mov_b32 m0, s16
	ds_read_b128 v[198:201], v155 offset:16384
	ds_read_b128 v[202:205], v155 offset:17408
	ds_read_b128 v[206:209], v155 offset:18432
	ds_read_b128 v[224:227], v155 offset:19456
	ds_read_b128 v[228:231], v155 offset:20480
	ds_read_b128 v[232:235], v155 offset:21504
	ds_read_b128 v[236:239], v155 offset:22528
	ds_read_b128 v[240:243], v155 offset:23552
	global_load_lds_dwordx4 v[210:211], off
	s_add_i32 m0, s16, 0x2000
	s_add_u32 s16, s30, 0x20000
	v_lshl_add_u64 v[244:245], s[30:31], 0, v[128:129]
	s_addc_u32 s17, s31, 0
	s_add_i32 s28, s29, s4
	global_load_lds_dwordx4 v[244:245], off
	v_lshl_add_u64 v[246:247], s[16:17], 0, v[184:185]
	s_mov_b32 m0, s28
	v_lshl_add_u64 v[218:219], s[36:37], 0, v[130:131]
	global_load_lds_dwordx4 v[246:247], off
	v_lshl_add_u64 v[246:247], s[16:17], 0, v[128:129]
	s_add_i32 m0, s28, 0x2000
	s_nop 0
	global_load_lds_dwordx4 v[246:247], off
	v_lshl_add_u64 v[246:247], s[36:37], 0, v[132:133]
	s_mov_b32 m0, s20
	s_nop 0
	global_load_lds_dwordx4 v[246:247], off
	s_mov_b32 m0, s21
	s_nop 0
	global_load_lds_dwordx4 v[218:219], off
	s_waitcnt vmcnt(8)
	s_waitcnt lgkmcnt(0)
	s_barrier
	s_setprio 0
	s_waitcnt lgkmcnt(0)
	v_mfma_f32_16x16x32_bf16 v[60:63], v[156:159], v[198:201], v[60:63]
	v_mfma_f32_16x16x32_bf16 v[56:59], v[164:167], v[198:201], v[56:59]
	v_mfma_f32_16x16x32_bf16 v[52:55], v[156:159], v[206:209], v[52:55]
	v_mfma_f32_16x16x32_bf16 v[44:47], v[164:167], v[206:209], v[44:47]
	v_mfma_f32_16x16x32_bf16 v[36:39], v[156:159], v[228:231], v[36:39]
	v_mfma_f32_16x16x32_bf16 v[28:31], v[164:167], v[228:231], v[28:31]
	v_mfma_f32_16x16x32_bf16 v[20:23], v[156:159], v[236:239], v[20:23]
	v_mfma_f32_16x16x32_bf16 v[12:15], v[164:167], v[236:239], v[12:15]
	v_mfma_f32_16x16x32_bf16 v[60:63], v[160:163], v[202:205], v[60:63]
	v_mfma_f32_16x16x32_bf16 v[56:59], v[168:171], v[202:205], v[56:59]
	v_mfma_f32_16x16x32_bf16 v[52:55], v[160:163], v[224:227], v[52:55]
	v_mfma_f32_16x16x32_bf16 v[44:47], v[168:171], v[224:227], v[44:47]
	v_mfma_f32_16x16x32_bf16 v[36:39], v[160:163], v[232:235], v[36:39]
	v_mfma_f32_16x16x32_bf16 v[28:31], v[168:171], v[232:235], v[28:31]
	v_mfma_f32_16x16x32_bf16 v[20:23], v[160:163], v[240:243], v[20:23]
	v_mfma_f32_16x16x32_bf16 v[12:15], v[168:171], v[240:243], v[12:15]
	s_setprio 1
	s_setprio 0
	v_mfma_f32_16x16x32_bf16 v[48:51], v[172:175], v[198:201], v[48:51]
	v_mfma_f32_16x16x32_bf16 v[40:43], v[180:183], v[198:201], v[40:43]
	v_mfma_f32_16x16x32_bf16 v[32:35], v[172:175], v[206:209], v[32:35]
	v_mfma_f32_16x16x32_bf16 v[24:27], v[180:183], v[206:209], v[24:27]
	v_mfma_f32_16x16x32_bf16 v[16:19], v[172:175], v[228:231], v[16:19]
	v_mfma_f32_16x16x32_bf16 v[8:11], v[180:183], v[228:231], v[8:11]
	v_mfma_f32_16x16x32_bf16 v[4:7], v[172:175], v[236:239], v[4:7]
	v_mfma_f32_16x16x32_bf16 v[0:3], v[180:183], v[236:239], v[0:3]
	v_mfma_f32_16x16x32_bf16 v[48:51], v[176:179], v[202:205], v[48:51]
	v_mfma_f32_16x16x32_bf16 v[40:43], v[194:197], v[202:205], v[40:43]
	v_mfma_f32_16x16x32_bf16 v[32:35], v[176:179], v[224:227], v[32:35]
	v_mfma_f32_16x16x32_bf16 v[24:27], v[194:197], v[224:227], v[24:27]
	v_mfma_f32_16x16x32_bf16 v[16:19], v[176:179], v[232:235], v[16:19]
	v_mfma_f32_16x16x32_bf16 v[8:11], v[194:197], v[232:235], v[8:11]
	v_mfma_f32_16x16x32_bf16 v[4:7], v[176:179], v[240:243], v[4:7]
	v_mfma_f32_16x16x32_bf16 v[0:3], v[194:197], v[240:243], v[0:3]
	s_setprio 1
	s_barrier
	s_add_i32 s28, 0, 0x18000
	s_add_i32 s29, 0, 0x1c000
	v_add_u32_e32 v168, s28, v154
	v_add_u32_e32 v194, s29, v154
	ds_read_b128 v[156:159], v168
	ds_read_b128 v[160:163], v168 offset:1024
	ds_read_b128 v[164:167], v168 offset:2048
	ds_read_b128 v[168:171], v168 offset:3072
	ds_read_b128 v[172:175], v194
	ds_read_b128 v[176:179], v194 offset:1024
	ds_read_b128 v[180:183], v194 offset:2048
	ds_read_b128 v[194:197], v194 offset:3072
	s_add_u32 s16, s36, 0x20000
	s_addc_u32 s17, s37, 0
	s_mov_b32 m0, s26
	v_lshl_add_u64 v[216:217], s[16:17], 0, v[132:133]
	ds_read_b128 v[198:201], v155 offset:32768
	ds_read_b128 v[202:205], v155 offset:33792
	ds_read_b128 v[206:209], v155 offset:34816
	ds_read_b128 v[224:227], v155 offset:35840
	ds_read_b128 v[228:231], v155 offset:36864
	ds_read_b128 v[232:235], v155 offset:37888
	ds_read_b128 v[236:239], v155 offset:38912
	ds_read_b128 v[240:243], v155 offset:39936
	global_load_lds_dwordx4 v[216:217], off
	v_lshl_add_u64 v[216:217], s[16:17], 0, v[130:131]
	s_mov_b32 m0, s27
	s_nop 0
	global_load_lds_dwordx4 v[216:217], off
	s_waitcnt vmcnt(8)
	s_waitcnt lgkmcnt(0)
	s_barrier
	s_setprio 0
	s_waitcnt lgkmcnt(0)
	v_mfma_f32_16x16x32_bf16 v[124:127], v[156:159], v[198:201], v[124:127]
	v_mfma_f32_16x16x32_bf16 v[120:123], v[164:167], v[198:201], v[120:123]
	v_mfma_f32_16x16x32_bf16 v[116:119], v[156:159], v[206:209], v[116:119]
	v_mfma_f32_16x16x32_bf16 v[108:111], v[164:167], v[206:209], v[108:111]
	v_mfma_f32_16x16x32_bf16 v[100:103], v[156:159], v[228:231], v[100:103]
	v_mfma_f32_16x16x32_bf16 v[92:95], v[164:167], v[228:231], v[92:95]
	v_mfma_f32_16x16x32_bf16 v[84:87], v[156:159], v[236:239], v[84:87]
	v_mfma_f32_16x16x32_bf16 v[76:79], v[164:167], v[236:239], v[76:79]
	v_mfma_f32_16x16x32_bf16 v[124:127], v[160:163], v[202:205], v[124:127]
	v_mfma_f32_16x16x32_bf16 v[120:123], v[168:171], v[202:205], v[120:123]
	v_mfma_f32_16x16x32_bf16 v[116:119], v[160:163], v[224:227], v[116:119]
	v_mfma_f32_16x16x32_bf16 v[108:111], v[168:171], v[224:227], v[108:111]
	v_mfma_f32_16x16x32_bf16 v[100:103], v[160:163], v[232:235], v[100:103]
	v_mfma_f32_16x16x32_bf16 v[92:95], v[168:171], v[232:235], v[92:95]
	v_mfma_f32_16x16x32_bf16 v[84:87], v[160:163], v[240:243], v[84:87]
	v_mfma_f32_16x16x32_bf16 v[76:79], v[168:171], v[240:243], v[76:79]
	s_setprio 1
	s_setprio 0
	v_mfma_f32_16x16x32_bf16 v[112:115], v[172:175], v[198:201], v[112:115]
	v_mfma_f32_16x16x32_bf16 v[104:107], v[180:183], v[198:201], v[104:107]
	v_mfma_f32_16x16x32_bf16 v[96:99], v[172:175], v[206:209], v[96:99]
	v_mfma_f32_16x16x32_bf16 v[88:91], v[180:183], v[206:209], v[88:91]
	v_mfma_f32_16x16x32_bf16 v[80:83], v[172:175], v[228:231], v[80:83]
	v_mfma_f32_16x16x32_bf16 v[72:75], v[180:183], v[228:231], v[72:75]
	v_mfma_f32_16x16x32_bf16 v[68:71], v[172:175], v[236:239], v[68:71]
	v_mfma_f32_16x16x32_bf16 v[64:67], v[180:183], v[236:239], v[64:67]
	v_mfma_f32_16x16x32_bf16 v[112:115], v[176:179], v[202:205], v[112:115]
	v_mfma_f32_16x16x32_bf16 v[104:107], v[194:197], v[202:205], v[104:107]
	v_mfma_f32_16x16x32_bf16 v[96:99], v[176:179], v[224:227], v[96:99]
	v_mfma_f32_16x16x32_bf16 v[88:91], v[194:197], v[224:227], v[88:91]
	v_mfma_f32_16x16x32_bf16 v[80:83], v[176:179], v[232:235], v[80:83]
	v_mfma_f32_16x16x32_bf16 v[72:75], v[194:197], v[232:235], v[72:75]
	v_mfma_f32_16x16x32_bf16 v[68:71], v[176:179], v[240:243], v[68:71]
	v_mfma_f32_16x16x32_bf16 v[64:67], v[194:197], v[240:243], v[64:67]
	s_setprio 1
	s_barrier
	s_add_i32 s16, s28, s4
	v_lshl_add_u64 v[210:211], v[210:211], 0, s[68:69]
	s_mov_b32 m0, s16
	ds_read_b128 v[198:201], v155 offset:49152
	ds_read_b128 v[202:205], v155 offset:50176
	ds_read_b128 v[206:209], v155 offset:51200
	ds_read_b128 v[224:227], v155 offset:52224
	ds_read_b128 v[228:231], v155 offset:53248
	ds_read_b128 v[232:235], v155 offset:54272
	ds_read_b128 v[236:239], v155 offset:55296
	ds_read_b128 v[240:243], v155 offset:56320
	global_load_lds_dwordx4 v[210:211], off
	s_add_i32 m0, s16, 0x2000
	s_add_u32 s16, s30, 0x20080
	v_lshl_add_u64 v[210:211], v[244:245], 0, s[68:69]
	s_addc_u32 s17, s31, 0
	s_add_i32 s28, s29, s4
	global_load_lds_dwordx4 v[210:211], off
	v_lshl_add_u64 v[210:211], s[16:17], 0, v[184:185]
	s_mov_b32 m0, s28
	s_nop 0
	global_load_lds_dwordx4 v[210:211], off
	v_lshl_add_u64 v[210:211], s[16:17], 0, v[128:129]
	s_add_i32 m0, s28, 0x2000
	s_nop 0
	global_load_lds_dwordx4 v[210:211], off
	v_lshl_add_u64 v[210:211], v[246:247], 0, s[68:69]
	s_mov_b32 m0, s38
	s_nop 0
	global_load_lds_dwordx4 v[210:211], off
	v_lshl_add_u64 v[210:211], v[218:219], 0, s[68:69]
	s_mov_b32 m0, s39
	s_nop 0
	global_load_lds_dwordx4 v[210:211], off
	s_waitcnt vmcnt(8)
	s_waitcnt lgkmcnt(0)
	s_barrier
	s_setprio 0
	s_waitcnt lgkmcnt(0)
	v_mfma_f32_16x16x32_bf16 v[60:63], v[156:159], v[198:201], v[60:63]
	v_mfma_f32_16x16x32_bf16 v[56:59], v[164:167], v[198:201], v[56:59]
	v_mfma_f32_16x16x32_bf16 v[52:55], v[156:159], v[206:209], v[52:55]
	v_mfma_f32_16x16x32_bf16 v[44:47], v[164:167], v[206:209], v[44:47]
	v_mfma_f32_16x16x32_bf16 v[36:39], v[156:159], v[228:231], v[36:39]
	v_mfma_f32_16x16x32_bf16 v[28:31], v[164:167], v[228:231], v[28:31]
	v_mfma_f32_16x16x32_bf16 v[20:23], v[156:159], v[236:239], v[20:23]
	v_mfma_f32_16x16x32_bf16 v[12:15], v[164:167], v[236:239], v[12:15]
	v_mfma_f32_16x16x32_bf16 v[60:63], v[160:163], v[202:205], v[60:63]
	v_mfma_f32_16x16x32_bf16 v[56:59], v[168:171], v[202:205], v[56:59]
	v_mfma_f32_16x16x32_bf16 v[52:55], v[160:163], v[224:227], v[52:55]
	v_mfma_f32_16x16x32_bf16 v[44:47], v[168:171], v[224:227], v[44:47]
	v_mfma_f32_16x16x32_bf16 v[36:39], v[160:163], v[232:235], v[36:39]
	v_mfma_f32_16x16x32_bf16 v[28:31], v[168:171], v[232:235], v[28:31]
	v_mfma_f32_16x16x32_bf16 v[20:23], v[160:163], v[240:243], v[20:23]
	v_mfma_f32_16x16x32_bf16 v[12:15], v[168:171], v[240:243], v[12:15]
	s_setprio 1
	s_setprio 0
	v_mfma_f32_16x16x32_bf16 v[48:51], v[172:175], v[198:201], v[48:51]
	v_mfma_f32_16x16x32_bf16 v[40:43], v[180:183], v[198:201], v[40:43]
	v_mfma_f32_16x16x32_bf16 v[32:35], v[172:175], v[206:209], v[32:35]
	v_mfma_f32_16x16x32_bf16 v[24:27], v[180:183], v[206:209], v[24:27]
	v_mfma_f32_16x16x32_bf16 v[16:19], v[172:175], v[228:231], v[16:19]
	v_mfma_f32_16x16x32_bf16 v[8:11], v[180:183], v[228:231], v[8:11]
	v_mfma_f32_16x16x32_bf16 v[4:7], v[172:175], v[236:239], v[4:7]
	v_mfma_f32_16x16x32_bf16 v[0:3], v[180:183], v[236:239], v[0:3]
	v_mfma_f32_16x16x32_bf16 v[48:51], v[176:179], v[202:205], v[48:51]
	v_mfma_f32_16x16x32_bf16 v[40:43], v[194:197], v[202:205], v[40:43]
	v_mfma_f32_16x16x32_bf16 v[32:35], v[176:179], v[224:227], v[32:35]
	v_mfma_f32_16x16x32_bf16 v[24:27], v[194:197], v[224:227], v[24:27]
	v_mfma_f32_16x16x32_bf16 v[16:19], v[176:179], v[232:235], v[16:19]
	v_mfma_f32_16x16x32_bf16 v[8:11], v[194:197], v[232:235], v[8:11]
	v_mfma_f32_16x16x32_bf16 v[4:7], v[176:179], v[240:243], v[4:7]
	v_mfma_f32_16x16x32_bf16 v[0:3], v[194:197], v[240:243], v[0:3]
	s_setprio 1
	s_barrier
	s_add_i32 s47, s47, 2
	s_cmp_gt_u32 s47, 5
	s_mov_b64 s[16:17], s[18:19]
	s_cbranch_scc0 .LBB0_682
	s_and_b64 vcc, exec, s[6:7]
	s_cbranch_vccz .LBB0_685
	s_barrier

.LBB0_805:
	s_add_u32 s28, s30, 0xfff80080
	s_addc_u32 s29, s31, -1
	s_add_i32 s38, 0, 0x10000
	s_cmp_eq_u32 s78, 28
	s_cselect_b32 s45, s9, s29
	s_cselect_b32 s44, s11, s28
	s_cselect_b32 s41, s60, s63
	s_cselect_b32 s40, s61, s62
	s_add_i32 s39, 0, 0x14000
	v_add_u32_e32 v154, s38, v143
	v_add_u32_e32 v170, s39, v143
	ds_read_b128 v[138:141], v154
	ds_read_b128 v[146:149], v154 offset:1024
	ds_read_b128 v[150:153], v154 offset:2048
	ds_read_b128 v[154:157], v154 offset:3072
	ds_read_b128 v[158:161], v170
	ds_read_b128 v[162:165], v170 offset:1024
	ds_read_b128 v[166:169], v170 offset:2048
	ds_read_b128 v[170:173], v170 offset:3072
	v_lshl_add_u64 v[182:183], s[30:31], 0, v[134:135]
	s_add_i32 m0, s21, 0xc000
	ds_read_b128 v[174:177], v145
	ds_read_b128 v[178:181], v145 offset:1024
	ds_read_b128 v[194:197], v145 offset:2048
	ds_read_b128 v[198:201], v145 offset:3072
	ds_read_b128 v[202:205], v145 offset:4096
	ds_read_b128 v[206:209], v145 offset:5120
	ds_read_b128 v[224:227], v145 offset:6144
	ds_read_b128 v[228:231], v145 offset:7168
	global_load_lds_dwordx4 v[182:183], off
	v_lshl_add_u64 v[182:183], s[30:31], 0, v[136:137]
	s_add_i32 m0, s21, 0xe000
	s_nop 0
	global_load_lds_dwordx4 v[182:183], off
	s_waitcnt vmcnt(8)
	s_waitcnt lgkmcnt(0)
	s_barrier
	s_setprio 0
	s_waitcnt lgkmcnt(0)
	v_mfma_f32_16x16x32_bf16 v[124:127], v[138:141], v[174:177], v[124:127]
	v_mfma_f32_16x16x32_bf16 v[120:123], v[150:153], v[174:177], v[120:123]
	v_mfma_f32_16x16x32_bf16 v[116:119], v[138:141], v[194:197], v[116:119]
	v_mfma_f32_16x16x32_bf16 v[104:107], v[150:153], v[194:197], v[104:107]
	v_mfma_f32_16x16x32_bf16 v[100:103], v[138:141], v[202:205], v[100:103]
	v_mfma_f32_16x16x32_bf16 v[88:91], v[150:153], v[202:205], v[88:91]
	v_mfma_f32_16x16x32_bf16 v[84:87], v[138:141], v[224:227], v[84:87]
	v_mfma_f32_16x16x32_bf16 v[72:75], v[150:153], v[224:227], v[72:75]
	v_mfma_f32_16x16x32_bf16 v[124:127], v[146:149], v[178:181], v[124:127]
	v_mfma_f32_16x16x32_bf16 v[120:123], v[154:157], v[178:181], v[120:123]
	v_mfma_f32_16x16x32_bf16 v[116:119], v[146:149], v[198:201], v[116:119]
	v_mfma_f32_16x16x32_bf16 v[104:107], v[154:157], v[198:201], v[104:107]
	v_mfma_f32_16x16x32_bf16 v[100:103], v[146:149], v[206:209], v[100:103]
	v_mfma_f32_16x16x32_bf16 v[88:91], v[154:157], v[206:209], v[88:91]
	v_mfma_f32_16x16x32_bf16 v[84:87], v[146:149], v[228:231], v[84:87]
	v_mfma_f32_16x16x32_bf16 v[72:75], v[154:157], v[228:231], v[72:75]
	s_setprio 1
	s_setprio 0
	v_mfma_f32_16x16x32_bf16 v[112:115], v[158:161], v[174:177], v[112:115]
	v_mfma_f32_16x16x32_bf16 v[108:111], v[166:169], v[174:177], v[108:111]
	v_mfma_f32_16x16x32_bf16 v[96:99], v[158:161], v[194:197], v[96:99]
	v_mfma_f32_16x16x32_bf16 v[92:95], v[166:169], v[194:197], v[92:95]
	v_mfma_f32_16x16x32_bf16 v[80:83], v[158:161], v[202:205], v[80:83]
	v_mfma_f32_16x16x32_bf16 v[76:79], v[166:169], v[202:205], v[76:79]
	v_mfma_f32_16x16x32_bf16 v[68:71], v[158:161], v[224:227], v[68:71]
	v_mfma_f32_16x16x32_bf16 v[64:67], v[166:169], v[224:227], v[64:67]
	v_mfma_f32_16x16x32_bf16 v[112:115], v[162:165], v[178:181], v[112:115]
	v_mfma_f32_16x16x32_bf16 v[108:111], v[170:173], v[178:181], v[108:111]
	v_mfma_f32_16x16x32_bf16 v[96:99], v[162:165], v[198:201], v[96:99]
	v_mfma_f32_16x16x32_bf16 v[92:95], v[170:173], v[198:201], v[92:95]
	v_mfma_f32_16x16x32_bf16 v[80:83], v[162:165], v[206:209], v[80:83]
	v_mfma_f32_16x16x32_bf16 v[76:79], v[170:173], v[206:209], v[76:79]
	v_mfma_f32_16x16x32_bf16 v[68:71], v[162:165], v[228:231], v[68:71]
	v_mfma_f32_16x16x32_bf16 v[64:67], v[170:173], v[228:231], v[64:67]
	s_setprio 1
	s_barrier
	s_add_i32 s28, s38, s20
	v_lshl_add_u64 v[182:183], s[40:41], 0, v[184:185]
	s_mov_b32 m0, s28
	ds_read_b128 v[174:177], v145 offset:16384
	ds_read_b128 v[178:181], v145 offset:17408
	ds_read_b128 v[194:197], v145 offset:18432
	ds_read_b128 v[198:201], v145 offset:19456
	ds_read_b128 v[202:205], v145 offset:20480
	ds_read_b128 v[206:209], v145 offset:21504
	ds_read_b128 v[224:227], v145 offset:22528
	ds_read_b128 v[228:231], v145 offset:23552
	global_load_lds_dwordx4 v[182:183], off
	s_add_i32 m0, s28, 0x2000
	s_add_u32 s28, s40, 0x80000
	v_lshl_add_u64 v[210:211], s[40:41], 0, v[128:129]
	s_addc_u32 s29, s41, 0
	s_add_i32 s38, s39, s20
	global_load_lds_dwordx4 v[210:211], off
	v_lshl_add_u64 v[216:217], s[28:29], 0, v[184:185]
	s_mov_b32 m0, s38
	v_lshl_add_u64 v[218:219], s[44:45], 0, v[130:131]
	global_load_lds_dwordx4 v[216:217], off
	v_lshl_add_u64 v[216:217], s[28:29], 0, v[128:129]
	s_add_i32 m0, s38, 0x2000
	s_nop 0
	global_load_lds_dwordx4 v[216:217], off
	v_lshl_add_u64 v[216:217], s[44:45], 0, v[132:133]
	s_mov_b32 m0, s21
	s_nop 0
	global_load_lds_dwordx4 v[216:217], off
	s_mov_b32 m0, s46
	s_nop 0
	global_load_lds_dwordx4 v[218:219], off
	s_waitcnt vmcnt(8)
	s_waitcnt lgkmcnt(0)
	s_barrier
	s_setprio 0
	s_waitcnt lgkmcnt(0)
	v_mfma_f32_16x16x32_bf16 v[60:63], v[138:141], v[174:177], v[60:63]
	v_mfma_f32_16x16x32_bf16 v[56:59], v[150:153], v[174:177], v[56:59]
	v_mfma_f32_16x16x32_bf16 v[52:55], v[138:141], v[194:197], v[52:55]
	v_mfma_f32_16x16x32_bf16 v[40:43], v[150:153], v[194:197], v[40:43]
	v_mfma_f32_16x16x32_bf16 v[36:39], v[138:141], v[202:205], v[36:39]
	v_mfma_f32_16x16x32_bf16 v[24:27], v[150:153], v[202:205], v[24:27]
	v_mfma_f32_16x16x32_bf16 v[20:23], v[138:141], v[224:227], v[20:23]
	v_mfma_f32_16x16x32_bf16 v[8:11], v[150:153], v[224:227], v[8:11]
	v_mfma_f32_16x16x32_bf16 v[60:63], v[146:149], v[178:181], v[60:63]
	v_mfma_f32_16x16x32_bf16 v[56:59], v[154:157], v[178:181], v[56:59]
	v_mfma_f32_16x16x32_bf16 v[52:55], v[146:149], v[198:201], v[52:55]
	v_mfma_f32_16x16x32_bf16 v[40:43], v[154:157], v[198:201], v[40:43]
	v_mfma_f32_16x16x32_bf16 v[36:39], v[146:149], v[206:209], v[36:39]
	v_mfma_f32_16x16x32_bf16 v[24:27], v[154:157], v[206:209], v[24:27]
	v_mfma_f32_16x16x32_bf16 v[20:23], v[146:149], v[228:231], v[20:23]
	v_mfma_f32_16x16x32_bf16 v[8:11], v[154:157], v[228:231], v[8:11]
	s_setprio 1
	s_setprio 0
	v_mfma_f32_16x16x32_bf16 v[48:51], v[158:161], v[174:177], v[48:51]
	v_mfma_f32_16x16x32_bf16 v[44:47], v[166:169], v[174:177], v[44:47]
	v_mfma_f32_16x16x32_bf16 v[32:35], v[158:161], v[194:197], v[32:35]
	v_mfma_f32_16x16x32_bf16 v[28:31], v[166:169], v[194:197], v[28:31]
	v_mfma_f32_16x16x32_bf16 v[16:19], v[158:161], v[202:205], v[16:19]
	v_mfma_f32_16x16x32_bf16 v[12:15], v[166:169], v[202:205], v[12:15]
	v_mfma_f32_16x16x32_bf16 v[4:7], v[158:161], v[224:227], v[4:7]
	v_mfma_f32_16x16x32_bf16 v[0:3], v[166:169], v[224:227], v[0:3]
	v_mfma_f32_16x16x32_bf16 v[48:51], v[162:165], v[178:181], v[48:51]
	v_mfma_f32_16x16x32_bf16 v[44:47], v[170:173], v[178:181], v[44:47]
	v_mfma_f32_16x16x32_bf16 v[32:35], v[162:165], v[198:201], v[32:35]
	v_mfma_f32_16x16x32_bf16 v[28:31], v[170:173], v[198:201], v[28:31]
	v_mfma_f32_16x16x32_bf16 v[16:19], v[162:165], v[206:209], v[16:19]
	v_mfma_f32_16x16x32_bf16 v[12:15], v[170:173], v[206:209], v[12:15]
	v_mfma_f32_16x16x32_bf16 v[4:7], v[162:165], v[228:231], v[4:7]
	v_mfma_f32_16x16x32_bf16 v[0:3], v[170:173], v[228:231], v[0:3]
	s_setprio 1
	s_barrier
	s_add_i32 s38, 0, 0x18000
	s_add_i32 s39, 0, 0x1c000
	v_add_u32_e32 v154, s38, v143
	v_add_u32_e32 v170, s39, v143
	ds_read_b128 v[138:141], v154
	ds_read_b128 v[146:149], v154 offset:1024
	ds_read_b128 v[150:153], v154 offset:2048
	ds_read_b128 v[154:157], v154 offset:3072
	ds_read_b128 v[158:161], v170
	ds_read_b128 v[162:165], v170 offset:1024
	ds_read_b128 v[166:169], v170 offset:2048
	ds_read_b128 v[170:173], v170 offset:3072
	s_add_u32 s28, s44, 0x80000
	s_addc_u32 s29, s45, 0
	s_mov_b32 m0, s47
	v_lshl_add_u64 v[232:233], s[28:29], 0, v[132:133]
	ds_read_b128 v[174:177], v145 offset:32768
	ds_read_b128 v[178:181], v145 offset:33792
	ds_read_b128 v[194:197], v145 offset:34816
	ds_read_b128 v[198:201], v145 offset:35840
	ds_read_b128 v[202:205], v145 offset:36864
	ds_read_b128 v[206:209], v145 offset:37888
	ds_read_b128 v[224:227], v145 offset:38912
	ds_read_b128 v[228:231], v145 offset:39936
	global_load_lds_dwordx4 v[232:233], off
	v_lshl_add_u64 v[232:233], s[28:29], 0, v[130:131]
	s_mov_b32 m0, s50
	s_nop 0
	global_load_lds_dwordx4 v[232:233], off
	s_waitcnt vmcnt(8)
	s_waitcnt lgkmcnt(0)
	s_barrier
	s_setprio 0
	s_waitcnt lgkmcnt(0)
	v_mfma_f32_16x16x32_bf16 v[124:127], v[138:141], v[174:177], v[124:127]
	v_mfma_f32_16x16x32_bf16 v[120:123], v[150:153], v[174:177], v[120:123]
	v_mfma_f32_16x16x32_bf16 v[116:119], v[138:141], v[194:197], v[116:119]
	v_mfma_f32_16x16x32_bf16 v[104:107], v[150:153], v[194:197], v[104:107]
	v_mfma_f32_16x16x32_bf16 v[100:103], v[138:141], v[202:205], v[100:103]
	v_mfma_f32_16x16x32_bf16 v[88:91], v[150:153], v[202:205], v[88:91]
	v_mfma_f32_16x16x32_bf16 v[84:87], v[138:141], v[224:227], v[84:87]
	v_mfma_f32_16x16x32_bf16 v[72:75], v[150:153], v[224:227], v[72:75]
	v_mfma_f32_16x16x32_bf16 v[124:127], v[146:149], v[178:181], v[124:127]
	v_mfma_f32_16x16x32_bf16 v[120:123], v[154:157], v[178:181], v[120:123]
	v_mfma_f32_16x16x32_bf16 v[116:119], v[146:149], v[198:201], v[116:119]
	v_mfma_f32_16x16x32_bf16 v[104:107], v[154:157], v[198:201], v[104:107]
	v_mfma_f32_16x16x32_bf16 v[100:103], v[146:149], v[206:209], v[100:103]
	v_mfma_f32_16x16x32_bf16 v[88:91], v[154:157], v[206:209], v[88:91]
	v_mfma_f32_16x16x32_bf16 v[84:87], v[146:149], v[228:231], v[84:87]
	v_mfma_f32_16x16x32_bf16 v[72:75], v[154:157], v[228:231], v[72:75]
	s_setprio 1
	s_setprio 0
	v_mfma_f32_16x16x32_bf16 v[112:115], v[158:161], v[174:177], v[112:115]
	v_mfma_f32_16x16x32_bf16 v[108:111], v[166:169], v[174:177], v[108:111]
	v_mfma_f32_16x16x32_bf16 v[96:99], v[158:161], v[194:197], v[96:99]
	v_mfma_f32_16x16x32_bf16 v[92:95], v[166:169], v[194:197], v[92:95]
	v_mfma_f32_16x16x32_bf16 v[80:83], v[158:161], v[202:205], v[80:83]
	v_mfma_f32_16x16x32_bf16 v[76:79], v[166:169], v[202:205], v[76:79]
	v_mfma_f32_16x16x32_bf16 v[68:71], v[158:161], v[224:227], v[68:71]
	v_mfma_f32_16x16x32_bf16 v[64:67], v[166:169], v[224:227], v[64:67]
	v_mfma_f32_16x16x32_bf16 v[112:115], v[162:165], v[178:181], v[112:115]
	v_mfma_f32_16x16x32_bf16 v[108:111], v[170:173], v[178:181], v[108:111]
	v_mfma_f32_16x16x32_bf16 v[96:99], v[162:165], v[198:201], v[96:99]
	v_mfma_f32_16x16x32_bf16 v[92:95], v[170:173], v[198:201], v[92:95]
	v_mfma_f32_16x16x32_bf16 v[80:83], v[162:165], v[206:209], v[80:83]
	v_mfma_f32_16x16x32_bf16 v[76:79], v[170:173], v[206:209], v[76:79]
	v_mfma_f32_16x16x32_bf16 v[68:71], v[162:165], v[228:231], v[68:71]
	v_mfma_f32_16x16x32_bf16 v[64:67], v[170:173], v[228:231], v[64:67]
	s_setprio 1
	s_barrier
	s_add_i32 s28, s38, s20
	v_lshl_add_u64 v[182:183], v[182:183], 0, s[68:69]
	s_mov_b32 m0, s28
	ds_read_b128 v[174:177], v145 offset:49152
	ds_read_b128 v[178:181], v145 offset:50176
	ds_read_b128 v[194:197], v145 offset:51200
	ds_read_b128 v[198:201], v145 offset:52224
	ds_read_b128 v[202:205], v145 offset:53248
	ds_read_b128 v[206:209], v145 offset:54272
	ds_read_b128 v[224:227], v145 offset:55296
	ds_read_b128 v[228:231], v145 offset:56320
	global_load_lds_dwordx4 v[182:183], off
	s_add_i32 m0, s28, 0x2000
	s_add_u32 s28, s40, 0x80080
	v_lshl_add_u64 v[182:183], v[210:211], 0, s[68:69]
	s_addc_u32 s29, s41, 0
	s_add_i32 s38, s39, s20
	global_load_lds_dwordx4 v[182:183], off
	v_lshl_add_u64 v[182:183], s[28:29], 0, v[184:185]
	s_mov_b32 m0, s38
	s_nop 0
	global_load_lds_dwordx4 v[182:183], off
	v_lshl_add_u64 v[182:183], s[28:29], 0, v[128:129]
	s_add_i32 m0, s38, 0x2000
	s_nop 0
	global_load_lds_dwordx4 v[182:183], off
	v_lshl_add_u64 v[182:183], v[216:217], 0, s[68:69]
	s_mov_b32 m0, s51
	s_nop 0
	global_load_lds_dwordx4 v[182:183], off
	v_lshl_add_u64 v[182:183], v[218:219], 0, s[68:69]
	s_mov_b32 m0, s52
	s_nop 0
	global_load_lds_dwordx4 v[182:183], off
	s_waitcnt vmcnt(8)
	s_waitcnt lgkmcnt(0)
	s_barrier
	s_setprio 0
	s_waitcnt lgkmcnt(0)
	v_mfma_f32_16x16x32_bf16 v[60:63], v[138:141], v[174:177], v[60:63]
	v_mfma_f32_16x16x32_bf16 v[56:59], v[150:153], v[174:177], v[56:59]
	v_mfma_f32_16x16x32_bf16 v[52:55], v[138:141], v[194:197], v[52:55]
	v_mfma_f32_16x16x32_bf16 v[40:43], v[150:153], v[194:197], v[40:43]
	v_mfma_f32_16x16x32_bf16 v[36:39], v[138:141], v[202:205], v[36:39]
	v_mfma_f32_16x16x32_bf16 v[24:27], v[150:153], v[202:205], v[24:27]
	v_mfma_f32_16x16x32_bf16 v[20:23], v[138:141], v[224:227], v[20:23]
	v_mfma_f32_16x16x32_bf16 v[8:11], v[150:153], v[224:227], v[8:11]
	v_mfma_f32_16x16x32_bf16 v[60:63], v[146:149], v[178:181], v[60:63]
	v_mfma_f32_16x16x32_bf16 v[56:59], v[154:157], v[178:181], v[56:59]
	v_mfma_f32_16x16x32_bf16 v[52:55], v[146:149], v[198:201], v[52:55]
	v_mfma_f32_16x16x32_bf16 v[40:43], v[154:157], v[198:201], v[40:43]
	v_mfma_f32_16x16x32_bf16 v[36:39], v[146:149], v[206:209], v[36:39]
	v_mfma_f32_16x16x32_bf16 v[24:27], v[154:157], v[206:209], v[24:27]
	v_mfma_f32_16x16x32_bf16 v[20:23], v[146:149], v[228:231], v[20:23]
	v_mfma_f32_16x16x32_bf16 v[8:11], v[154:157], v[228:231], v[8:11]
	s_setprio 1
	s_setprio 0
	v_mfma_f32_16x16x32_bf16 v[48:51], v[158:161], v[174:177], v[48:51]
	v_mfma_f32_16x16x32_bf16 v[44:47], v[166:169], v[174:177], v[44:47]
	v_mfma_f32_16x16x32_bf16 v[32:35], v[158:161], v[194:197], v[32:35]
	v_mfma_f32_16x16x32_bf16 v[28:31], v[166:169], v[194:197], v[28:31]
	v_mfma_f32_16x16x32_bf16 v[16:19], v[158:161], v[202:205], v[16:19]
	v_mfma_f32_16x16x32_bf16 v[12:15], v[166:169], v[202:205], v[12:15]
	v_mfma_f32_16x16x32_bf16 v[4:7], v[158:161], v[224:227], v[4:7]
	v_mfma_f32_16x16x32_bf16 v[0:3], v[166:169], v[224:227], v[0:3]
	v_mfma_f32_16x16x32_bf16 v[48:51], v[162:165], v[178:181], v[48:51]
	v_mfma_f32_16x16x32_bf16 v[44:47], v[170:173], v[178:181], v[44:47]
	v_mfma_f32_16x16x32_bf16 v[32:35], v[162:165], v[198:201], v[32:35]
	v_mfma_f32_16x16x32_bf16 v[28:31], v[170:173], v[198:201], v[28:31]
	v_mfma_f32_16x16x32_bf16 v[16:19], v[162:165], v[206:209], v[16:19]
	v_mfma_f32_16x16x32_bf16 v[12:15], v[170:173], v[206:209], v[12:15]
	v_mfma_f32_16x16x32_bf16 v[4:7], v[162:165], v[228:231], v[4:7]
	v_mfma_f32_16x16x32_bf16 v[0:3], v[170:173], v[228:231], v[0:3]
	s_setprio 1
	s_barrier
	s_add_i32 s78, s78, 2
	s_add_u32 s30, s30, 0x100
	s_addc_u32 s31, s31, 0
	s_add_u32 s62, s62, 0x100
	s_addc_u32 s63, s63, 0
	s_cmp_gt_u32 s78, 29
	s_cbranch_scc0 .LBB0_805
	s_and_b64 vcc, exec, s[6:7]
	s_cbranch_vccz .LBB0_808
	s_barrier

.LBB0_822:
	s_add_u32 s38, s46, s50
	s_addc_u32 s39, s47, 0
	s_add_u32 s42, s38, 0x100
	s_addc_u32 s43, s39, 0
	s_and_b64 s[28:29], s[78:79], exec
	s_cselect_b32 s53, s11, s43
	s_cselect_b32 s52, s13, s42
	s_add_u32 s28, s6, s50
	s_addc_u32 s29, s7, 0
	s_add_u32 s42, s28, 0x100
	s_addc_u32 s43, s29, 0
	s_add_i32 s76, 0, 0x10000
	s_and_b64 s[28:29], s[78:79], exec
	s_cselect_b32 s61, s36, s43
	s_cselect_b32 s60, s37, s42
	s_add_i32 s29, 0, 0x14000
	s_add_u32 vcc_lo, s38, 0x80080
	s_addc_u32 vcc_hi, s39, 0
	s_add_i32 s85, s76, s20
	s_add_i32 m0, s21, 0xc000
	s_add_i32 s90, s21, 0xe000
	s_add_i32 s49, s85, 0x2000
	v_add_u32_e32 v153, s76, v150
	s_add_u32 s62, s60, 0x80000
	ds_read_b128 v[154:157], v153
	ds_read_b128 v[158:161], v153 offset:1024
	ds_read_b128 v[162:165], v153 offset:2048
	ds_read_b128 v[166:169], v153 offset:3072
	v_add_u32_e32 v153, s29, v150
	s_addc_u32 s63, s61, 0
	s_add_i32 s43, s29, s20
	ds_read_b128 v[170:173], v153
	ds_read_b128 v[174:177], v153 offset:1024
	ds_read_b128 v[178:181], v153 offset:2048
	ds_read_b128 v[194:197], v153 offset:3072
	s_add_i32 s42, s43, 0x2000
	s_add_i32 s39, 0, 0x18000
	s_add_i32 s28, 0, 0x1c000
	s_add_u32 s50, s52, 0x80000
	s_addc_u32 s51, s53, 0
	s_add_i32 s38, s39, s20
	s_add_i32 s48, s38, 0x2000
	s_add_u32 s78, s60, 0x80080
	s_addc_u32 s79, s61, 0
	s_add_i32 s76, s28, s20
	s_add_i32 s29, s76, 0x2000
	v_lshl_add_u64 v[182:183], vcc, 0, v[132:133]
	ds_read_b128 v[198:201], v152
	ds_read_b128 v[202:205], v152 offset:1024
	ds_read_b128 v[206:209], v152 offset:2048
	ds_read_b128 v[224:227], v152 offset:3072
	ds_read_b128 v[228:231], v152 offset:4096
	ds_read_b128 v[232:235], v152 offset:5120
	ds_read_b128 v[236:239], v152 offset:6144
	ds_read_b128 v[240:243], v152 offset:7168
	global_load_lds_dwordx4 v[182:183], off
	v_lshl_add_u64 v[182:183], vcc, 0, v[130:131]
	s_mov_b32 m0, s90
	s_nop 0
	global_load_lds_dwordx4 v[182:183], off
	s_waitcnt vmcnt(8)
	s_waitcnt lgkmcnt(0)
	s_barrier
	s_setprio 0
	s_waitcnt lgkmcnt(0)
	v_mfma_f32_16x16x32_bf16 v[124:127], v[154:157], v[198:201], v[124:127]
	v_mfma_f32_16x16x32_bf16 v[120:123], v[162:165], v[198:201], v[120:123]
	v_mfma_f32_16x16x32_bf16 v[116:119], v[154:157], v[206:209], v[116:119]
	v_mfma_f32_16x16x32_bf16 v[112:115], v[162:165], v[206:209], v[112:115]
	v_mfma_f32_16x16x32_bf16 v[108:111], v[154:157], v[228:231], v[108:111]
	v_mfma_f32_16x16x32_bf16 v[104:107], v[162:165], v[228:231], v[104:107]
	v_mfma_f32_16x16x32_bf16 v[96:99], v[154:157], v[236:239], v[96:99]
	v_mfma_f32_16x16x32_bf16 v[88:91], v[162:165], v[236:239], v[88:91]
	v_mfma_f32_16x16x32_bf16 v[124:127], v[158:161], v[202:205], v[124:127]
	v_mfma_f32_16x16x32_bf16 v[120:123], v[166:169], v[202:205], v[120:123]
	v_mfma_f32_16x16x32_bf16 v[116:119], v[158:161], v[224:227], v[116:119]
	v_mfma_f32_16x16x32_bf16 v[112:115], v[166:169], v[224:227], v[112:115]
	v_mfma_f32_16x16x32_bf16 v[108:111], v[158:161], v[232:235], v[108:111]
	v_mfma_f32_16x16x32_bf16 v[104:107], v[166:169], v[232:235], v[104:107]
	v_mfma_f32_16x16x32_bf16 v[96:99], v[158:161], v[240:243], v[96:99]
	v_mfma_f32_16x16x32_bf16 v[88:91], v[166:169], v[240:243], v[88:91]
	s_setprio 1
	s_setprio 0
	v_mfma_f32_16x16x32_bf16 v[100:103], v[170:173], v[198:201], v[100:103]
	v_mfma_f32_16x16x32_bf16 v[92:95], v[178:181], v[198:201], v[92:95]
	v_mfma_f32_16x16x32_bf16 v[84:87], v[170:173], v[206:209], v[84:87]
	v_mfma_f32_16x16x32_bf16 v[80:83], v[178:181], v[206:209], v[80:83]
	v_mfma_f32_16x16x32_bf16 v[76:79], v[170:173], v[228:231], v[76:79]
	v_mfma_f32_16x16x32_bf16 v[72:75], v[178:181], v[228:231], v[72:75]
	v_mfma_f32_16x16x32_bf16 v[68:71], v[170:173], v[236:239], v[68:71]
	v_mfma_f32_16x16x32_bf16 v[64:67], v[178:181], v[236:239], v[64:67]
	v_mfma_f32_16x16x32_bf16 v[100:103], v[174:177], v[202:205], v[100:103]
	v_mfma_f32_16x16x32_bf16 v[92:95], v[194:197], v[202:205], v[92:95]
	v_mfma_f32_16x16x32_bf16 v[84:87], v[174:177], v[224:227], v[84:87]
	v_mfma_f32_16x16x32_bf16 v[80:83], v[194:197], v[224:227], v[80:83]
	v_mfma_f32_16x16x32_bf16 v[76:79], v[174:177], v[232:235], v[76:79]
	v_mfma_f32_16x16x32_bf16 v[72:75], v[194:197], v[232:235], v[72:75]
	v_mfma_f32_16x16x32_bf16 v[68:71], v[174:177], v[240:243], v[68:71]
	v_mfma_f32_16x16x32_bf16 v[64:67], v[194:197], v[240:243], v[64:67]
	s_setprio 1
	s_barrier
	s_mov_b32 m0, s85
	v_lshl_add_u64 v[182:183], s[60:61], 0, v[184:185]
	ds_read_b128 v[198:201], v152 offset:16384
	ds_read_b128 v[202:205], v152 offset:17408
	ds_read_b128 v[206:209], v152 offset:18432
	ds_read_b128 v[224:227], v152 offset:19456
	ds_read_b128 v[228:231], v152 offset:20480
	ds_read_b128 v[232:235], v152 offset:21504
	ds_read_b128 v[236:239], v152 offset:22528
	ds_read_b128 v[240:243], v152 offset:23552
	global_load_lds_dwordx4 v[182:183], off
	v_lshl_add_u64 v[210:211], s[60:61], 0, v[128:129]
	s_mov_b32 m0, s49
	v_lshl_add_u64 v[216:217], s[62:63], 0, v[184:185]
	global_load_lds_dwordx4 v[210:211], off
	s_mov_b32 m0, s43
	v_lshl_add_u64 v[218:219], s[52:53], 0, v[130:131]
	global_load_lds_dwordx4 v[216:217], off
	v_lshl_add_u64 v[216:217], s[62:63], 0, v[128:129]
	s_mov_b32 m0, s42
	s_nop 0
	global_load_lds_dwordx4 v[216:217], off
	v_lshl_add_u64 v[216:217], s[52:53], 0, v[132:133]
	s_mov_b32 m0, s21
	s_nop 0
	global_load_lds_dwordx4 v[216:217], off
	s_mov_b32 m0, s88
	s_nop 0
	global_load_lds_dwordx4 v[218:219], off
	s_waitcnt vmcnt(8)
	s_waitcnt lgkmcnt(0)
	s_barrier
	s_setprio 0
	s_waitcnt lgkmcnt(0)
	v_mfma_f32_16x16x32_bf16 v[60:63], v[154:157], v[198:201], v[60:63]
	v_mfma_f32_16x16x32_bf16 v[56:59], v[162:165], v[198:201], v[56:59]
	v_mfma_f32_16x16x32_bf16 v[52:55], v[154:157], v[206:209], v[52:55]
	v_mfma_f32_16x16x32_bf16 v[48:51], v[162:165], v[206:209], v[48:51]
	v_mfma_f32_16x16x32_bf16 v[44:47], v[154:157], v[228:231], v[44:47]
	v_mfma_f32_16x16x32_bf16 v[40:43], v[162:165], v[228:231], v[40:43]
	v_mfma_f32_16x16x32_bf16 v[32:35], v[154:157], v[236:239], v[32:35]
	v_mfma_f32_16x16x32_bf16 v[24:27], v[162:165], v[236:239], v[24:27]
	v_mfma_f32_16x16x32_bf16 v[60:63], v[158:161], v[202:205], v[60:63]
	v_mfma_f32_16x16x32_bf16 v[56:59], v[166:169], v[202:205], v[56:59]
	v_mfma_f32_16x16x32_bf16 v[52:55], v[158:161], v[224:227], v[52:55]
	v_mfma_f32_16x16x32_bf16 v[48:51], v[166:169], v[224:227], v[48:51]
	v_mfma_f32_16x16x32_bf16 v[44:47], v[158:161], v[232:235], v[44:47]
	v_mfma_f32_16x16x32_bf16 v[40:43], v[166:169], v[232:235], v[40:43]
	v_mfma_f32_16x16x32_bf16 v[32:35], v[158:161], v[240:243], v[32:35]
	v_mfma_f32_16x16x32_bf16 v[24:27], v[166:169], v[240:243], v[24:27]
	s_setprio 1
	s_setprio 0
	v_mfma_f32_16x16x32_bf16 v[36:39], v[170:173], v[198:201], v[36:39]
	v_mfma_f32_16x16x32_bf16 v[28:31], v[178:181], v[198:201], v[28:31]
	v_mfma_f32_16x16x32_bf16 v[20:23], v[170:173], v[206:209], v[20:23]
	v_mfma_f32_16x16x32_bf16 v[16:19], v[178:181], v[206:209], v[16:19]
	v_mfma_f32_16x16x32_bf16 v[12:15], v[170:173], v[228:231], v[12:15]
	v_mfma_f32_16x16x32_bf16 v[8:11], v[178:181], v[228:231], v[8:11]
	v_mfma_f32_16x16x32_bf16 v[4:7], v[170:173], v[236:239], v[4:7]
	v_mfma_f32_16x16x32_bf16 v[0:3], v[178:181], v[236:239], v[0:3]
	v_mfma_f32_16x16x32_bf16 v[36:39], v[174:177], v[202:205], v[36:39]
	v_mfma_f32_16x16x32_bf16 v[28:31], v[194:197], v[202:205], v[28:31]
	v_mfma_f32_16x16x32_bf16 v[20:23], v[174:177], v[224:227], v[20:23]
	v_mfma_f32_16x16x32_bf16 v[16:19], v[194:197], v[224:227], v[16:19]
	v_mfma_f32_16x16x32_bf16 v[12:15], v[174:177], v[232:235], v[12:15]
	v_mfma_f32_16x16x32_bf16 v[8:11], v[194:197], v[232:235], v[8:11]
	v_mfma_f32_16x16x32_bf16 v[4:7], v[174:177], v[240:243], v[4:7]
	v_mfma_f32_16x16x32_bf16 v[0:3], v[194:197], v[240:243], v[0:3]
	s_setprio 1
	s_barrier
	v_add_u32_e32 v153, s39, v150
	ds_read_b128 v[154:157], v153
	ds_read_b128 v[158:161], v153 offset:1024
	ds_read_b128 v[162:165], v153 offset:2048
	ds_read_b128 v[166:169], v153 offset:3072
	v_add_u32_e32 v153, s28, v150
	ds_read_b128 v[170:173], v153
	ds_read_b128 v[174:177], v153 offset:1024
	ds_read_b128 v[178:181], v153 offset:2048
	ds_read_b128 v[194:197], v153 offset:3072
	s_mov_b32 m0, s89
	v_lshl_add_u64 v[244:245], s[50:51], 0, v[132:133]
	ds_read_b128 v[198:201], v152 offset:32768
	ds_read_b128 v[202:205], v152 offset:33792
	ds_read_b128 v[206:209], v152 offset:34816
	ds_read_b128 v[224:227], v152 offset:35840
	ds_read_b128 v[228:231], v152 offset:36864
	ds_read_b128 v[232:235], v152 offset:37888
	ds_read_b128 v[236:239], v152 offset:38912
	ds_read_b128 v[240:243], v152 offset:39936
	global_load_lds_dwordx4 v[244:245], off
	v_lshl_add_u64 v[244:245], s[50:51], 0, v[130:131]
	s_mov_b32 m0, s92
	s_nop 0
	global_load_lds_dwordx4 v[244:245], off
	s_waitcnt vmcnt(8)
	s_waitcnt lgkmcnt(0)
	s_barrier
	s_setprio 0
	s_waitcnt lgkmcnt(0)
	v_mfma_f32_16x16x32_bf16 v[124:127], v[154:157], v[198:201], v[124:127]
	v_mfma_f32_16x16x32_bf16 v[120:123], v[162:165], v[198:201], v[120:123]
	v_mfma_f32_16x16x32_bf16 v[116:119], v[154:157], v[206:209], v[116:119]
	v_mfma_f32_16x16x32_bf16 v[112:115], v[162:165], v[206:209], v[112:115]
	v_mfma_f32_16x16x32_bf16 v[108:111], v[154:157], v[228:231], v[108:111]
	v_mfma_f32_16x16x32_bf16 v[104:107], v[162:165], v[228:231], v[104:107]
	v_mfma_f32_16x16x32_bf16 v[96:99], v[154:157], v[236:239], v[96:99]
	v_mfma_f32_16x16x32_bf16 v[88:91], v[162:165], v[236:239], v[88:91]
	v_mfma_f32_16x16x32_bf16 v[124:127], v[158:161], v[202:205], v[124:127]
	v_mfma_f32_16x16x32_bf16 v[120:123], v[166:169], v[202:205], v[120:123]
	v_mfma_f32_16x16x32_bf16 v[116:119], v[158:161], v[224:227], v[116:119]
	v_mfma_f32_16x16x32_bf16 v[112:115], v[166:169], v[224:227], v[112:115]
	v_mfma_f32_16x16x32_bf16 v[108:111], v[158:161], v[232:235], v[108:111]
	v_mfma_f32_16x16x32_bf16 v[104:107], v[166:169], v[232:235], v[104:107]
	v_mfma_f32_16x16x32_bf16 v[96:99], v[158:161], v[240:243], v[96:99]
	v_mfma_f32_16x16x32_bf16 v[88:91], v[166:169], v[240:243], v[88:91]
	s_setprio 1
	s_setprio 0
	v_mfma_f32_16x16x32_bf16 v[100:103], v[170:173], v[198:201], v[100:103]
	v_mfma_f32_16x16x32_bf16 v[92:95], v[178:181], v[198:201], v[92:95]
	v_mfma_f32_16x16x32_bf16 v[84:87], v[170:173], v[206:209], v[84:87]
	v_mfma_f32_16x16x32_bf16 v[80:83], v[178:181], v[206:209], v[80:83]
	v_mfma_f32_16x16x32_bf16 v[76:79], v[170:173], v[228:231], v[76:79]
	v_mfma_f32_16x16x32_bf16 v[72:75], v[178:181], v[228:231], v[72:75]
	v_mfma_f32_16x16x32_bf16 v[68:71], v[170:173], v[236:239], v[68:71]
	v_mfma_f32_16x16x32_bf16 v[64:67], v[178:181], v[236:239], v[64:67]
	v_mfma_f32_16x16x32_bf16 v[100:103], v[174:177], v[202:205], v[100:103]
	v_mfma_f32_16x16x32_bf16 v[92:95], v[194:197], v[202:205], v[92:95]
	v_mfma_f32_16x16x32_bf16 v[84:87], v[174:177], v[224:227], v[84:87]
	v_mfma_f32_16x16x32_bf16 v[80:83], v[194:197], v[224:227], v[80:83]
	v_mfma_f32_16x16x32_bf16 v[76:79], v[174:177], v[232:235], v[76:79]
	v_mfma_f32_16x16x32_bf16 v[72:75], v[194:197], v[232:235], v[72:75]
	v_mfma_f32_16x16x32_bf16 v[68:71], v[174:177], v[240:243], v[68:71]
	v_mfma_f32_16x16x32_bf16 v[64:67], v[194:197], v[240:243], v[64:67]
	s_setprio 1
	s_barrier
	s_mov_b32 m0, s38
	v_lshl_add_u64 v[182:183], v[182:183], 0, s[68:69]
	ds_read_b128 v[198:201], v152 offset:49152
	ds_read_b128 v[202:205], v152 offset:50176
	ds_read_b128 v[206:209], v152 offset:51200
	ds_read_b128 v[224:227], v152 offset:52224
	ds_read_b128 v[228:231], v152 offset:53248
	ds_read_b128 v[232:235], v152 offset:54272
	ds_read_b128 v[236:239], v152 offset:55296
	ds_read_b128 v[240:243], v152 offset:56320
	global_load_lds_dwordx4 v[182:183], off
	v_lshl_add_u64 v[182:183], v[210:211], 0, s[68:69]
	s_mov_b32 m0, s48
	s_nop 0
	global_load_lds_dwordx4 v[182:183], off
	v_lshl_add_u64 v[182:183], s[78:79], 0, v[184:185]
	s_mov_b32 m0, s76
	s_nop 0
	global_load_lds_dwordx4 v[182:183], off
	v_lshl_add_u64 v[182:183], s[78:79], 0, v[128:129]
	s_mov_b32 m0, s29
	s_nop 0
	global_load_lds_dwordx4 v[182:183], off
	v_lshl_add_u64 v[182:183], v[216:217], 0, s[68:69]
	s_mov_b32 m0, s93
	s_nop 0
	global_load_lds_dwordx4 v[182:183], off
	v_lshl_add_u64 v[182:183], v[218:219], 0, s[68:69]
	s_mov_b32 m0, s94
	s_nop 0
	global_load_lds_dwordx4 v[182:183], off
	s_waitcnt vmcnt(8)
	s_waitcnt lgkmcnt(0)
	s_barrier
	s_setprio 0
	s_waitcnt lgkmcnt(0)
	v_mfma_f32_16x16x32_bf16 v[60:63], v[154:157], v[198:201], v[60:63]
	v_mfma_f32_16x16x32_bf16 v[56:59], v[162:165], v[198:201], v[56:59]
	v_mfma_f32_16x16x32_bf16 v[52:55], v[154:157], v[206:209], v[52:55]
	v_mfma_f32_16x16x32_bf16 v[48:51], v[162:165], v[206:209], v[48:51]
	v_mfma_f32_16x16x32_bf16 v[44:47], v[154:157], v[228:231], v[44:47]
	v_mfma_f32_16x16x32_bf16 v[40:43], v[162:165], v[228:231], v[40:43]
	v_mfma_f32_16x16x32_bf16 v[32:35], v[154:157], v[236:239], v[32:35]
	v_mfma_f32_16x16x32_bf16 v[24:27], v[162:165], v[236:239], v[24:27]
	v_mfma_f32_16x16x32_bf16 v[60:63], v[158:161], v[202:205], v[60:63]
	v_mfma_f32_16x16x32_bf16 v[56:59], v[166:169], v[202:205], v[56:59]
	v_mfma_f32_16x16x32_bf16 v[52:55], v[158:161], v[224:227], v[52:55]
	v_mfma_f32_16x16x32_bf16 v[48:51], v[166:169], v[224:227], v[48:51]
	v_mfma_f32_16x16x32_bf16 v[44:47], v[158:161], v[232:235], v[44:47]
	v_mfma_f32_16x16x32_bf16 v[40:43], v[166:169], v[232:235], v[40:43]
	v_mfma_f32_16x16x32_bf16 v[32:35], v[158:161], v[240:243], v[32:35]
	v_mfma_f32_16x16x32_bf16 v[24:27], v[166:169], v[240:243], v[24:27]
	s_setprio 1
	s_setprio 0
	v_mfma_f32_16x16x32_bf16 v[36:39], v[170:173], v[198:201], v[36:39]
	v_mfma_f32_16x16x32_bf16 v[28:31], v[178:181], v[198:201], v[28:31]
	v_mfma_f32_16x16x32_bf16 v[20:23], v[170:173], v[206:209], v[20:23]
	v_mfma_f32_16x16x32_bf16 v[16:19], v[178:181], v[206:209], v[16:19]
	v_mfma_f32_16x16x32_bf16 v[12:15], v[170:173], v[228:231], v[12:15]
	v_mfma_f32_16x16x32_bf16 v[8:11], v[178:181], v[228:231], v[8:11]
	v_mfma_f32_16x16x32_bf16 v[4:7], v[170:173], v[236:239], v[4:7]
	v_mfma_f32_16x16x32_bf16 v[0:3], v[178:181], v[236:239], v[0:3]
	v_mfma_f32_16x16x32_bf16 v[36:39], v[174:177], v[202:205], v[36:39]
	v_mfma_f32_16x16x32_bf16 v[28:31], v[194:197], v[202:205], v[28:31]
	v_mfma_f32_16x16x32_bf16 v[20:23], v[174:177], v[224:227], v[20:23]
	v_mfma_f32_16x16x32_bf16 v[16:19], v[194:197], v[224:227], v[16:19]
	v_mfma_f32_16x16x32_bf16 v[12:15], v[174:177], v[232:235], v[12:15]
	v_mfma_f32_16x16x32_bf16 v[8:11], v[194:197], v[232:235], v[8:11]
	v_mfma_f32_16x16x32_bf16 v[4:7], v[174:177], v[240:243], v[4:7]
	v_mfma_f32_16x16x32_bf16 v[0:3], v[194:197], v[240:243], v[0:3]
	s_setprio 1
	s_barrier
	s_movk_i32 s50, 0x100
	s_andn2_b64 vcc, exec, s[58:59]
	s_mov_b64 s[78:79], -1
	s_mov_b64 s[58:59], 0
	s_cbranch_vccz .LBB0_822
	s_and_b64 vcc, exec, s[8:9]
	s_cbranch_vccz .LBB0_825
	s_barrier

.LBB0_842:
	s_add_u32 s28, s30, 0xfffc0080
	s_addc_u32 s29, s31, -1
	s_add_i32 s42, 0, 0x10000
	s_cmp_eq_u32 s60, 12
	s_cselect_b32 s45, s9, s29
	s_cselect_b32 s44, s11, s28
	s_cselect_b32 s41, s36, s59
	s_cselect_b32 s40, s37, s58
	s_add_i32 s43, 0, 0x14000
	v_add_u32_e32 v154, s42, v147
	v_add_u32_e32 v170, s43, v147
	ds_read_b128 v[138:141], v154
	ds_read_b128 v[142:145], v154 offset:1024
	ds_read_b128 v[150:153], v154 offset:2048
	ds_read_b128 v[154:157], v154 offset:3072
	ds_read_b128 v[158:161], v170
	ds_read_b128 v[162:165], v170 offset:1024
	ds_read_b128 v[166:169], v170 offset:2048
	ds_read_b128 v[170:173], v170 offset:3072
	v_lshl_add_u64 v[182:183], s[30:31], 0, v[134:135]
	s_add_i32 m0, s21, 0xc000
	ds_read_b128 v[174:177], v149
	ds_read_b128 v[178:181], v149 offset:1024
	ds_read_b128 v[194:197], v149 offset:2048
	ds_read_b128 v[198:201], v149 offset:3072
	ds_read_b128 v[202:205], v149 offset:4096
	ds_read_b128 v[206:209], v149 offset:5120
	ds_read_b128 v[224:227], v149 offset:6144
	ds_read_b128 v[228:231], v149 offset:7168
	global_load_lds_dwordx4 v[182:183], off
	v_lshl_add_u64 v[182:183], s[30:31], 0, v[136:137]
	s_add_i32 m0, s21, 0xe000
	s_nop 0
	global_load_lds_dwordx4 v[182:183], off
	s_waitcnt vmcnt(8)
	s_waitcnt lgkmcnt(0)
	s_barrier
	s_setprio 0
	s_waitcnt lgkmcnt(0)
	v_mfma_f32_16x16x32_bf16 v[124:127], v[138:141], v[174:177], v[124:127]
	v_mfma_f32_16x16x32_bf16 v[120:123], v[150:153], v[174:177], v[120:123]
	v_mfma_f32_16x16x32_bf16 v[108:111], v[138:141], v[194:197], v[108:111]
	v_mfma_f32_16x16x32_bf16 v[104:107], v[150:153], v[194:197], v[104:107]
	v_mfma_f32_16x16x32_bf16 v[92:95], v[138:141], v[202:205], v[92:95]
	v_mfma_f32_16x16x32_bf16 v[88:91], v[150:153], v[202:205], v[88:91]
	v_mfma_f32_16x16x32_bf16 v[76:79], v[138:141], v[224:227], v[76:79]
	v_mfma_f32_16x16x32_bf16 v[72:75], v[150:153], v[224:227], v[72:75]
	v_mfma_f32_16x16x32_bf16 v[124:127], v[142:145], v[178:181], v[124:127]
	v_mfma_f32_16x16x32_bf16 v[120:123], v[154:157], v[178:181], v[120:123]
	v_mfma_f32_16x16x32_bf16 v[108:111], v[142:145], v[198:201], v[108:111]
	v_mfma_f32_16x16x32_bf16 v[104:107], v[154:157], v[198:201], v[104:107]
	v_mfma_f32_16x16x32_bf16 v[92:95], v[142:145], v[206:209], v[92:95]
	v_mfma_f32_16x16x32_bf16 v[88:91], v[154:157], v[206:209], v[88:91]
	v_mfma_f32_16x16x32_bf16 v[76:79], v[142:145], v[228:231], v[76:79]
	v_mfma_f32_16x16x32_bf16 v[72:75], v[154:157], v[228:231], v[72:75]
	s_setprio 1
	s_setprio 0
	v_mfma_f32_16x16x32_bf16 v[116:119], v[158:161], v[174:177], v[116:119]
	v_mfma_f32_16x16x32_bf16 v[112:115], v[166:169], v[174:177], v[112:115]
	v_mfma_f32_16x16x32_bf16 v[100:103], v[158:161], v[194:197], v[100:103]
	v_mfma_f32_16x16x32_bf16 v[96:99], v[166:169], v[194:197], v[96:99]
	v_mfma_f32_16x16x32_bf16 v[84:87], v[158:161], v[202:205], v[84:87]
	v_mfma_f32_16x16x32_bf16 v[80:83], v[166:169], v[202:205], v[80:83]
	v_mfma_f32_16x16x32_bf16 v[68:71], v[158:161], v[224:227], v[68:71]
	v_mfma_f32_16x16x32_bf16 v[64:67], v[166:169], v[224:227], v[64:67]
	v_mfma_f32_16x16x32_bf16 v[116:119], v[162:165], v[178:181], v[116:119]
	v_mfma_f32_16x16x32_bf16 v[112:115], v[170:173], v[178:181], v[112:115]
	v_mfma_f32_16x16x32_bf16 v[100:103], v[162:165], v[198:201], v[100:103]
	v_mfma_f32_16x16x32_bf16 v[96:99], v[170:173], v[198:201], v[96:99]
	v_mfma_f32_16x16x32_bf16 v[84:87], v[162:165], v[206:209], v[84:87]
	v_mfma_f32_16x16x32_bf16 v[80:83], v[170:173], v[206:209], v[80:83]
	v_mfma_f32_16x16x32_bf16 v[68:71], v[162:165], v[228:231], v[68:71]
	v_mfma_f32_16x16x32_bf16 v[64:67], v[170:173], v[228:231], v[64:67]
	s_setprio 1
	s_barrier
	s_add_i32 s28, s42, s20
	v_lshl_add_u64 v[182:183], s[40:41], 0, v[184:185]
	s_mov_b32 m0, s28
	ds_read_b128 v[174:177], v149 offset:16384
	ds_read_b128 v[178:181], v149 offset:17408
	ds_read_b128 v[194:197], v149 offset:18432
	ds_read_b128 v[198:201], v149 offset:19456
	ds_read_b128 v[202:205], v149 offset:20480
	ds_read_b128 v[206:209], v149 offset:21504
	ds_read_b128 v[224:227], v149 offset:22528
	ds_read_b128 v[228:231], v149 offset:23552
	global_load_lds_dwordx4 v[182:183], off
	s_add_i32 m0, s28, 0x2000
	s_add_u32 s28, s40, 0x40000
	v_lshl_add_u64 v[210:211], s[40:41], 0, v[128:129]
	s_addc_u32 s29, s41, 0
	s_add_i32 s42, s43, s20
	global_load_lds_dwordx4 v[210:211], off
	v_lshl_add_u64 v[216:217], s[28:29], 0, v[184:185]
	s_mov_b32 m0, s42
	v_lshl_add_u64 v[218:219], s[44:45], 0, v[130:131]
	global_load_lds_dwordx4 v[216:217], off
	v_lshl_add_u64 v[216:217], s[28:29], 0, v[128:129]
	s_add_i32 m0, s42, 0x2000
	s_nop 0
	global_load_lds_dwordx4 v[216:217], off
	v_lshl_add_u64 v[216:217], s[44:45], 0, v[132:133]
	s_mov_b32 m0, s21
	s_nop 0
	global_load_lds_dwordx4 v[216:217], off
	s_mov_b32 m0, s26
	s_nop 0
	global_load_lds_dwordx4 v[218:219], off
	s_waitcnt vmcnt(8)
	s_waitcnt lgkmcnt(0)
	s_barrier
	s_setprio 0
	s_waitcnt lgkmcnt(0)
	v_mfma_f32_16x16x32_bf16 v[60:63], v[138:141], v[174:177], v[60:63]
	v_mfma_f32_16x16x32_bf16 v[56:59], v[150:153], v[174:177], v[56:59]
	v_mfma_f32_16x16x32_bf16 v[44:47], v[138:141], v[194:197], v[44:47]
	v_mfma_f32_16x16x32_bf16 v[40:43], v[150:153], v[194:197], v[40:43]
	v_mfma_f32_16x16x32_bf16 v[28:31], v[138:141], v[202:205], v[28:31]
	v_mfma_f32_16x16x32_bf16 v[24:27], v[150:153], v[202:205], v[24:27]
	v_mfma_f32_16x16x32_bf16 v[12:15], v[138:141], v[224:227], v[12:15]
	v_mfma_f32_16x16x32_bf16 v[8:11], v[150:153], v[224:227], v[8:11]
	v_mfma_f32_16x16x32_bf16 v[60:63], v[142:145], v[178:181], v[60:63]
	v_mfma_f32_16x16x32_bf16 v[56:59], v[154:157], v[178:181], v[56:59]
	v_mfma_f32_16x16x32_bf16 v[44:47], v[142:145], v[198:201], v[44:47]
	v_mfma_f32_16x16x32_bf16 v[40:43], v[154:157], v[198:201], v[40:43]
	v_mfma_f32_16x16x32_bf16 v[28:31], v[142:145], v[206:209], v[28:31]
	v_mfma_f32_16x16x32_bf16 v[24:27], v[154:157], v[206:209], v[24:27]
	v_mfma_f32_16x16x32_bf16 v[12:15], v[142:145], v[228:231], v[12:15]
	v_mfma_f32_16x16x32_bf16 v[8:11], v[154:157], v[228:231], v[8:11]
	s_setprio 1
	s_setprio 0
	v_mfma_f32_16x16x32_bf16 v[52:55], v[158:161], v[174:177], v[52:55]
	v_mfma_f32_16x16x32_bf16 v[48:51], v[166:169], v[174:177], v[48:51]
	v_mfma_f32_16x16x32_bf16 v[36:39], v[158:161], v[194:197], v[36:39]
	v_mfma_f32_16x16x32_bf16 v[32:35], v[166:169], v[194:197], v[32:35]
	v_mfma_f32_16x16x32_bf16 v[20:23], v[158:161], v[202:205], v[20:23]
	v_mfma_f32_16x16x32_bf16 v[16:19], v[166:169], v[202:205], v[16:19]
	v_mfma_f32_16x16x32_bf16 v[4:7], v[158:161], v[224:227], v[4:7]
	v_mfma_f32_16x16x32_bf16 v[0:3], v[166:169], v[224:227], v[0:3]
	v_mfma_f32_16x16x32_bf16 v[52:55], v[162:165], v[178:181], v[52:55]
	v_mfma_f32_16x16x32_bf16 v[48:51], v[170:173], v[178:181], v[48:51]
	v_mfma_f32_16x16x32_bf16 v[36:39], v[162:165], v[198:201], v[36:39]
	v_mfma_f32_16x16x32_bf16 v[32:35], v[170:173], v[198:201], v[32:35]
	v_mfma_f32_16x16x32_bf16 v[20:23], v[162:165], v[206:209], v[20:23]
	v_mfma_f32_16x16x32_bf16 v[16:19], v[170:173], v[206:209], v[16:19]
	v_mfma_f32_16x16x32_bf16 v[4:7], v[162:165], v[228:231], v[4:7]
	v_mfma_f32_16x16x32_bf16 v[0:3], v[170:173], v[228:231], v[0:3]
	s_setprio 1
	s_barrier
	s_add_i32 s42, 0, 0x18000
	s_add_i32 s43, 0, 0x1c000
	v_add_u32_e32 v154, s42, v147
	v_add_u32_e32 v170, s43, v147
	ds_read_b128 v[138:141], v154
	ds_read_b128 v[142:145], v154 offset:1024
	ds_read_b128 v[150:153], v154 offset:2048
	ds_read_b128 v[154:157], v154 offset:3072
	ds_read_b128 v[158:161], v170
	ds_read_b128 v[162:165], v170 offset:1024
	ds_read_b128 v[166:169], v170 offset:2048
	ds_read_b128 v[170:173], v170 offset:3072
	s_add_u32 s28, s44, 0x40000
	s_addc_u32 s29, s45, 0
	s_mov_b32 m0, s27
	v_lshl_add_u64 v[232:233], s[28:29], 0, v[132:133]
	ds_read_b128 v[174:177], v149 offset:32768
	ds_read_b128 v[178:181], v149 offset:33792
	ds_read_b128 v[194:197], v149 offset:34816
	ds_read_b128 v[198:201], v149 offset:35840
	ds_read_b128 v[202:205], v149 offset:36864
	ds_read_b128 v[206:209], v149 offset:37888
	ds_read_b128 v[224:227], v149 offset:38912
	ds_read_b128 v[228:231], v149 offset:39936
	global_load_lds_dwordx4 v[232:233], off
	v_lshl_add_u64 v[232:233], s[28:29], 0, v[130:131]
	s_mov_b32 m0, s46
	s_nop 0
	global_load_lds_dwordx4 v[232:233], off
	s_waitcnt vmcnt(8)
	s_waitcnt lgkmcnt(0)
	s_barrier
	s_setprio 0
	s_waitcnt lgkmcnt(0)
	v_mfma_f32_16x16x32_bf16 v[124:127], v[138:141], v[174:177], v[124:127]
	v_mfma_f32_16x16x32_bf16 v[120:123], v[150:153], v[174:177], v[120:123]
	v_mfma_f32_16x16x32_bf16 v[108:111], v[138:141], v[194:197], v[108:111]
	v_mfma_f32_16x16x32_bf16 v[104:107], v[150:153], v[194:197], v[104:107]
	v_mfma_f32_16x16x32_bf16 v[92:95], v[138:141], v[202:205], v[92:95]
	v_mfma_f32_16x16x32_bf16 v[88:91], v[150:153], v[202:205], v[88:91]
	v_mfma_f32_16x16x32_bf16 v[76:79], v[138:141], v[224:227], v[76:79]
	v_mfma_f32_16x16x32_bf16 v[72:75], v[150:153], v[224:227], v[72:75]
	v_mfma_f32_16x16x32_bf16 v[124:127], v[142:145], v[178:181], v[124:127]
	v_mfma_f32_16x16x32_bf16 v[120:123], v[154:157], v[178:181], v[120:123]
	v_mfma_f32_16x16x32_bf16 v[108:111], v[142:145], v[198:201], v[108:111]
	v_mfma_f32_16x16x32_bf16 v[104:107], v[154:157], v[198:201], v[104:107]
	v_mfma_f32_16x16x32_bf16 v[92:95], v[142:145], v[206:209], v[92:95]
	v_mfma_f32_16x16x32_bf16 v[88:91], v[154:157], v[206:209], v[88:91]
	v_mfma_f32_16x16x32_bf16 v[76:79], v[142:145], v[228:231], v[76:79]
	v_mfma_f32_16x16x32_bf16 v[72:75], v[154:157], v[228:231], v[72:75]
	s_setprio 1
	s_setprio 0
	v_mfma_f32_16x16x32_bf16 v[116:119], v[158:161], v[174:177], v[116:119]
	v_mfma_f32_16x16x32_bf16 v[112:115], v[166:169], v[174:177], v[112:115]
	v_mfma_f32_16x16x32_bf16 v[100:103], v[158:161], v[194:197], v[100:103]
	v_mfma_f32_16x16x32_bf16 v[96:99], v[166:169], v[194:197], v[96:99]
	v_mfma_f32_16x16x32_bf16 v[84:87], v[158:161], v[202:205], v[84:87]
	v_mfma_f32_16x16x32_bf16 v[80:83], v[166:169], v[202:205], v[80:83]
	v_mfma_f32_16x16x32_bf16 v[68:71], v[158:161], v[224:227], v[68:71]
	v_mfma_f32_16x16x32_bf16 v[64:67], v[166:169], v[224:227], v[64:67]
	v_mfma_f32_16x16x32_bf16 v[116:119], v[162:165], v[178:181], v[116:119]
	v_mfma_f32_16x16x32_bf16 v[112:115], v[170:173], v[178:181], v[112:115]
	v_mfma_f32_16x16x32_bf16 v[100:103], v[162:165], v[198:201], v[100:103]
	v_mfma_f32_16x16x32_bf16 v[96:99], v[170:173], v[198:201], v[96:99]
	v_mfma_f32_16x16x32_bf16 v[84:87], v[162:165], v[206:209], v[84:87]
	v_mfma_f32_16x16x32_bf16 v[80:83], v[170:173], v[206:209], v[80:83]
	v_mfma_f32_16x16x32_bf16 v[68:71], v[162:165], v[228:231], v[68:71]
	v_mfma_f32_16x16x32_bf16 v[64:67], v[170:173], v[228:231], v[64:67]
	s_setprio 1
	s_barrier
	s_add_i32 s28, s42, s20
	v_lshl_add_u64 v[182:183], v[182:183], 0, s[68:69]
	s_mov_b32 m0, s28
	ds_read_b128 v[174:177], v149 offset:49152
	ds_read_b128 v[178:181], v149 offset:50176
	ds_read_b128 v[194:197], v149 offset:51200
	ds_read_b128 v[198:201], v149 offset:52224
	ds_read_b128 v[202:205], v149 offset:53248
	ds_read_b128 v[206:209], v149 offset:54272
	ds_read_b128 v[224:227], v149 offset:55296
	ds_read_b128 v[228:231], v149 offset:56320
	global_load_lds_dwordx4 v[182:183], off
	s_add_i32 m0, s28, 0x2000
	s_add_u32 s28, s40, 0x40080
	v_lshl_add_u64 v[182:183], v[210:211], 0, s[68:69]
	s_addc_u32 s29, s41, 0
	s_add_i32 s40, s43, s20
	global_load_lds_dwordx4 v[182:183], off
	v_lshl_add_u64 v[182:183], s[28:29], 0, v[184:185]
	s_mov_b32 m0, s40
	s_nop 0
	global_load_lds_dwordx4 v[182:183], off
	v_lshl_add_u64 v[182:183], s[28:29], 0, v[128:129]
	s_add_i32 m0, s40, 0x2000
	s_nop 0
	global_load_lds_dwordx4 v[182:183], off
	v_lshl_add_u64 v[182:183], v[216:217], 0, s[68:69]
	s_mov_b32 m0, s47
	s_nop 0
	global_load_lds_dwordx4 v[182:183], off
	v_lshl_add_u64 v[182:183], v[218:219], 0, s[68:69]
	s_mov_b32 m0, s50
	s_nop 0
	global_load_lds_dwordx4 v[182:183], off
	s_waitcnt vmcnt(8)
	s_waitcnt lgkmcnt(0)
	s_barrier
	s_setprio 0
	s_waitcnt lgkmcnt(0)
	v_mfma_f32_16x16x32_bf16 v[60:63], v[138:141], v[174:177], v[60:63]
	v_mfma_f32_16x16x32_bf16 v[56:59], v[150:153], v[174:177], v[56:59]
	v_mfma_f32_16x16x32_bf16 v[44:47], v[138:141], v[194:197], v[44:47]
	v_mfma_f32_16x16x32_bf16 v[40:43], v[150:153], v[194:197], v[40:43]
	v_mfma_f32_16x16x32_bf16 v[28:31], v[138:141], v[202:205], v[28:31]
	v_mfma_f32_16x16x32_bf16 v[24:27], v[150:153], v[202:205], v[24:27]
	v_mfma_f32_16x16x32_bf16 v[12:15], v[138:141], v[224:227], v[12:15]
	v_mfma_f32_16x16x32_bf16 v[8:11], v[150:153], v[224:227], v[8:11]
	v_mfma_f32_16x16x32_bf16 v[60:63], v[142:145], v[178:181], v[60:63]
	v_mfma_f32_16x16x32_bf16 v[56:59], v[154:157], v[178:181], v[56:59]
	v_mfma_f32_16x16x32_bf16 v[44:47], v[142:145], v[198:201], v[44:47]
	v_mfma_f32_16x16x32_bf16 v[40:43], v[154:157], v[198:201], v[40:43]
	v_mfma_f32_16x16x32_bf16 v[28:31], v[142:145], v[206:209], v[28:31]
	v_mfma_f32_16x16x32_bf16 v[24:27], v[154:157], v[206:209], v[24:27]
	v_mfma_f32_16x16x32_bf16 v[12:15], v[142:145], v[228:231], v[12:15]
	v_mfma_f32_16x16x32_bf16 v[8:11], v[154:157], v[228:231], v[8:11]
	s_setprio 1
	s_setprio 0
	v_mfma_f32_16x16x32_bf16 v[52:55], v[158:161], v[174:177], v[52:55]
	v_mfma_f32_16x16x32_bf16 v[48:51], v[166:169], v[174:177], v[48:51]
	v_mfma_f32_16x16x32_bf16 v[36:39], v[158:161], v[194:197], v[36:39]
	v_mfma_f32_16x16x32_bf16 v[32:35], v[166:169], v[194:197], v[32:35]
	v_mfma_f32_16x16x32_bf16 v[20:23], v[158:161], v[202:205], v[20:23]
	v_mfma_f32_16x16x32_bf16 v[16:19], v[166:169], v[202:205], v[16:19]
	v_mfma_f32_16x16x32_bf16 v[4:7], v[158:161], v[224:227], v[4:7]
	v_mfma_f32_16x16x32_bf16 v[0:3], v[166:169], v[224:227], v[0:3]
	v_mfma_f32_16x16x32_bf16 v[52:55], v[162:165], v[178:181], v[52:55]
	v_mfma_f32_16x16x32_bf16 v[48:51], v[170:173], v[178:181], v[48:51]
	v_mfma_f32_16x16x32_bf16 v[36:39], v[162:165], v[198:201], v[36:39]
	v_mfma_f32_16x16x32_bf16 v[32:35], v[170:173], v[198:201], v[32:35]
	v_mfma_f32_16x16x32_bf16 v[20:23], v[162:165], v[206:209], v[20:23]
	v_mfma_f32_16x16x32_bf16 v[16:19], v[170:173], v[206:209], v[16:19]
	v_mfma_f32_16x16x32_bf16 v[4:7], v[162:165], v[228:231], v[4:7]
	v_mfma_f32_16x16x32_bf16 v[0:3], v[170:173], v[228:231], v[0:3]
	s_setprio 1
	s_barrier
	s_add_i32 s60, s60, 2
	s_add_u32 s30, s30, 0x100
	s_addc_u32 s31, s31, 0
	s_add_u32 s58, s58, 0x100
	s_addc_u32 s59, s59, 0
	s_cmp_gt_u32 s60, 13
	s_cbranch_scc0 .LBB0_842
	s_and_b64 vcc, exec, s[6:7]
	s_cbranch_vccz .LBB0_845
	s_barrier

.LBB0_859:
	s_add_u32 s42, s40, s50
	s_addc_u32 s43, s41, 0
	s_add_u32 s48, s42, 0x100
	s_addc_u32 s49, s43, 0
	s_and_b64 s[28:29], s[46:47], exec
	s_cselect_b32 s53, s11, s49
	s_cselect_b32 s52, s13, s48
	s_add_u32 s28, s6, s50
	s_addc_u32 s29, s7, 0
	s_add_u32 s48, s28, 0x100
	s_addc_u32 s49, s29, 0
	s_add_i32 s76, 0, 0x10000
	s_and_b64 s[28:29], s[46:47], exec
	s_cselect_b32 s59, s93, s49
	s_cselect_b32 s58, s94, s48
	s_add_i32 s29, 0, 0x14000
	s_add_u32 s62, s42, 0x40080
	s_addc_u32 s63, s43, 0
	s_add_i32 s85, s76, s20
	s_add_i32 m0, s21, 0xc000
	s_add_i32 s90, s21, 0xe000
	s_add_i32 s42, s85, 0x2000
	v_add_u32_e32 v153, s76, v150
	s_add_u32 s60, s58, 0x40000
	ds_read_b128 v[154:157], v153
	ds_read_b128 v[158:161], v153 offset:1024
	ds_read_b128 v[162:165], v153 offset:2048
	ds_read_b128 v[166:169], v153 offset:3072
	v_add_u32_e32 v153, s29, v150
	s_addc_u32 s61, s59, 0
	s_add_i32 s49, s29, s20
	ds_read_b128 v[170:173], v153
	ds_read_b128 v[174:177], v153 offset:1024
	ds_read_b128 v[178:181], v153 offset:2048
	ds_read_b128 v[194:197], v153 offset:3072
	s_add_i32 s43, s49, 0x2000
	s_add_i32 s48, 0, 0x18000
	s_add_i32 s28, 0, 0x1c000
	s_add_u32 s50, s52, 0x40000
	s_addc_u32 s51, s53, 0
	s_add_i32 vcc_lo, s48, s20
	s_add_i32 s95, vcc_lo, 0x2000
	s_add_u32 s46, s58, 0x40080
	s_addc_u32 s47, s59, 0
	s_add_i32 s76, s28, s20
	s_add_i32 s29, s76, 0x2000
	v_lshl_add_u64 v[182:183], s[62:63], 0, v[132:133]
	ds_read_b128 v[198:201], v152
	ds_read_b128 v[202:205], v152 offset:1024
	ds_read_b128 v[206:209], v152 offset:2048
	ds_read_b128 v[224:227], v152 offset:3072
	ds_read_b128 v[228:231], v152 offset:4096
	ds_read_b128 v[232:235], v152 offset:5120
	ds_read_b128 v[236:239], v152 offset:6144
	ds_read_b128 v[240:243], v152 offset:7168
	global_load_lds_dwordx4 v[182:183], off
	v_lshl_add_u64 v[182:183], s[62:63], 0, v[130:131]
	s_mov_b32 m0, s90
	s_nop 0
	global_load_lds_dwordx4 v[182:183], off
	s_waitcnt vmcnt(8)
	s_waitcnt lgkmcnt(0)
	s_barrier
	s_setprio 0
	s_waitcnt lgkmcnt(0)
	v_mfma_f32_16x16x32_bf16 v[124:127], v[154:157], v[198:201], v[124:127]
	v_mfma_f32_16x16x32_bf16 v[120:123], v[162:165], v[198:201], v[120:123]
	v_mfma_f32_16x16x32_bf16 v[116:119], v[154:157], v[206:209], v[116:119]
	v_mfma_f32_16x16x32_bf16 v[112:115], v[162:165], v[206:209], v[112:115]
	v_mfma_f32_16x16x32_bf16 v[108:111], v[154:157], v[228:231], v[108:111]
	v_mfma_f32_16x16x32_bf16 v[104:107], v[162:165], v[228:231], v[104:107]
	v_mfma_f32_16x16x32_bf16 v[96:99], v[154:157], v[236:239], v[96:99]
	v_mfma_f32_16x16x32_bf16 v[88:91], v[162:165], v[236:239], v[88:91]
	v_mfma_f32_16x16x32_bf16 v[124:127], v[158:161], v[202:205], v[124:127]
	v_mfma_f32_16x16x32_bf16 v[120:123], v[166:169], v[202:205], v[120:123]
	v_mfma_f32_16x16x32_bf16 v[116:119], v[158:161], v[224:227], v[116:119]
	v_mfma_f32_16x16x32_bf16 v[112:115], v[166:169], v[224:227], v[112:115]
	v_mfma_f32_16x16x32_bf16 v[108:111], v[158:161], v[232:235], v[108:111]
	v_mfma_f32_16x16x32_bf16 v[104:107], v[166:169], v[232:235], v[104:107]
	v_mfma_f32_16x16x32_bf16 v[96:99], v[158:161], v[240:243], v[96:99]
	v_mfma_f32_16x16x32_bf16 v[88:91], v[166:169], v[240:243], v[88:91]
	s_setprio 1
	s_setprio 0
	v_mfma_f32_16x16x32_bf16 v[100:103], v[170:173], v[198:201], v[100:103]
	v_mfma_f32_16x16x32_bf16 v[92:95], v[178:181], v[198:201], v[92:95]
	v_mfma_f32_16x16x32_bf16 v[84:87], v[170:173], v[206:209], v[84:87]
	v_mfma_f32_16x16x32_bf16 v[80:83], v[178:181], v[206:209], v[80:83]
	v_mfma_f32_16x16x32_bf16 v[76:79], v[170:173], v[228:231], v[76:79]
	v_mfma_f32_16x16x32_bf16 v[72:75], v[178:181], v[228:231], v[72:75]
	v_mfma_f32_16x16x32_bf16 v[68:71], v[170:173], v[236:239], v[68:71]
	v_mfma_f32_16x16x32_bf16 v[64:67], v[178:181], v[236:239], v[64:67]
	v_mfma_f32_16x16x32_bf16 v[100:103], v[174:177], v[202:205], v[100:103]
	v_mfma_f32_16x16x32_bf16 v[92:95], v[194:197], v[202:205], v[92:95]
	v_mfma_f32_16x16x32_bf16 v[84:87], v[174:177], v[224:227], v[84:87]
	v_mfma_f32_16x16x32_bf16 v[80:83], v[194:197], v[224:227], v[80:83]
	v_mfma_f32_16x16x32_bf16 v[76:79], v[174:177], v[232:235], v[76:79]
	v_mfma_f32_16x16x32_bf16 v[72:75], v[194:197], v[232:235], v[72:75]
	v_mfma_f32_16x16x32_bf16 v[68:71], v[174:177], v[240:243], v[68:71]
	v_mfma_f32_16x16x32_bf16 v[64:67], v[194:197], v[240:243], v[64:67]
	s_setprio 1
	s_barrier
	s_mov_b32 m0, s85
	v_lshl_add_u64 v[182:183], s[58:59], 0, v[184:185]
	ds_read_b128 v[198:201], v152 offset:16384
	ds_read_b128 v[202:205], v152 offset:17408
	ds_read_b128 v[206:209], v152 offset:18432
	ds_read_b128 v[224:227], v152 offset:19456
	ds_read_b128 v[228:231], v152 offset:20480
	ds_read_b128 v[232:235], v152 offset:21504
	ds_read_b128 v[236:239], v152 offset:22528
	ds_read_b128 v[240:243], v152 offset:23552
	global_load_lds_dwordx4 v[182:183], off
	v_lshl_add_u64 v[210:211], s[58:59], 0, v[128:129]
	s_mov_b32 m0, s42
	v_lshl_add_u64 v[216:217], s[60:61], 0, v[184:185]
	global_load_lds_dwordx4 v[210:211], off
	s_mov_b32 m0, s49
	v_lshl_add_u64 v[218:219], s[52:53], 0, v[130:131]
	global_load_lds_dwordx4 v[216:217], off
	v_lshl_add_u64 v[216:217], s[60:61], 0, v[128:129]
	s_mov_b32 m0, s43
	s_nop 0
	global_load_lds_dwordx4 v[216:217], off
	v_lshl_add_u64 v[216:217], s[52:53], 0, v[132:133]
	s_mov_b32 m0, s21
	s_nop 0
	global_load_lds_dwordx4 v[216:217], off
	s_mov_b32 m0, s26
	s_nop 0
	global_load_lds_dwordx4 v[218:219], off
	s_waitcnt vmcnt(8)
	s_waitcnt lgkmcnt(0)
	s_barrier
	s_setprio 0
	s_waitcnt lgkmcnt(0)
	v_mfma_f32_16x16x32_bf16 v[60:63], v[154:157], v[198:201], v[60:63]
	v_mfma_f32_16x16x32_bf16 v[56:59], v[162:165], v[198:201], v[56:59]
	v_mfma_f32_16x16x32_bf16 v[52:55], v[154:157], v[206:209], v[52:55]
	v_mfma_f32_16x16x32_bf16 v[48:51], v[162:165], v[206:209], v[48:51]
	v_mfma_f32_16x16x32_bf16 v[44:47], v[154:157], v[228:231], v[44:47]
	v_mfma_f32_16x16x32_bf16 v[40:43], v[162:165], v[228:231], v[40:43]
	v_mfma_f32_16x16x32_bf16 v[32:35], v[154:157], v[236:239], v[32:35]
	v_mfma_f32_16x16x32_bf16 v[24:27], v[162:165], v[236:239], v[24:27]
	v_mfma_f32_16x16x32_bf16 v[60:63], v[158:161], v[202:205], v[60:63]
	v_mfma_f32_16x16x32_bf16 v[56:59], v[166:169], v[202:205], v[56:59]
	v_mfma_f32_16x16x32_bf16 v[52:55], v[158:161], v[224:227], v[52:55]
	v_mfma_f32_16x16x32_bf16 v[48:51], v[166:169], v[224:227], v[48:51]
	v_mfma_f32_16x16x32_bf16 v[44:47], v[158:161], v[232:235], v[44:47]
	v_mfma_f32_16x16x32_bf16 v[40:43], v[166:169], v[232:235], v[40:43]
	v_mfma_f32_16x16x32_bf16 v[32:35], v[158:161], v[240:243], v[32:35]
	v_mfma_f32_16x16x32_bf16 v[24:27], v[166:169], v[240:243], v[24:27]
	s_setprio 1
	s_setprio 0
	v_mfma_f32_16x16x32_bf16 v[36:39], v[170:173], v[198:201], v[36:39]
	v_mfma_f32_16x16x32_bf16 v[28:31], v[178:181], v[198:201], v[28:31]
	v_mfma_f32_16x16x32_bf16 v[20:23], v[170:173], v[206:209], v[20:23]
	v_mfma_f32_16x16x32_bf16 v[16:19], v[178:181], v[206:209], v[16:19]
	v_mfma_f32_16x16x32_bf16 v[12:15], v[170:173], v[228:231], v[12:15]
	v_mfma_f32_16x16x32_bf16 v[8:11], v[178:181], v[228:231], v[8:11]
	v_mfma_f32_16x16x32_bf16 v[4:7], v[170:173], v[236:239], v[4:7]
	v_mfma_f32_16x16x32_bf16 v[0:3], v[178:181], v[236:239], v[0:3]
	v_mfma_f32_16x16x32_bf16 v[36:39], v[174:177], v[202:205], v[36:39]
	v_mfma_f32_16x16x32_bf16 v[28:31], v[194:197], v[202:205], v[28:31]
	v_mfma_f32_16x16x32_bf16 v[20:23], v[174:177], v[224:227], v[20:23]
	v_mfma_f32_16x16x32_bf16 v[16:19], v[194:197], v[224:227], v[16:19]
	v_mfma_f32_16x16x32_bf16 v[12:15], v[174:177], v[232:235], v[12:15]
	v_mfma_f32_16x16x32_bf16 v[8:11], v[194:197], v[232:235], v[8:11]
	v_mfma_f32_16x16x32_bf16 v[4:7], v[174:177], v[240:243], v[4:7]
	v_mfma_f32_16x16x32_bf16 v[0:3], v[194:197], v[240:243], v[0:3]
	s_setprio 1
	s_barrier
	v_add_u32_e32 v153, s48, v150
	ds_read_b128 v[154:157], v153
	ds_read_b128 v[158:161], v153 offset:1024
	ds_read_b128 v[162:165], v153 offset:2048
	ds_read_b128 v[166:169], v153 offset:3072
	v_add_u32_e32 v153, s28, v150
	ds_read_b128 v[170:173], v153
	ds_read_b128 v[174:177], v153 offset:1024
	ds_read_b128 v[178:181], v153 offset:2048
	ds_read_b128 v[194:197], v153 offset:3072
	s_mov_b32 m0, s27
	v_lshl_add_u64 v[244:245], s[50:51], 0, v[132:133]
	ds_read_b128 v[198:201], v152 offset:32768
	ds_read_b128 v[202:205], v152 offset:33792
	ds_read_b128 v[206:209], v152 offset:34816
	ds_read_b128 v[224:227], v152 offset:35840
	ds_read_b128 v[228:231], v152 offset:36864
	ds_read_b128 v[232:235], v152 offset:37888
	ds_read_b128 v[236:239], v152 offset:38912
	ds_read_b128 v[240:243], v152 offset:39936
	global_load_lds_dwordx4 v[244:245], off
	v_lshl_add_u64 v[244:245], s[50:51], 0, v[130:131]
	s_mov_b32 m0, s79
	s_nop 0
	global_load_lds_dwordx4 v[244:245], off
	s_waitcnt vmcnt(8)
	s_waitcnt lgkmcnt(0)
	s_barrier
	s_setprio 0
	s_waitcnt lgkmcnt(0)
	v_mfma_f32_16x16x32_bf16 v[124:127], v[154:157], v[198:201], v[124:127]
	v_mfma_f32_16x16x32_bf16 v[120:123], v[162:165], v[198:201], v[120:123]
	v_mfma_f32_16x16x32_bf16 v[116:119], v[154:157], v[206:209], v[116:119]
	v_mfma_f32_16x16x32_bf16 v[112:115], v[162:165], v[206:209], v[112:115]
	v_mfma_f32_16x16x32_bf16 v[108:111], v[154:157], v[228:231], v[108:111]
	v_mfma_f32_16x16x32_bf16 v[104:107], v[162:165], v[228:231], v[104:107]
	v_mfma_f32_16x16x32_bf16 v[96:99], v[154:157], v[236:239], v[96:99]
	v_mfma_f32_16x16x32_bf16 v[88:91], v[162:165], v[236:239], v[88:91]
	v_mfma_f32_16x16x32_bf16 v[124:127], v[158:161], v[202:205], v[124:127]
	v_mfma_f32_16x16x32_bf16 v[120:123], v[166:169], v[202:205], v[120:123]
	v_mfma_f32_16x16x32_bf16 v[116:119], v[158:161], v[224:227], v[116:119]
	v_mfma_f32_16x16x32_bf16 v[112:115], v[166:169], v[224:227], v[112:115]
	v_mfma_f32_16x16x32_bf16 v[108:111], v[158:161], v[232:235], v[108:111]
	v_mfma_f32_16x16x32_bf16 v[104:107], v[166:169], v[232:235], v[104:107]
	v_mfma_f32_16x16x32_bf16 v[96:99], v[158:161], v[240:243], v[96:99]
	v_mfma_f32_16x16x32_bf16 v[88:91], v[166:169], v[240:243], v[88:91]
	s_setprio 1
	s_setprio 0
	v_mfma_f32_16x16x32_bf16 v[100:103], v[170:173], v[198:201], v[100:103]
	v_mfma_f32_16x16x32_bf16 v[92:95], v[178:181], v[198:201], v[92:95]
	v_mfma_f32_16x16x32_bf16 v[84:87], v[170:173], v[206:209], v[84:87]
	v_mfma_f32_16x16x32_bf16 v[80:83], v[178:181], v[206:209], v[80:83]
	v_mfma_f32_16x16x32_bf16 v[76:79], v[170:173], v[228:231], v[76:79]
	v_mfma_f32_16x16x32_bf16 v[72:75], v[178:181], v[228:231], v[72:75]
	v_mfma_f32_16x16x32_bf16 v[68:71], v[170:173], v[236:239], v[68:71]
	v_mfma_f32_16x16x32_bf16 v[64:67], v[178:181], v[236:239], v[64:67]
	v_mfma_f32_16x16x32_bf16 v[100:103], v[174:177], v[202:205], v[100:103]
	v_mfma_f32_16x16x32_bf16 v[92:95], v[194:197], v[202:205], v[92:95]
	v_mfma_f32_16x16x32_bf16 v[84:87], v[174:177], v[224:227], v[84:87]
	v_mfma_f32_16x16x32_bf16 v[80:83], v[194:197], v[224:227], v[80:83]
	v_mfma_f32_16x16x32_bf16 v[76:79], v[174:177], v[232:235], v[76:79]
	v_mfma_f32_16x16x32_bf16 v[72:75], v[194:197], v[232:235], v[72:75]
	v_mfma_f32_16x16x32_bf16 v[68:71], v[174:177], v[240:243], v[68:71]
	v_mfma_f32_16x16x32_bf16 v[64:67], v[194:197], v[240:243], v[64:67]
	s_setprio 1
	s_barrier
	s_mov_b32 m0, vcc_lo
	v_lshl_add_u64 v[182:183], v[182:183], 0, s[68:69]
	ds_read_b128 v[198:201], v152 offset:49152
	ds_read_b128 v[202:205], v152 offset:50176
	ds_read_b128 v[206:209], v152 offset:51200
	ds_read_b128 v[224:227], v152 offset:52224
	ds_read_b128 v[228:231], v152 offset:53248
	ds_read_b128 v[232:235], v152 offset:54272
	ds_read_b128 v[236:239], v152 offset:55296
	ds_read_b128 v[240:243], v152 offset:56320
	global_load_lds_dwordx4 v[182:183], off
	v_lshl_add_u64 v[182:183], v[210:211], 0, s[68:69]
	s_mov_b32 m0, s95
	s_nop 0
	global_load_lds_dwordx4 v[182:183], off
	v_lshl_add_u64 v[182:183], s[46:47], 0, v[184:185]
	s_mov_b32 m0, s76
	s_nop 0
	global_load_lds_dwordx4 v[182:183], off
	v_lshl_add_u64 v[182:183], s[46:47], 0, v[128:129]
	s_mov_b32 m0, s29
	s_nop 0
	global_load_lds_dwordx4 v[182:183], off
	v_lshl_add_u64 v[182:183], v[216:217], 0, s[68:69]
	s_mov_b32 m0, s88
	s_nop 0
	global_load_lds_dwordx4 v[182:183], off
	v_lshl_add_u64 v[182:183], v[218:219], 0, s[68:69]
	s_mov_b32 m0, s89
	s_nop 0
	global_load_lds_dwordx4 v[182:183], off
	s_waitcnt vmcnt(8)
	s_waitcnt lgkmcnt(0)
	s_barrier
	s_setprio 0
	s_waitcnt lgkmcnt(0)
	v_mfma_f32_16x16x32_bf16 v[60:63], v[154:157], v[198:201], v[60:63]
	v_mfma_f32_16x16x32_bf16 v[56:59], v[162:165], v[198:201], v[56:59]
	v_mfma_f32_16x16x32_bf16 v[52:55], v[154:157], v[206:209], v[52:55]
	v_mfma_f32_16x16x32_bf16 v[48:51], v[162:165], v[206:209], v[48:51]
	v_mfma_f32_16x16x32_bf16 v[44:47], v[154:157], v[228:231], v[44:47]
	v_mfma_f32_16x16x32_bf16 v[40:43], v[162:165], v[228:231], v[40:43]
	v_mfma_f32_16x16x32_bf16 v[32:35], v[154:157], v[236:239], v[32:35]
	v_mfma_f32_16x16x32_bf16 v[24:27], v[162:165], v[236:239], v[24:27]
	v_mfma_f32_16x16x32_bf16 v[60:63], v[158:161], v[202:205], v[60:63]
	v_mfma_f32_16x16x32_bf16 v[56:59], v[166:169], v[202:205], v[56:59]
	v_mfma_f32_16x16x32_bf16 v[52:55], v[158:161], v[224:227], v[52:55]
	v_mfma_f32_16x16x32_bf16 v[48:51], v[166:169], v[224:227], v[48:51]
	v_mfma_f32_16x16x32_bf16 v[44:47], v[158:161], v[232:235], v[44:47]
	v_mfma_f32_16x16x32_bf16 v[40:43], v[166:169], v[232:235], v[40:43]
	v_mfma_f32_16x16x32_bf16 v[32:35], v[158:161], v[240:243], v[32:35]
	v_mfma_f32_16x16x32_bf16 v[24:27], v[166:169], v[240:243], v[24:27]
	s_setprio 1
	s_setprio 0
	v_mfma_f32_16x16x32_bf16 v[36:39], v[170:173], v[198:201], v[36:39]
	v_mfma_f32_16x16x32_bf16 v[28:31], v[178:181], v[198:201], v[28:31]
	v_mfma_f32_16x16x32_bf16 v[20:23], v[170:173], v[206:209], v[20:23]
	v_mfma_f32_16x16x32_bf16 v[16:19], v[178:181], v[206:209], v[16:19]
	v_mfma_f32_16x16x32_bf16 v[12:15], v[170:173], v[228:231], v[12:15]
	v_mfma_f32_16x16x32_bf16 v[8:11], v[178:181], v[228:231], v[8:11]
	v_mfma_f32_16x16x32_bf16 v[4:7], v[170:173], v[236:239], v[4:7]
	v_mfma_f32_16x16x32_bf16 v[0:3], v[178:181], v[236:239], v[0:3]
	v_mfma_f32_16x16x32_bf16 v[36:39], v[174:177], v[202:205], v[36:39]
	v_mfma_f32_16x16x32_bf16 v[28:31], v[194:197], v[202:205], v[28:31]
	v_mfma_f32_16x16x32_bf16 v[20:23], v[174:177], v[224:227], v[20:23]
	v_mfma_f32_16x16x32_bf16 v[16:19], v[194:197], v[224:227], v[16:19]
	v_mfma_f32_16x16x32_bf16 v[12:15], v[174:177], v[232:235], v[12:15]
	v_mfma_f32_16x16x32_bf16 v[8:11], v[194:197], v[232:235], v[8:11]
	v_mfma_f32_16x16x32_bf16 v[4:7], v[174:177], v[240:243], v[4:7]
	v_mfma_f32_16x16x32_bf16 v[0:3], v[194:197], v[240:243], v[0:3]
	s_setprio 1
	s_barrier
	s_movk_i32 s50, 0x100
	s_andn2_b64 vcc, exec, s[44:45]
	s_mov_b64 s[46:47], -1
	s_mov_b64 s[44:45], 0
	s_cbranch_vccz .LBB0_859
	s_and_b64 vcc, exec, s[8:9]
	s_cbranch_vccz .LBB0_862
	s_barrier

.LBB0_991:
	s_add_u32 s28, s40, 0xfff80080
	s_addc_u32 s29, s41, -1
	s_add_i32 s48, 0, 0x10000
	s_cmp_eq_u32 s79, 28
	s_cselect_b32 s45, s11, s29
	s_cselect_b32 s44, s13, s28
	s_cselect_b32 s43, s60, s63
	s_cselect_b32 s42, s61, s62
	s_add_i32 s49, 0, 0x14000
	s_waitcnt vmcnt(0)
	v_add_u32_e32 v60, s48, v169
	v_add_u32_e32 v166, s49, v169
	ds_read_b128 v[40:43], v60
	ds_read_b128 v[44:47], v60 offset:1024
	ds_read_b128 v[56:59], v60 offset:2048
	ds_read_b128 v[60:63], v60 offset:3072
	ds_read_b128 v[144:147], v166
	ds_read_b128 v[148:151], v166 offset:1024
	ds_read_b128 v[162:165], v166 offset:2048
	ds_read_b128 v[172:175], v166 offset:3072
	v_lshl_add_u64 v[166:167], s[40:41], 0, v[158:159]
	s_add_i32 m0, s26, 0xc000
	ds_read_b128 v[176:179], v171
	ds_read_b128 v[180:183], v171 offset:1024
	ds_read_b128 v[194:197], v171 offset:2048
	ds_read_b128 v[198:201], v171 offset:3072
	ds_read_b128 v[202:205], v171 offset:4096
	ds_read_b128 v[206:209], v171 offset:5120
	ds_read_b128 v[224:227], v171 offset:6144
	ds_read_b128 v[228:231], v171 offset:7168
	global_load_lds_dwordx4 v[166:167], off
	v_lshl_add_u64 v[166:167], s[40:41], 0, v[160:161]
	s_add_i32 m0, s26, 0xe000
	s_nop 0
	global_load_lds_dwordx4 v[166:167], off
	s_waitcnt vmcnt(8)
	s_waitcnt lgkmcnt(0)
	s_barrier
	s_setprio 0
	s_waitcnt lgkmcnt(0)
	v_mfma_f32_16x16x32_bf16 v[140:143], v[40:43], v[176:179], v[140:143]
	v_mfma_f32_16x16x32_bf16 v[136:139], v[56:59], v[176:179], v[136:139]
	v_mfma_f32_16x16x32_bf16 v[124:127], v[40:43], v[194:197], v[124:127]
	v_mfma_f32_16x16x32_bf16 v[120:123], v[56:59], v[194:197], v[120:123]
	v_mfma_f32_16x16x32_bf16 v[108:111], v[40:43], v[202:205], v[108:111]
	v_mfma_f32_16x16x32_bf16 v[104:107], v[56:59], v[202:205], v[104:107]
	v_mfma_f32_16x16x32_bf16 v[92:95], v[40:43], v[224:227], v[92:95]
	v_mfma_f32_16x16x32_bf16 v[88:91], v[56:59], v[224:227], v[88:91]
	v_mfma_f32_16x16x32_bf16 v[140:143], v[44:47], v[180:183], v[140:143]
	v_mfma_f32_16x16x32_bf16 v[136:139], v[60:63], v[180:183], v[136:139]
	v_mfma_f32_16x16x32_bf16 v[124:127], v[44:47], v[198:201], v[124:127]
	v_mfma_f32_16x16x32_bf16 v[120:123], v[60:63], v[198:201], v[120:123]
	v_mfma_f32_16x16x32_bf16 v[108:111], v[44:47], v[206:209], v[108:111]
	v_mfma_f32_16x16x32_bf16 v[104:107], v[60:63], v[206:209], v[104:107]
	v_mfma_f32_16x16x32_bf16 v[92:95], v[44:47], v[228:231], v[92:95]
	v_mfma_f32_16x16x32_bf16 v[88:91], v[60:63], v[228:231], v[88:91]
	s_setprio 1
	s_setprio 0
	v_mfma_f32_16x16x32_bf16 v[132:135], v[144:147], v[176:179], v[132:135]
	v_mfma_f32_16x16x32_bf16 v[128:131], v[162:165], v[176:179], v[128:131]
	v_mfma_f32_16x16x32_bf16 v[116:119], v[144:147], v[194:197], v[116:119]
	v_mfma_f32_16x16x32_bf16 v[112:115], v[162:165], v[194:197], v[112:115]
	v_mfma_f32_16x16x32_bf16 v[100:103], v[144:147], v[202:205], v[100:103]
	v_mfma_f32_16x16x32_bf16 v[96:99], v[162:165], v[202:205], v[96:99]
	v_mfma_f32_16x16x32_bf16 v[84:87], v[144:147], v[224:227], v[84:87]
	v_mfma_f32_16x16x32_bf16 v[80:83], v[162:165], v[224:227], v[80:83]
	v_mfma_f32_16x16x32_bf16 v[132:135], v[148:151], v[180:183], v[132:135]
	v_mfma_f32_16x16x32_bf16 v[128:131], v[172:175], v[180:183], v[128:131]
	v_mfma_f32_16x16x32_bf16 v[116:119], v[148:151], v[198:201], v[116:119]
	v_mfma_f32_16x16x32_bf16 v[112:115], v[172:175], v[198:201], v[112:115]
	v_mfma_f32_16x16x32_bf16 v[100:103], v[148:151], v[206:209], v[100:103]
	v_mfma_f32_16x16x32_bf16 v[96:99], v[172:175], v[206:209], v[96:99]
	v_mfma_f32_16x16x32_bf16 v[84:87], v[148:151], v[228:231], v[84:87]
	v_mfma_f32_16x16x32_bf16 v[80:83], v[172:175], v[228:231], v[80:83]
	s_setprio 1
	s_barrier
	s_add_i32 s28, s48, s46
	v_lshl_add_u64 v[166:167], s[42:43], 0, v[184:185]
	s_mov_b32 m0, s28
	ds_read_b128 v[176:179], v171 offset:16384
	ds_read_b128 v[180:183], v171 offset:17408
	ds_read_b128 v[194:197], v171 offset:18432
	ds_read_b128 v[198:201], v171 offset:19456
	ds_read_b128 v[202:205], v171 offset:20480
	ds_read_b128 v[206:209], v171 offset:21504
	ds_read_b128 v[224:227], v171 offset:22528
	ds_read_b128 v[228:231], v171 offset:23552
	global_load_lds_dwordx4 v[166:167], off
	s_add_i32 m0, s28, 0x2000
	s_add_u32 s28, s42, 0x80000
	v_lshl_add_u64 v[210:211], s[42:43], 0, v[152:153]
	s_addc_u32 s29, s43, 0
	s_add_i32 s48, s49, s46
	global_load_lds_dwordx4 v[210:211], off
	v_lshl_add_u64 v[216:217], s[28:29], 0, v[184:185]
	s_mov_b32 m0, s48
	v_lshl_add_u64 v[218:219], s[44:45], 0, v[154:155]
	global_load_lds_dwordx4 v[216:217], off
	v_lshl_add_u64 v[216:217], s[28:29], 0, v[152:153]
	s_add_i32 m0, s48, 0x2000
	s_nop 0
	global_load_lds_dwordx4 v[216:217], off
	v_lshl_add_u64 v[216:217], s[44:45], 0, v[156:157]
	s_mov_b32 m0, s26
	s_nop 0
	global_load_lds_dwordx4 v[216:217], off
	s_mov_b32 m0, s27
	s_nop 0
	global_load_lds_dwordx4 v[218:219], off
	s_waitcnt vmcnt(8)
	s_waitcnt lgkmcnt(0)
	s_barrier
	s_setprio 0
	s_waitcnt lgkmcnt(0)
	v_mfma_f32_16x16x32_bf16 v[76:79], v[40:43], v[176:179], v[76:79]
	v_mfma_f32_16x16x32_bf16 v[72:75], v[56:59], v[176:179], v[72:75]
	v_mfma_f32_16x16x32_bf16 v[52:55], v[40:43], v[194:197], v[52:55]
	v_mfma_f32_16x16x32_bf16 v[48:51], v[56:59], v[194:197], v[48:51]
	v_mfma_f32_16x16x32_bf16 v[28:31], v[40:43], v[202:205], v[28:31]
	v_mfma_f32_16x16x32_bf16 v[24:27], v[56:59], v[202:205], v[24:27]
	v_mfma_f32_16x16x32_bf16 v[12:15], v[40:43], v[224:227], v[12:15]
	v_mfma_f32_16x16x32_bf16 v[8:11], v[56:59], v[224:227], v[8:11]
	v_mfma_f32_16x16x32_bf16 v[76:79], v[44:47], v[180:183], v[76:79]
	v_mfma_f32_16x16x32_bf16 v[72:75], v[60:63], v[180:183], v[72:75]
	v_mfma_f32_16x16x32_bf16 v[52:55], v[44:47], v[198:201], v[52:55]
	v_mfma_f32_16x16x32_bf16 v[48:51], v[60:63], v[198:201], v[48:51]
	v_mfma_f32_16x16x32_bf16 v[28:31], v[44:47], v[206:209], v[28:31]
	v_mfma_f32_16x16x32_bf16 v[24:27], v[60:63], v[206:209], v[24:27]
	v_mfma_f32_16x16x32_bf16 v[12:15], v[44:47], v[228:231], v[12:15]
	v_mfma_f32_16x16x32_bf16 v[8:11], v[60:63], v[228:231], v[8:11]
	s_setprio 1
	s_setprio 0
	v_mfma_f32_16x16x32_bf16 v[36:39], v[144:147], v[194:197], v[36:39]
	v_mfma_f32_16x16x32_bf16 v[32:35], v[162:165], v[194:197], v[32:35]
	v_mfma_f32_16x16x32_bf16 v[20:23], v[144:147], v[202:205], v[20:23]
	v_mfma_f32_16x16x32_bf16 v[16:19], v[162:165], v[202:205], v[16:19]
	v_mfma_f32_16x16x32_bf16 v[4:7], v[144:147], v[224:227], v[4:7]
	v_mfma_f32_16x16x32_bf16 v[0:3], v[162:165], v[224:227], v[0:3]
	v_mfma_f32_16x16x32_bf16 v[40:43], v[144:147], v[176:179], v[68:71]
	v_mfma_f32_16x16x32_bf16 v[44:47], v[162:165], v[176:179], v[64:67]
	v_mfma_f32_16x16x32_bf16 v[36:39], v[148:151], v[198:201], v[36:39]
	v_mfma_f32_16x16x32_bf16 v[32:35], v[172:175], v[198:201], v[32:35]
	v_mfma_f32_16x16x32_bf16 v[20:23], v[148:151], v[206:209], v[20:23]
	v_mfma_f32_16x16x32_bf16 v[16:19], v[172:175], v[206:209], v[16:19]
	v_mfma_f32_16x16x32_bf16 v[4:7], v[148:151], v[228:231], v[4:7]
	v_mfma_f32_16x16x32_bf16 v[0:3], v[172:175], v[228:231], v[0:3]
	v_mfma_f32_16x16x32_bf16 v[40:43], v[148:151], v[180:183], v[40:43]
	v_mfma_f32_16x16x32_bf16 v[44:47], v[172:175], v[180:183], v[44:47]
	s_setprio 1
	s_barrier
	s_add_i32 s48, 0, 0x18000
	s_add_i32 s49, 0, 0x1c000
	v_add_u32_e32 v68, s48, v169
	v_add_u32_e32 v172, s49, v169
	ds_read_b128 v[56:59], v68
	ds_read_b128 v[60:63], v68 offset:1024
	ds_read_b128 v[64:67], v68 offset:2048
	ds_read_b128 v[68:71], v68 offset:3072
	ds_read_b128 v[144:147], v172
	ds_read_b128 v[148:151], v172 offset:1024
	ds_read_b128 v[162:165], v172 offset:2048
	ds_read_b128 v[172:175], v172 offset:3072
	s_add_u32 s28, s44, 0x80000
	s_addc_u32 s29, s45, 0
	s_mov_b32 m0, s47
	v_lshl_add_u64 v[232:233], s[28:29], 0, v[156:157]
	ds_read_b128 v[176:179], v171 offset:32768
	ds_read_b128 v[180:183], v171 offset:33792
	ds_read_b128 v[194:197], v171 offset:34816
	ds_read_b128 v[198:201], v171 offset:35840
	ds_read_b128 v[202:205], v171 offset:36864
	ds_read_b128 v[206:209], v171 offset:37888
	ds_read_b128 v[224:227], v171 offset:38912
	ds_read_b128 v[228:231], v171 offset:39936
	global_load_lds_dwordx4 v[232:233], off
	v_lshl_add_u64 v[232:233], s[28:29], 0, v[154:155]
	s_mov_b32 m0, s50
	s_nop 0
	global_load_lds_dwordx4 v[232:233], off
	s_waitcnt vmcnt(8)
	s_waitcnt lgkmcnt(0)
	s_barrier
	s_setprio 0
	s_waitcnt lgkmcnt(0)
	v_mfma_f32_16x16x32_bf16 v[140:143], v[56:59], v[176:179], v[140:143]
	v_mfma_f32_16x16x32_bf16 v[136:139], v[64:67], v[176:179], v[136:139]
	v_mfma_f32_16x16x32_bf16 v[124:127], v[56:59], v[194:197], v[124:127]
	v_mfma_f32_16x16x32_bf16 v[120:123], v[64:67], v[194:197], v[120:123]
	v_mfma_f32_16x16x32_bf16 v[108:111], v[56:59], v[202:205], v[108:111]
	v_mfma_f32_16x16x32_bf16 v[104:107], v[64:67], v[202:205], v[104:107]
	v_mfma_f32_16x16x32_bf16 v[92:95], v[56:59], v[224:227], v[92:95]
	v_mfma_f32_16x16x32_bf16 v[88:91], v[64:67], v[224:227], v[88:91]
	v_mfma_f32_16x16x32_bf16 v[140:143], v[60:63], v[180:183], v[140:143]
	v_mfma_f32_16x16x32_bf16 v[136:139], v[68:71], v[180:183], v[136:139]
	v_mfma_f32_16x16x32_bf16 v[124:127], v[60:63], v[198:201], v[124:127]
	v_mfma_f32_16x16x32_bf16 v[120:123], v[68:71], v[198:201], v[120:123]
	v_mfma_f32_16x16x32_bf16 v[108:111], v[60:63], v[206:209], v[108:111]
	v_mfma_f32_16x16x32_bf16 v[104:107], v[68:71], v[206:209], v[104:107]
	v_mfma_f32_16x16x32_bf16 v[92:95], v[60:63], v[228:231], v[92:95]
	v_mfma_f32_16x16x32_bf16 v[88:91], v[68:71], v[228:231], v[88:91]
	s_setprio 1
	s_setprio 0
	v_mfma_f32_16x16x32_bf16 v[132:135], v[144:147], v[176:179], v[132:135]
	v_mfma_f32_16x16x32_bf16 v[128:131], v[162:165], v[176:179], v[128:131]
	v_mfma_f32_16x16x32_bf16 v[116:119], v[144:147], v[194:197], v[116:119]
	v_mfma_f32_16x16x32_bf16 v[112:115], v[162:165], v[194:197], v[112:115]
	v_mfma_f32_16x16x32_bf16 v[100:103], v[144:147], v[202:205], v[100:103]
	v_mfma_f32_16x16x32_bf16 v[96:99], v[162:165], v[202:205], v[96:99]
	v_mfma_f32_16x16x32_bf16 v[84:87], v[144:147], v[224:227], v[84:87]
	v_mfma_f32_16x16x32_bf16 v[80:83], v[162:165], v[224:227], v[80:83]
	v_mfma_f32_16x16x32_bf16 v[132:135], v[148:151], v[180:183], v[132:135]
	v_mfma_f32_16x16x32_bf16 v[128:131], v[172:175], v[180:183], v[128:131]
	v_mfma_f32_16x16x32_bf16 v[116:119], v[148:151], v[198:201], v[116:119]
	v_mfma_f32_16x16x32_bf16 v[112:115], v[172:175], v[198:201], v[112:115]
	v_mfma_f32_16x16x32_bf16 v[100:103], v[148:151], v[206:209], v[100:103]
	v_mfma_f32_16x16x32_bf16 v[96:99], v[172:175], v[206:209], v[96:99]
	v_mfma_f32_16x16x32_bf16 v[84:87], v[148:151], v[228:231], v[84:87]
	v_mfma_f32_16x16x32_bf16 v[80:83], v[172:175], v[228:231], v[80:83]
	s_setprio 1
	s_barrier
	s_add_i32 s28, s48, s46
	v_lshl_add_u64 v[166:167], v[166:167], 0, s[68:69]
	s_mov_b32 m0, s28
	ds_read_b128 v[176:179], v171 offset:49152
	ds_read_b128 v[180:183], v171 offset:50176
	ds_read_b128 v[194:197], v171 offset:51200
	ds_read_b128 v[198:201], v171 offset:52224
	ds_read_b128 v[202:205], v171 offset:53248
	ds_read_b128 v[206:209], v171 offset:54272
	ds_read_b128 v[224:227], v171 offset:55296
	ds_read_b128 v[228:231], v171 offset:56320
	global_load_lds_dwordx4 v[166:167], off
	s_add_i32 m0, s28, 0x2000
	s_add_u32 s28, s42, 0x80080
	v_lshl_add_u64 v[166:167], v[210:211], 0, s[68:69]
	s_addc_u32 s29, s43, 0
	s_add_i32 s42, s49, s46
	global_load_lds_dwordx4 v[166:167], off
	v_lshl_add_u64 v[166:167], s[28:29], 0, v[184:185]
	s_mov_b32 m0, s42
	s_nop 0
	global_load_lds_dwordx4 v[166:167], off
	v_lshl_add_u64 v[166:167], s[28:29], 0, v[152:153]
	s_add_i32 m0, s42, 0x2000
	s_nop 0
	global_load_lds_dwordx4 v[166:167], off
	v_lshl_add_u64 v[166:167], v[216:217], 0, s[68:69]
	s_mov_b32 m0, s53
	s_nop 0
	global_load_lds_dwordx4 v[166:167], off
	v_lshl_add_u64 v[166:167], v[218:219], 0, s[68:69]
	s_mov_b32 m0, s58
	s_nop 0
	global_load_lds_dwordx4 v[166:167], off
	s_waitcnt vmcnt(8)
	s_waitcnt lgkmcnt(0)
	s_barrier
	s_setprio 0
	s_waitcnt lgkmcnt(0)
	v_mfma_f32_16x16x32_bf16 v[76:79], v[56:59], v[176:179], v[76:79]
	v_mfma_f32_16x16x32_bf16 v[72:75], v[64:67], v[176:179], v[72:75]
	v_mfma_f32_16x16x32_bf16 v[52:55], v[56:59], v[194:197], v[52:55]
	v_mfma_f32_16x16x32_bf16 v[48:51], v[64:67], v[194:197], v[48:51]
	v_mfma_f32_16x16x32_bf16 v[28:31], v[56:59], v[202:205], v[28:31]
	v_mfma_f32_16x16x32_bf16 v[24:27], v[64:67], v[202:205], v[24:27]
	v_mfma_f32_16x16x32_bf16 v[12:15], v[56:59], v[224:227], v[12:15]
	v_mfma_f32_16x16x32_bf16 v[8:11], v[64:67], v[224:227], v[8:11]
	v_mfma_f32_16x16x32_bf16 v[76:79], v[60:63], v[180:183], v[76:79]
	v_mfma_f32_16x16x32_bf16 v[72:75], v[68:71], v[180:183], v[72:75]
	v_mfma_f32_16x16x32_bf16 v[52:55], v[60:63], v[198:201], v[52:55]
	v_mfma_f32_16x16x32_bf16 v[48:51], v[68:71], v[198:201], v[48:51]
	v_mfma_f32_16x16x32_bf16 v[28:31], v[60:63], v[206:209], v[28:31]
	v_mfma_f32_16x16x32_bf16 v[24:27], v[68:71], v[206:209], v[24:27]
	v_mfma_f32_16x16x32_bf16 v[12:15], v[60:63], v[228:231], v[12:15]
	v_mfma_f32_16x16x32_bf16 v[8:11], v[68:71], v[228:231], v[8:11]
	s_setprio 1
	s_setprio 0
	v_mfma_f32_16x16x32_bf16 v[40:43], v[144:147], v[176:179], v[40:43]
	v_mfma_f32_16x16x32_bf16 v[68:71], v[148:151], v[180:183], v[40:43]
	v_mfma_f32_16x16x32_bf16 v[40:43], v[162:165], v[176:179], v[44:47]
	v_mfma_f32_16x16x32_bf16 v[36:39], v[144:147], v[194:197], v[36:39]
	v_mfma_f32_16x16x32_bf16 v[32:35], v[162:165], v[194:197], v[32:35]
	v_mfma_f32_16x16x32_bf16 v[20:23], v[144:147], v[202:205], v[20:23]
	v_mfma_f32_16x16x32_bf16 v[16:19], v[162:165], v[202:205], v[16:19]
	v_mfma_f32_16x16x32_bf16 v[4:7], v[144:147], v[224:227], v[4:7]
	v_mfma_f32_16x16x32_bf16 v[0:3], v[162:165], v[224:227], v[0:3]
	v_mfma_f32_16x16x32_bf16 v[64:67], v[172:175], v[180:183], v[40:43]
	v_mfma_f32_16x16x32_bf16 v[36:39], v[148:151], v[198:201], v[36:39]
	v_mfma_f32_16x16x32_bf16 v[32:35], v[172:175], v[198:201], v[32:35]
	v_mfma_f32_16x16x32_bf16 v[20:23], v[148:151], v[206:209], v[20:23]
	v_mfma_f32_16x16x32_bf16 v[16:19], v[172:175], v[206:209], v[16:19]
	v_mfma_f32_16x16x32_bf16 v[4:7], v[148:151], v[228:231], v[4:7]
	v_mfma_f32_16x16x32_bf16 v[0:3], v[172:175], v[228:231], v[0:3]
	s_setprio 1
	s_barrier
	s_add_i32 s79, s79, 2
	s_add_u32 s40, s40, 0x100
	s_addc_u32 s41, s41, 0
	s_add_u32 s62, s62, 0x100
	s_addc_u32 s63, s63, 0
	s_cmp_gt_u32 s79, 29
	s_cbranch_scc0 .LBB0_991
	s_and_b64 vcc, exec, s[8:9]
	s_cbranch_vccz .LBB0_994
	s_barrier

.LBB0_1136:
	s_add_u32 s48, s42, s50
	s_addc_u32 s49, s43, 0
	s_add_u32 s51, s48, 0x100
	s_addc_u32 s52, s49, 0
	s_and_b64 s[28:29], s[46:47], exec
	s_cselect_b32 s53, s11, s52
	s_cselect_b32 s52, s13, s51
	s_add_u32 s28, s38, s50
	s_addc_u32 s29, s39, 0
	s_add_u32 s50, s28, 0x100
	s_addc_u32 s51, s29, 0
	s_add_i32 s76, 0, 0x10000
	s_and_b64 s[28:29], s[46:47], exec
	s_cselect_b32 s59, s93, s51
	s_cselect_b32 s58, s94, s50
	s_add_i32 s47, 0, 0x14000
	s_add_u32 s62, s48, 0x80080
	s_addc_u32 s63, s49, 0
	s_add_i32 s49, s76, s20
	s_add_i32 m0, s21, 0xc000
	s_add_i32 s91, s21, 0xe000
	s_add_i32 s29, s49, 0x2000
	s_add_u32 s60, s58, 0x80000
	v_add_u32_e32 v132, s76, v168
	v_add_u32_e32 v166, s47, v168
	s_addc_u32 s61, s59, 0
	s_add_i32 vcc_hi, s47, s20
	ds_read_b128 v[112:115], v132
	ds_read_b128 v[116:119], v132 offset:1024
	ds_read_b128 v[124:127], v132 offset:2048
	ds_read_b128 v[132:135], v132 offset:3072
	ds_read_b128 v[172:175], v166
	ds_read_b128 v[176:179], v166 offset:1024
	ds_read_b128 v[180:183], v166 offset:2048
	ds_read_b128 v[194:197], v166 offset:3072
	s_add_i32 s85, vcc_hi, 0x2000
	s_add_i32 s48, 0, 0x18000
	s_add_i32 s28, 0, 0x1c000
	s_add_u32 s50, s52, 0x80000
	s_addc_u32 s51, s53, 0
	s_add_i32 vcc_lo, s48, s20
	s_add_i32 s95, vcc_lo, 0x2000
	s_add_u32 s46, s58, 0x80080
	s_addc_u32 s47, s59, 0
	s_add_i32 s76, s28, s20
	s_add_i32 s90, s76, 0x2000
	v_lshl_add_u64 v[166:167], s[62:63], 0, v[148:149]
	ds_read_b128 v[198:201], v170
	ds_read_b128 v[202:205], v170 offset:1024
	ds_read_b128 v[206:209], v170 offset:2048
	ds_read_b128 v[224:227], v170 offset:3072
	ds_read_b128 v[228:231], v170 offset:4096
	ds_read_b128 v[232:235], v170 offset:5120
	ds_read_b128 v[236:239], v170 offset:6144
	ds_read_b128 v[240:243], v170 offset:7168
	global_load_lds_dwordx4 v[166:167], off
	v_lshl_add_u64 v[166:167], s[62:63], 0, v[146:147]
	s_mov_b32 m0, s91
	s_nop 0
	global_load_lds_dwordx4 v[166:167], off
	s_waitcnt vmcnt(8)
	s_waitcnt lgkmcnt(0)
	s_barrier
	s_setprio 0
	s_waitcnt lgkmcnt(0)
	v_mfma_f32_16x16x32_bf16 v[140:143], v[112:115], v[198:201], v[140:143]
	v_mfma_f32_16x16x32_bf16 v[136:139], v[124:127], v[198:201], v[136:139]
	v_mfma_f32_16x16x32_bf16 v[108:111], v[112:115], v[206:209], v[108:111]
	v_mfma_f32_16x16x32_bf16 v[104:107], v[124:127], v[206:209], v[104:107]
	v_mfma_f32_16x16x32_bf16 v[92:95], v[112:115], v[228:231], v[92:95]
	v_mfma_f32_16x16x32_bf16 v[88:91], v[124:127], v[228:231], v[88:91]
	v_mfma_f32_16x16x32_bf16 v[76:79], v[112:115], v[236:239], v[76:79]
	v_mfma_f32_16x16x32_bf16 v[72:75], v[124:127], v[236:239], v[72:75]
	v_mfma_f32_16x16x32_bf16 v[140:143], v[116:119], v[202:205], v[140:143]
	v_mfma_f32_16x16x32_bf16 v[136:139], v[132:135], v[202:205], v[136:139]
	v_mfma_f32_16x16x32_bf16 v[108:111], v[116:119], v[224:227], v[108:111]
	v_mfma_f32_16x16x32_bf16 v[104:107], v[132:135], v[224:227], v[104:107]
	v_mfma_f32_16x16x32_bf16 v[92:95], v[116:119], v[232:235], v[92:95]
	v_mfma_f32_16x16x32_bf16 v[88:91], v[132:135], v[232:235], v[88:91]
	v_mfma_f32_16x16x32_bf16 v[76:79], v[116:119], v[240:243], v[76:79]
	v_mfma_f32_16x16x32_bf16 v[72:75], v[132:135], v[240:243], v[72:75]
	s_setprio 1
	s_setprio 0
	v_mfma_f32_16x16x32_bf16 v[128:131], v[172:175], v[198:201], v[128:131]
	v_mfma_f32_16x16x32_bf16 v[120:123], v[180:183], v[198:201], v[120:123]
	v_mfma_f32_16x16x32_bf16 v[100:103], v[172:175], v[206:209], v[100:103]
	v_mfma_f32_16x16x32_bf16 v[96:99], v[180:183], v[206:209], v[96:99]
	v_mfma_f32_16x16x32_bf16 v[84:87], v[172:175], v[228:231], v[84:87]
	v_mfma_f32_16x16x32_bf16 v[80:83], v[180:183], v[228:231], v[80:83]
	v_mfma_f32_16x16x32_bf16 v[68:71], v[172:175], v[236:239], v[68:71]
	v_mfma_f32_16x16x32_bf16 v[64:67], v[180:183], v[236:239], v[64:67]
	v_mfma_f32_16x16x32_bf16 v[128:131], v[176:179], v[202:205], v[128:131]
	v_mfma_f32_16x16x32_bf16 v[120:123], v[194:197], v[202:205], v[120:123]
	v_mfma_f32_16x16x32_bf16 v[100:103], v[176:179], v[224:227], v[100:103]
	v_mfma_f32_16x16x32_bf16 v[96:99], v[194:197], v[224:227], v[96:99]
	v_mfma_f32_16x16x32_bf16 v[84:87], v[176:179], v[232:235], v[84:87]
	v_mfma_f32_16x16x32_bf16 v[80:83], v[194:197], v[232:235], v[80:83]
	v_mfma_f32_16x16x32_bf16 v[68:71], v[176:179], v[240:243], v[68:71]
	v_mfma_f32_16x16x32_bf16 v[64:67], v[194:197], v[240:243], v[64:67]
	s_setprio 1
	s_barrier
	s_mov_b32 m0, s49
	v_lshl_add_u64 v[166:167], s[58:59], 0, v[184:185]
	ds_read_b128 v[198:201], v170 offset:16384
	ds_read_b128 v[202:205], v170 offset:17408
	ds_read_b128 v[206:209], v170 offset:18432
	ds_read_b128 v[224:227], v170 offset:19456
	ds_read_b128 v[228:231], v170 offset:20480
	ds_read_b128 v[232:235], v170 offset:21504
	ds_read_b128 v[236:239], v170 offset:22528
	ds_read_b128 v[240:243], v170 offset:23552
	global_load_lds_dwordx4 v[166:167], off
	v_lshl_add_u64 v[210:211], s[58:59], 0, v[144:145]
	s_mov_b32 m0, s29
	v_lshl_add_u64 v[216:217], s[60:61], 0, v[184:185]
	global_load_lds_dwordx4 v[210:211], off
	s_mov_b32 m0, vcc_hi
	v_lshl_add_u64 v[218:219], s[52:53], 0, v[146:147]
	global_load_lds_dwordx4 v[216:217], off
	v_lshl_add_u64 v[216:217], s[60:61], 0, v[144:145]
	s_mov_b32 m0, s85
	s_nop 0
	global_load_lds_dwordx4 v[216:217], off
	v_lshl_add_u64 v[216:217], s[52:53], 0, v[148:149]
	s_mov_b32 m0, s21
	s_nop 0
	global_load_lds_dwordx4 v[216:217], off
	s_mov_b32 m0, s26
	s_nop 0
	global_load_lds_dwordx4 v[218:219], off
	s_waitcnt vmcnt(8)
	s_waitcnt lgkmcnt(0)
	s_barrier
	s_setprio 0
	s_waitcnt lgkmcnt(0)
	v_mfma_f32_16x16x32_bf16 v[60:63], v[112:115], v[198:201], v[60:63]
	v_mfma_f32_16x16x32_bf16 v[56:59], v[124:127], v[198:201], v[56:59]
	v_mfma_f32_16x16x32_bf16 v[44:47], v[112:115], v[206:209], v[44:47]
	v_mfma_f32_16x16x32_bf16 v[40:43], v[124:127], v[206:209], v[40:43]
	v_mfma_f32_16x16x32_bf16 v[36:39], v[112:115], v[228:231], v[36:39]
	v_mfma_f32_16x16x32_bf16 v[28:31], v[124:127], v[228:231], v[28:31]
	v_mfma_f32_16x16x32_bf16 v[20:23], v[112:115], v[236:239], v[20:23]
	v_mfma_f32_16x16x32_bf16 v[12:15], v[124:127], v[236:239], v[12:15]
	v_mfma_f32_16x16x32_bf16 v[60:63], v[116:119], v[202:205], v[60:63]
	v_mfma_f32_16x16x32_bf16 v[56:59], v[132:135], v[202:205], v[56:59]
	v_mfma_f32_16x16x32_bf16 v[44:47], v[116:119], v[224:227], v[44:47]
	v_mfma_f32_16x16x32_bf16 v[40:43], v[132:135], v[224:227], v[40:43]
	v_mfma_f32_16x16x32_bf16 v[36:39], v[116:119], v[232:235], v[36:39]
	v_mfma_f32_16x16x32_bf16 v[28:31], v[132:135], v[232:235], v[28:31]
	v_mfma_f32_16x16x32_bf16 v[20:23], v[116:119], v[240:243], v[20:23]
	v_mfma_f32_16x16x32_bf16 v[12:15], v[132:135], v[240:243], v[12:15]
	s_setprio 1
	s_setprio 0
	v_mfma_f32_16x16x32_bf16 v[52:55], v[172:175], v[198:201], v[52:55]
	v_mfma_f32_16x16x32_bf16 v[48:51], v[180:183], v[198:201], v[48:51]
	v_mfma_f32_16x16x32_bf16 v[32:35], v[172:175], v[206:209], v[32:35]
	v_mfma_f32_16x16x32_bf16 v[24:27], v[180:183], v[206:209], v[24:27]
	v_mfma_f32_16x16x32_bf16 v[16:19], v[172:175], v[228:231], v[16:19]
	v_mfma_f32_16x16x32_bf16 v[8:11], v[180:183], v[228:231], v[8:11]
	v_mfma_f32_16x16x32_bf16 v[4:7], v[172:175], v[236:239], v[4:7]
	v_mfma_f32_16x16x32_bf16 v[0:3], v[180:183], v[236:239], v[0:3]
	v_mfma_f32_16x16x32_bf16 v[52:55], v[176:179], v[202:205], v[52:55]
	v_mfma_f32_16x16x32_bf16 v[48:51], v[194:197], v[202:205], v[48:51]
	v_mfma_f32_16x16x32_bf16 v[32:35], v[176:179], v[224:227], v[32:35]
	v_mfma_f32_16x16x32_bf16 v[24:27], v[194:197], v[224:227], v[24:27]
	v_mfma_f32_16x16x32_bf16 v[16:19], v[176:179], v[232:235], v[16:19]
	v_mfma_f32_16x16x32_bf16 v[8:11], v[194:197], v[232:235], v[8:11]
	v_mfma_f32_16x16x32_bf16 v[4:7], v[176:179], v[240:243], v[4:7]
	v_mfma_f32_16x16x32_bf16 v[0:3], v[194:197], v[240:243], v[0:3]
	s_setprio 1
	s_barrier
	v_add_u32_e32 v132, s48, v168
	v_add_u32_e32 v171, s28, v168
	ds_read_b128 v[112:115], v132
	ds_read_b128 v[116:119], v132 offset:1024
	ds_read_b128 v[124:127], v132 offset:2048
	ds_read_b128 v[132:135], v132 offset:3072
	ds_read_b128 v[172:175], v171
	ds_read_b128 v[176:179], v171 offset:1024
	ds_read_b128 v[180:183], v171 offset:2048
	ds_read_b128 v[194:197], v171 offset:3072
	s_mov_b32 m0, s27
	v_lshl_add_u64 v[244:245], s[50:51], 0, v[148:149]
	ds_read_b128 v[198:201], v170 offset:32768
	ds_read_b128 v[202:205], v170 offset:33792
	ds_read_b128 v[206:209], v170 offset:34816
	ds_read_b128 v[224:227], v170 offset:35840
	ds_read_b128 v[228:231], v170 offset:36864
	ds_read_b128 v[232:235], v170 offset:37888
	ds_read_b128 v[236:239], v170 offset:38912
	ds_read_b128 v[240:243], v170 offset:39936
	global_load_lds_dwordx4 v[244:245], off
	v_lshl_add_u64 v[244:245], s[50:51], 0, v[146:147]
	s_mov_b32 m0, s79
	s_nop 0
	global_load_lds_dwordx4 v[244:245], off
	s_waitcnt vmcnt(8)
	s_waitcnt lgkmcnt(0)
	s_barrier
	s_setprio 0
	s_waitcnt lgkmcnt(0)
	v_mfma_f32_16x16x32_bf16 v[140:143], v[112:115], v[198:201], v[140:143]
	v_mfma_f32_16x16x32_bf16 v[136:139], v[124:127], v[198:201], v[136:139]
	v_mfma_f32_16x16x32_bf16 v[108:111], v[112:115], v[206:209], v[108:111]
	v_mfma_f32_16x16x32_bf16 v[104:107], v[124:127], v[206:209], v[104:107]
	v_mfma_f32_16x16x32_bf16 v[92:95], v[112:115], v[228:231], v[92:95]
	v_mfma_f32_16x16x32_bf16 v[88:91], v[124:127], v[228:231], v[88:91]
	v_mfma_f32_16x16x32_bf16 v[76:79], v[112:115], v[236:239], v[76:79]
	v_mfma_f32_16x16x32_bf16 v[72:75], v[124:127], v[236:239], v[72:75]
	v_mfma_f32_16x16x32_bf16 v[140:143], v[116:119], v[202:205], v[140:143]
	v_mfma_f32_16x16x32_bf16 v[136:139], v[132:135], v[202:205], v[136:139]
	v_mfma_f32_16x16x32_bf16 v[108:111], v[116:119], v[224:227], v[108:111]
	v_mfma_f32_16x16x32_bf16 v[104:107], v[132:135], v[224:227], v[104:107]
	v_mfma_f32_16x16x32_bf16 v[92:95], v[116:119], v[232:235], v[92:95]
	v_mfma_f32_16x16x32_bf16 v[88:91], v[132:135], v[232:235], v[88:91]
	v_mfma_f32_16x16x32_bf16 v[76:79], v[116:119], v[240:243], v[76:79]
	v_mfma_f32_16x16x32_bf16 v[72:75], v[132:135], v[240:243], v[72:75]
	s_setprio 1
	s_setprio 0
	v_mfma_f32_16x16x32_bf16 v[128:131], v[172:175], v[198:201], v[128:131]
	v_mfma_f32_16x16x32_bf16 v[120:123], v[180:183], v[198:201], v[120:123]
	v_mfma_f32_16x16x32_bf16 v[100:103], v[172:175], v[206:209], v[100:103]
	v_mfma_f32_16x16x32_bf16 v[96:99], v[180:183], v[206:209], v[96:99]
	v_mfma_f32_16x16x32_bf16 v[84:87], v[172:175], v[228:231], v[84:87]
	v_mfma_f32_16x16x32_bf16 v[80:83], v[180:183], v[228:231], v[80:83]
	v_mfma_f32_16x16x32_bf16 v[68:71], v[172:175], v[236:239], v[68:71]
	v_mfma_f32_16x16x32_bf16 v[64:67], v[180:183], v[236:239], v[64:67]
	v_mfma_f32_16x16x32_bf16 v[128:131], v[176:179], v[202:205], v[128:131]
	v_mfma_f32_16x16x32_bf16 v[120:123], v[194:197], v[202:205], v[120:123]
	v_mfma_f32_16x16x32_bf16 v[100:103], v[176:179], v[224:227], v[100:103]
	v_mfma_f32_16x16x32_bf16 v[96:99], v[194:197], v[224:227], v[96:99]
	v_mfma_f32_16x16x32_bf16 v[84:87], v[176:179], v[232:235], v[84:87]
	v_mfma_f32_16x16x32_bf16 v[80:83], v[194:197], v[232:235], v[80:83]
	v_mfma_f32_16x16x32_bf16 v[68:71], v[176:179], v[240:243], v[68:71]
	v_mfma_f32_16x16x32_bf16 v[64:67], v[194:197], v[240:243], v[64:67]
	s_setprio 1
	s_barrier
	s_mov_b32 m0, vcc_lo
	v_lshl_add_u64 v[166:167], v[166:167], 0, s[68:69]
	ds_read_b128 v[198:201], v170 offset:49152
	ds_read_b128 v[202:205], v170 offset:50176
	ds_read_b128 v[206:209], v170 offset:51200
	ds_read_b128 v[224:227], v170 offset:52224
	ds_read_b128 v[228:231], v170 offset:53248
	ds_read_b128 v[232:235], v170 offset:54272
	ds_read_b128 v[236:239], v170 offset:55296
	ds_read_b128 v[240:243], v170 offset:56320
	global_load_lds_dwordx4 v[166:167], off
	v_lshl_add_u64 v[166:167], v[210:211], 0, s[68:69]
	s_mov_b32 m0, s95
	s_nop 0
	global_load_lds_dwordx4 v[166:167], off
	v_lshl_add_u64 v[166:167], s[46:47], 0, v[184:185]
	s_mov_b32 m0, s76
	s_nop 0
	global_load_lds_dwordx4 v[166:167], off
	v_lshl_add_u64 v[166:167], s[46:47], 0, v[144:145]
	s_mov_b32 m0, s90
	s_nop 0
	global_load_lds_dwordx4 v[166:167], off
	v_lshl_add_u64 v[166:167], v[216:217], 0, s[68:69]
	s_mov_b32 m0, s88
	s_nop 0
	global_load_lds_dwordx4 v[166:167], off
	v_lshl_add_u64 v[166:167], v[218:219], 0, s[68:69]
	s_mov_b32 m0, s89
	s_nop 0
	global_load_lds_dwordx4 v[166:167], off
	s_waitcnt vmcnt(8)
	s_waitcnt lgkmcnt(0)
	s_barrier
	s_setprio 0
	s_waitcnt lgkmcnt(0)
	v_mfma_f32_16x16x32_bf16 v[60:63], v[112:115], v[198:201], v[60:63]
	v_mfma_f32_16x16x32_bf16 v[56:59], v[124:127], v[198:201], v[56:59]
	v_mfma_f32_16x16x32_bf16 v[44:47], v[112:115], v[206:209], v[44:47]
	v_mfma_f32_16x16x32_bf16 v[40:43], v[124:127], v[206:209], v[40:43]
	v_mfma_f32_16x16x32_bf16 v[36:39], v[112:115], v[228:231], v[36:39]
	v_mfma_f32_16x16x32_bf16 v[28:31], v[124:127], v[228:231], v[28:31]
	v_mfma_f32_16x16x32_bf16 v[20:23], v[112:115], v[236:239], v[20:23]
	v_mfma_f32_16x16x32_bf16 v[12:15], v[124:127], v[236:239], v[12:15]
	v_mfma_f32_16x16x32_bf16 v[60:63], v[116:119], v[202:205], v[60:63]
	v_mfma_f32_16x16x32_bf16 v[56:59], v[132:135], v[202:205], v[56:59]
	v_mfma_f32_16x16x32_bf16 v[44:47], v[116:119], v[224:227], v[44:47]
	v_mfma_f32_16x16x32_bf16 v[40:43], v[132:135], v[224:227], v[40:43]
	v_mfma_f32_16x16x32_bf16 v[36:39], v[116:119], v[232:235], v[36:39]
	v_mfma_f32_16x16x32_bf16 v[28:31], v[132:135], v[232:235], v[28:31]
	v_mfma_f32_16x16x32_bf16 v[20:23], v[116:119], v[240:243], v[20:23]
	v_mfma_f32_16x16x32_bf16 v[12:15], v[132:135], v[240:243], v[12:15]
	s_setprio 1
	s_setprio 0
	v_mfma_f32_16x16x32_bf16 v[52:55], v[172:175], v[198:201], v[52:55]
	v_mfma_f32_16x16x32_bf16 v[48:51], v[180:183], v[198:201], v[48:51]
	v_mfma_f32_16x16x32_bf16 v[32:35], v[172:175], v[206:209], v[32:35]
	v_mfma_f32_16x16x32_bf16 v[24:27], v[180:183], v[206:209], v[24:27]
	v_mfma_f32_16x16x32_bf16 v[16:19], v[172:175], v[228:231], v[16:19]
	v_mfma_f32_16x16x32_bf16 v[8:11], v[180:183], v[228:231], v[8:11]
	v_mfma_f32_16x16x32_bf16 v[4:7], v[172:175], v[236:239], v[4:7]
	v_mfma_f32_16x16x32_bf16 v[0:3], v[180:183], v[236:239], v[0:3]
	v_mfma_f32_16x16x32_bf16 v[52:55], v[176:179], v[202:205], v[52:55]
	v_mfma_f32_16x16x32_bf16 v[48:51], v[194:197], v[202:205], v[48:51]
	v_mfma_f32_16x16x32_bf16 v[32:35], v[176:179], v[224:227], v[32:35]
	v_mfma_f32_16x16x32_bf16 v[24:27], v[194:197], v[224:227], v[24:27]
	v_mfma_f32_16x16x32_bf16 v[16:19], v[176:179], v[232:235], v[16:19]
	v_mfma_f32_16x16x32_bf16 v[8:11], v[194:197], v[232:235], v[8:11]
	v_mfma_f32_16x16x32_bf16 v[4:7], v[176:179], v[240:243], v[4:7]
	v_mfma_f32_16x16x32_bf16 v[0:3], v[194:197], v[240:243], v[0:3]
	s_setprio 1
	s_barrier
	s_movk_i32 s50, 0x100
	s_andn2_b64 vcc, exec, s[44:45]
	s_mov_b64 s[46:47], -1
	s_mov_b64 s[44:45], 0
	s_cbranch_vccz .LBB0_1136
	s_and_b64 vcc, exec, s[8:9]
	s_cbranch_vccz .LBB0_1139
	s_barrier

.LBB0_1419:
	s_add_u32 s28, s24, 0xfff80080
	s_addc_u32 s29, s25, -1
	s_add_i32 s48, 0, 0x10000
	s_cmp_eq_u32 s17, 28
	s_cselect_b32 s31, s9, s29
	s_cselect_b32 s30, s11, s28
	s_cselect_b64 vcc, -1, 0
	s_add_i32 s28, 0, 0x14000
	v_add_u32_e32 v164, s48, v147
	v_add_u32_e32 v180, s28, v147
	ds_read_b128 v[152:155], v164
	ds_read_b128 v[156:159], v164 offset:1024
	ds_read_b128 v[160:163], v164 offset:2048
	ds_read_b128 v[164:167], v164 offset:3072
	ds_read_b128 v[168:171], v180
	ds_read_b128 v[172:175], v180 offset:1024
	ds_read_b128 v[176:179], v180 offset:2048
	ds_read_b128 v[180:183], v180 offset:3072
	v_cndmask_b32_e32 v211, v145, v150, vcc
	v_cndmask_b32_e32 v210, v144, v151, vcc
	v_lshl_add_u64 v[216:217], s[24:25], 0, v[136:137]
	s_add_i32 m0, s19, 0xc000
	ds_read_b128 v[194:197], v149
	ds_read_b128 v[198:201], v149 offset:1024
	ds_read_b128 v[202:205], v149 offset:2048
	ds_read_b128 v[206:209], v149 offset:3072
	ds_read_b128 v[224:227], v149 offset:4096
	ds_read_b128 v[228:231], v149 offset:5120
	ds_read_b128 v[232:235], v149 offset:6144
	ds_read_b128 v[236:239], v149 offset:7168
	global_load_lds_dwordx4 v[216:217], off
	v_lshl_add_u64 v[216:217], s[24:25], 0, v[138:139]
	s_add_i32 m0, s19, 0xe000
	s_nop 0
	global_load_lds_dwordx4 v[216:217], off
	s_waitcnt vmcnt(8)
	s_waitcnt lgkmcnt(0)
	s_barrier
	s_setprio 0
	s_waitcnt lgkmcnt(0)
	v_mfma_f32_16x16x32_bf16 v[124:127], v[152:155], v[194:197], v[124:127]
	v_mfma_f32_16x16x32_bf16 v[116:119], v[160:163], v[194:197], v[116:119]
	v_mfma_f32_16x16x32_bf16 v[108:111], v[152:155], v[202:205], v[108:111]
	v_mfma_f32_16x16x32_bf16 v[100:103], v[160:163], v[202:205], v[100:103]
	v_mfma_f32_16x16x32_bf16 v[92:95], v[152:155], v[224:227], v[92:95]
	v_mfma_f32_16x16x32_bf16 v[84:87], v[160:163], v[224:227], v[84:87]
	v_mfma_f32_16x16x32_bf16 v[76:79], v[152:155], v[232:235], v[76:79]
	v_mfma_f32_16x16x32_bf16 v[68:71], v[160:163], v[232:235], v[68:71]
	v_mfma_f32_16x16x32_bf16 v[124:127], v[156:159], v[198:201], v[124:127]
	v_mfma_f32_16x16x32_bf16 v[116:119], v[164:167], v[198:201], v[116:119]
	v_mfma_f32_16x16x32_bf16 v[108:111], v[156:159], v[206:209], v[108:111]
	v_mfma_f32_16x16x32_bf16 v[100:103], v[164:167], v[206:209], v[100:103]
	v_mfma_f32_16x16x32_bf16 v[92:95], v[156:159], v[228:231], v[92:95]
	v_mfma_f32_16x16x32_bf16 v[84:87], v[164:167], v[228:231], v[84:87]
	v_mfma_f32_16x16x32_bf16 v[76:79], v[156:159], v[236:239], v[76:79]
	v_mfma_f32_16x16x32_bf16 v[68:71], v[164:167], v[236:239], v[68:71]
	s_setprio 1
	s_setprio 0
	v_mfma_f32_16x16x32_bf16 v[120:123], v[168:171], v[194:197], v[120:123]
	v_mfma_f32_16x16x32_bf16 v[112:115], v[176:179], v[194:197], v[112:115]
	v_mfma_f32_16x16x32_bf16 v[104:107], v[168:171], v[202:205], v[104:107]
	v_mfma_f32_16x16x32_bf16 v[96:99], v[176:179], v[202:205], v[96:99]
	v_mfma_f32_16x16x32_bf16 v[88:91], v[168:171], v[224:227], v[88:91]
	v_mfma_f32_16x16x32_bf16 v[80:83], v[176:179], v[224:227], v[80:83]
	v_mfma_f32_16x16x32_bf16 v[72:75], v[168:171], v[232:235], v[72:75]
	v_mfma_f32_16x16x32_bf16 v[64:67], v[176:179], v[232:235], v[64:67]
	v_mfma_f32_16x16x32_bf16 v[120:123], v[172:175], v[198:201], v[120:123]
	v_mfma_f32_16x16x32_bf16 v[112:115], v[180:183], v[198:201], v[112:115]
	v_mfma_f32_16x16x32_bf16 v[104:107], v[172:175], v[206:209], v[104:107]
	v_mfma_f32_16x16x32_bf16 v[96:99], v[180:183], v[206:209], v[96:99]
	v_mfma_f32_16x16x32_bf16 v[88:91], v[172:175], v[228:231], v[88:91]
	v_mfma_f32_16x16x32_bf16 v[80:83], v[180:183], v[228:231], v[80:83]
	v_mfma_f32_16x16x32_bf16 v[72:75], v[172:175], v[236:239], v[72:75]
	v_mfma_f32_16x16x32_bf16 v[64:67], v[180:183], v[236:239], v[64:67]
	s_setprio 1
	s_barrier
	s_add_i32 s29, s48, s50
	v_lshl_add_u64 v[216:217], v[210:211], 0, v[130:131]
	s_mov_b32 m0, s29
	ds_read_b128 v[194:197], v149 offset:16384
	ds_read_b128 v[198:201], v149 offset:17408
	ds_read_b128 v[202:205], v149 offset:18432
	ds_read_b128 v[206:209], v149 offset:19456
	ds_read_b128 v[224:227], v149 offset:20480
	ds_read_b128 v[228:231], v149 offset:21504
	ds_read_b128 v[232:235], v149 offset:22528
	ds_read_b128 v[236:239], v149 offset:23552
	global_load_lds_dwordx4 v[216:217], off
	v_lshl_add_u64 v[218:219], v[210:211], 0, v[134:135]
	s_add_i32 m0, s29, 0x2000
	v_lshl_add_u64 v[220:221], v[210:211], 0, s[72:73]
	s_add_i32 s28, s28, s50
	global_load_lds_dwordx4 v[218:219], off
	v_lshl_add_u64 v[240:241], v[220:221], 0, v[130:131]
	s_mov_b32 m0, s28
	v_lshl_add_u64 v[220:221], v[220:221], 0, v[134:135]
	global_load_lds_dwordx4 v[240:241], off
	s_add_i32 m0, s28, 0x2000
	v_lshl_add_u64 v[240:241], s[30:31], 0, v[132:133]
	global_load_lds_dwordx4 v[220:221], off
	v_lshl_add_u64 v[220:221], s[30:31], 0, v[128:129]
	s_mov_b32 m0, s19
	s_nop 0
	global_load_lds_dwordx4 v[220:221], off
	s_mov_b32 m0, s51
	s_nop 0
	global_load_lds_dwordx4 v[240:241], off
	s_waitcnt vmcnt(8)
	s_waitcnt lgkmcnt(0)
	s_barrier
	s_setprio 0
	s_waitcnt lgkmcnt(0)
	v_mfma_f32_16x16x32_bf16 v[60:63], v[152:155], v[194:197], v[60:63]
	v_mfma_f32_16x16x32_bf16 v[52:55], v[160:163], v[194:197], v[52:55]
	v_mfma_f32_16x16x32_bf16 v[44:47], v[152:155], v[202:205], v[44:47]
	v_mfma_f32_16x16x32_bf16 v[36:39], v[160:163], v[202:205], v[36:39]
	v_mfma_f32_16x16x32_bf16 v[28:31], v[152:155], v[224:227], v[28:31]
	v_mfma_f32_16x16x32_bf16 v[20:23], v[160:163], v[224:227], v[20:23]
	v_mfma_f32_16x16x32_bf16 v[12:15], v[152:155], v[232:235], v[12:15]
	v_mfma_f32_16x16x32_bf16 v[4:7], v[160:163], v[232:235], v[4:7]
	v_mfma_f32_16x16x32_bf16 v[60:63], v[156:159], v[198:201], v[60:63]
	v_mfma_f32_16x16x32_bf16 v[52:55], v[164:167], v[198:201], v[52:55]
	v_mfma_f32_16x16x32_bf16 v[44:47], v[156:159], v[206:209], v[44:47]
	v_mfma_f32_16x16x32_bf16 v[36:39], v[164:167], v[206:209], v[36:39]
	v_mfma_f32_16x16x32_bf16 v[28:31], v[156:159], v[228:231], v[28:31]
	v_mfma_f32_16x16x32_bf16 v[20:23], v[164:167], v[228:231], v[20:23]
	v_mfma_f32_16x16x32_bf16 v[12:15], v[156:159], v[236:239], v[12:15]
	v_mfma_f32_16x16x32_bf16 v[4:7], v[164:167], v[236:239], v[4:7]
	s_setprio 1
	s_setprio 0
	v_mfma_f32_16x16x32_bf16 v[56:59], v[168:171], v[194:197], v[56:59]
	v_mfma_f32_16x16x32_bf16 v[48:51], v[176:179], v[194:197], v[48:51]
	v_mfma_f32_16x16x32_bf16 v[40:43], v[168:171], v[202:205], v[40:43]
	v_mfma_f32_16x16x32_bf16 v[32:35], v[176:179], v[202:205], v[32:35]
	v_mfma_f32_16x16x32_bf16 v[24:27], v[168:171], v[224:227], v[24:27]
	v_mfma_f32_16x16x32_bf16 v[16:19], v[176:179], v[224:227], v[16:19]
	v_mfma_f32_16x16x32_bf16 v[8:11], v[168:171], v[232:235], v[8:11]
	v_mfma_f32_16x16x32_bf16 v[0:3], v[176:179], v[232:235], v[0:3]
	v_mfma_f32_16x16x32_bf16 v[56:59], v[172:175], v[198:201], v[56:59]
	v_mfma_f32_16x16x32_bf16 v[48:51], v[180:183], v[198:201], v[48:51]
	v_mfma_f32_16x16x32_bf16 v[40:43], v[172:175], v[206:209], v[40:43]
	v_mfma_f32_16x16x32_bf16 v[32:35], v[180:183], v[206:209], v[32:35]
	v_mfma_f32_16x16x32_bf16 v[24:27], v[172:175], v[228:231], v[24:27]
	v_mfma_f32_16x16x32_bf16 v[16:19], v[180:183], v[228:231], v[16:19]
	v_mfma_f32_16x16x32_bf16 v[8:11], v[172:175], v[236:239], v[8:11]
	v_mfma_f32_16x16x32_bf16 v[0:3], v[180:183], v[236:239], v[0:3]
	s_setprio 1
	s_barrier
	s_add_i32 s48, 0, 0x18000
	s_add_i32 s49, 0, 0x1c000
	v_add_u32_e32 v164, s48, v147
	v_add_u32_e32 v180, s49, v147
	ds_read_b128 v[152:155], v164
	ds_read_b128 v[156:159], v164 offset:1024
	ds_read_b128 v[160:163], v164 offset:2048
	ds_read_b128 v[164:167], v164 offset:3072
	ds_read_b128 v[168:171], v180
	ds_read_b128 v[172:175], v180 offset:1024
	ds_read_b128 v[176:179], v180 offset:2048
	ds_read_b128 v[180:183], v180 offset:3072
	s_add_u32 s28, s30, 0x80000
	s_addc_u32 s29, s31, 0
	s_mov_b32 m0, s52
	v_lshl_add_u64 v[242:243], s[28:29], 0, v[128:129]
	ds_read_b128 v[194:197], v149 offset:32768
	ds_read_b128 v[198:201], v149 offset:33792
	ds_read_b128 v[202:205], v149 offset:34816
	ds_read_b128 v[206:209], v149 offset:35840
	ds_read_b128 v[224:227], v149 offset:36864
	ds_read_b128 v[228:231], v149 offset:37888
	ds_read_b128 v[232:235], v149 offset:38912
	ds_read_b128 v[236:239], v149 offset:39936
	global_load_lds_dwordx4 v[242:243], off
	v_lshl_add_u64 v[242:243], s[28:29], 0, v[132:133]
	s_mov_b32 m0, s53
	s_nop 0
	global_load_lds_dwordx4 v[242:243], off
	s_waitcnt vmcnt(8)
	s_waitcnt lgkmcnt(0)
	s_barrier
	s_setprio 0
	s_waitcnt lgkmcnt(0)
	v_mfma_f32_16x16x32_bf16 v[124:127], v[152:155], v[194:197], v[124:127]
	v_mfma_f32_16x16x32_bf16 v[116:119], v[160:163], v[194:197], v[116:119]
	v_mfma_f32_16x16x32_bf16 v[108:111], v[152:155], v[202:205], v[108:111]
	v_mfma_f32_16x16x32_bf16 v[100:103], v[160:163], v[202:205], v[100:103]
	v_mfma_f32_16x16x32_bf16 v[92:95], v[152:155], v[224:227], v[92:95]
	v_mfma_f32_16x16x32_bf16 v[84:87], v[160:163], v[224:227], v[84:87]
	v_mfma_f32_16x16x32_bf16 v[76:79], v[152:155], v[232:235], v[76:79]
	v_mfma_f32_16x16x32_bf16 v[68:71], v[160:163], v[232:235], v[68:71]
	v_mfma_f32_16x16x32_bf16 v[124:127], v[156:159], v[198:201], v[124:127]
	v_mfma_f32_16x16x32_bf16 v[116:119], v[164:167], v[198:201], v[116:119]
	v_mfma_f32_16x16x32_bf16 v[108:111], v[156:159], v[206:209], v[108:111]
	v_mfma_f32_16x16x32_bf16 v[100:103], v[164:167], v[206:209], v[100:103]
	v_mfma_f32_16x16x32_bf16 v[92:95], v[156:159], v[228:231], v[92:95]
	v_mfma_f32_16x16x32_bf16 v[84:87], v[164:167], v[228:231], v[84:87]
	v_mfma_f32_16x16x32_bf16 v[76:79], v[156:159], v[236:239], v[76:79]
	v_mfma_f32_16x16x32_bf16 v[68:71], v[164:167], v[236:239], v[68:71]
	s_setprio 1
	s_setprio 0
	v_mfma_f32_16x16x32_bf16 v[120:123], v[168:171], v[194:197], v[120:123]
	v_mfma_f32_16x16x32_bf16 v[112:115], v[176:179], v[194:197], v[112:115]
	v_mfma_f32_16x16x32_bf16 v[104:107], v[168:171], v[202:205], v[104:107]
	v_mfma_f32_16x16x32_bf16 v[96:99], v[176:179], v[202:205], v[96:99]
	v_mfma_f32_16x16x32_bf16 v[88:91], v[168:171], v[224:227], v[88:91]
	v_mfma_f32_16x16x32_bf16 v[80:83], v[176:179], v[224:227], v[80:83]
	v_mfma_f32_16x16x32_bf16 v[72:75], v[168:171], v[232:235], v[72:75]
	v_mfma_f32_16x16x32_bf16 v[64:67], v[176:179], v[232:235], v[64:67]
	v_mfma_f32_16x16x32_bf16 v[120:123], v[172:175], v[198:201], v[120:123]
	v_mfma_f32_16x16x32_bf16 v[112:115], v[180:183], v[198:201], v[112:115]
	v_mfma_f32_16x16x32_bf16 v[104:107], v[172:175], v[206:209], v[104:107]
	v_mfma_f32_16x16x32_bf16 v[96:99], v[180:183], v[206:209], v[96:99]
	v_mfma_f32_16x16x32_bf16 v[88:91], v[172:175], v[228:231], v[88:91]
	v_mfma_f32_16x16x32_bf16 v[80:83], v[180:183], v[228:231], v[80:83]
	v_mfma_f32_16x16x32_bf16 v[72:75], v[172:175], v[236:239], v[72:75]
	v_mfma_f32_16x16x32_bf16 v[64:67], v[180:183], v[236:239], v[64:67]
	s_setprio 1
	s_barrier
	s_add_i32 s28, s48, s50
	v_lshl_add_u64 v[216:217], v[216:217], 0, s[68:69]
	s_mov_b32 m0, s28
	ds_read_b128 v[194:197], v149 offset:49152
	ds_read_b128 v[198:201], v149 offset:50176
	ds_read_b128 v[202:205], v149 offset:51200
	ds_read_b128 v[206:209], v149 offset:52224
	ds_read_b128 v[224:227], v149 offset:53248
	ds_read_b128 v[228:231], v149 offset:54272
	ds_read_b128 v[232:235], v149 offset:55296
	ds_read_b128 v[236:239], v149 offset:56320
	global_load_lds_dwordx4 v[216:217], off
	v_lshl_add_u64 v[216:217], v[218:219], 0, s[68:69]
	s_add_i32 m0, s28, 0x2000
	v_lshl_add_u64 v[210:211], v[210:211], 0, s[74:75]
	s_add_i32 s28, s49, s50
	global_load_lds_dwordx4 v[216:217], off
	v_lshl_add_u64 v[216:217], v[210:211], 0, v[130:131]
	s_mov_b32 m0, s28
	v_lshl_add_u64 v[210:211], v[210:211], 0, v[134:135]
	global_load_lds_dwordx4 v[216:217], off
	s_add_i32 m0, s28, 0x2000
	s_nop 0
	global_load_lds_dwordx4 v[210:211], off
	v_lshl_add_u64 v[210:211], v[220:221], 0, s[68:69]
	s_mov_b32 m0, s58
	s_nop 0
	global_load_lds_dwordx4 v[210:211], off
	v_lshl_add_u64 v[210:211], v[240:241], 0, s[68:69]
	s_mov_b32 m0, s59
	s_nop 0
	global_load_lds_dwordx4 v[210:211], off
	s_waitcnt vmcnt(8)
	s_waitcnt lgkmcnt(0)
	s_barrier
	s_setprio 0
	s_waitcnt lgkmcnt(0)
	v_mfma_f32_16x16x32_bf16 v[60:63], v[152:155], v[194:197], v[60:63]
	v_mfma_f32_16x16x32_bf16 v[52:55], v[160:163], v[194:197], v[52:55]
	v_mfma_f32_16x16x32_bf16 v[44:47], v[152:155], v[202:205], v[44:47]
	v_mfma_f32_16x16x32_bf16 v[36:39], v[160:163], v[202:205], v[36:39]
	v_mfma_f32_16x16x32_bf16 v[28:31], v[152:155], v[224:227], v[28:31]
	v_mfma_f32_16x16x32_bf16 v[20:23], v[160:163], v[224:227], v[20:23]
	v_mfma_f32_16x16x32_bf16 v[12:15], v[152:155], v[232:235], v[12:15]
	v_mfma_f32_16x16x32_bf16 v[4:7], v[160:163], v[232:235], v[4:7]
	v_mfma_f32_16x16x32_bf16 v[60:63], v[156:159], v[198:201], v[60:63]
	v_mfma_f32_16x16x32_bf16 v[52:55], v[164:167], v[198:201], v[52:55]
	v_mfma_f32_16x16x32_bf16 v[44:47], v[156:159], v[206:209], v[44:47]
	v_mfma_f32_16x16x32_bf16 v[36:39], v[164:167], v[206:209], v[36:39]
	v_mfma_f32_16x16x32_bf16 v[28:31], v[156:159], v[228:231], v[28:31]
	v_mfma_f32_16x16x32_bf16 v[20:23], v[164:167], v[228:231], v[20:23]
	v_mfma_f32_16x16x32_bf16 v[12:15], v[156:159], v[236:239], v[12:15]
	v_mfma_f32_16x16x32_bf16 v[4:7], v[164:167], v[236:239], v[4:7]
	s_setprio 1
	s_setprio 0
	v_mfma_f32_16x16x32_bf16 v[56:59], v[168:171], v[194:197], v[56:59]
	v_mfma_f32_16x16x32_bf16 v[48:51], v[176:179], v[194:197], v[48:51]
	v_mfma_f32_16x16x32_bf16 v[40:43], v[168:171], v[202:205], v[40:43]
	v_mfma_f32_16x16x32_bf16 v[32:35], v[176:179], v[202:205], v[32:35]
	v_mfma_f32_16x16x32_bf16 v[24:27], v[168:171], v[224:227], v[24:27]
	v_mfma_f32_16x16x32_bf16 v[16:19], v[176:179], v[224:227], v[16:19]
	v_mfma_f32_16x16x32_bf16 v[8:11], v[168:171], v[232:235], v[8:11]
	v_mfma_f32_16x16x32_bf16 v[0:3], v[176:179], v[232:235], v[0:3]
	v_mfma_f32_16x16x32_bf16 v[56:59], v[172:175], v[198:201], v[56:59]
	v_mfma_f32_16x16x32_bf16 v[48:51], v[180:183], v[198:201], v[48:51]
	v_mfma_f32_16x16x32_bf16 v[40:43], v[172:175], v[206:209], v[40:43]
	v_mfma_f32_16x16x32_bf16 v[32:35], v[180:183], v[206:209], v[32:35]
	v_mfma_f32_16x16x32_bf16 v[24:27], v[172:175], v[228:231], v[24:27]
	v_mfma_f32_16x16x32_bf16 v[16:19], v[180:183], v[228:231], v[16:19]
	v_mfma_f32_16x16x32_bf16 v[8:11], v[172:175], v[236:239], v[8:11]
	v_mfma_f32_16x16x32_bf16 v[0:3], v[180:183], v[236:239], v[0:3]
	s_setprio 1
	s_barrier
	s_add_i32 s17, s17, 2
	s_add_u32 s24, s24, 0x100
	s_addc_u32 s25, s25, 0
	s_cmp_gt_u32 s17, 29
	v_lshl_add_u64 v[144:145], v[144:145], 0, s[76:77]
	s_cbranch_scc0 .LBB0_1419
	s_and_b64 vcc, exec, s[6:7]
	s_cbranch_vccz .LBB0_1422
	s_barrier

.LBB0_1491:
	s_add_u32 s14, s12, 0x100
	s_addc_u32 s15, s13, 0
	s_add_i32 s28, 0, 0x10000
	s_cmp_eq_u32 s59, 40
	s_cselect_b32 s17, s53, s15
	s_cselect_b32 s16, s58, s14
	s_cselect_b64 vcc, -1, 0
	s_add_i32 s29, 0, 0x14000
	v_add_u32_e32 v164, s28, v147
	v_add_u32_e32 v180, s29, v147
	ds_read_b128 v[152:155], v164
	ds_read_b128 v[156:159], v164 offset:1024
	ds_read_b128 v[160:163], v164 offset:2048
	ds_read_b128 v[164:167], v164 offset:3072
	ds_read_b128 v[168:171], v180
	ds_read_b128 v[172:175], v180 offset:1024
	ds_read_b128 v[176:179], v180 offset:2048
	ds_read_b128 v[180:183], v180 offset:3072
	v_cndmask_b32_e32 v211, v145, v150, vcc
	v_cndmask_b32_e32 v210, v144, v151, vcc
	v_lshl_add_u64 v[216:217], s[12:13], 0, v[136:137]
	s_add_i32 m0, s40, 0xc000
	ds_read_b128 v[194:197], v149
	ds_read_b128 v[198:201], v149 offset:1024
	ds_read_b128 v[202:205], v149 offset:2048
	ds_read_b128 v[206:209], v149 offset:3072
	ds_read_b128 v[224:227], v149 offset:4096
	ds_read_b128 v[228:231], v149 offset:5120
	ds_read_b128 v[232:235], v149 offset:6144
	ds_read_b128 v[236:239], v149 offset:7168
	global_load_lds_dwordx4 v[216:217], off
	v_lshl_add_u64 v[216:217], s[12:13], 0, v[138:139]
	s_add_i32 m0, s40, 0xe000
	s_nop 0
	global_load_lds_dwordx4 v[216:217], off
	s_waitcnt vmcnt(8)
	s_waitcnt lgkmcnt(0)
	s_barrier
	s_setprio 0
	s_waitcnt lgkmcnt(0)
	v_mfma_f32_16x16x32_bf16 v[124:127], v[152:155], v[194:197], v[124:127]
	v_mfma_f32_16x16x32_bf16 v[120:123], v[160:163], v[194:197], v[120:123]
	v_mfma_f32_16x16x32_bf16 v[116:119], v[152:155], v[202:205], v[116:119]
	v_mfma_f32_16x16x32_bf16 v[108:111], v[160:163], v[202:205], v[108:111]
	v_mfma_f32_16x16x32_bf16 v[100:103], v[152:155], v[224:227], v[100:103]
	v_mfma_f32_16x16x32_bf16 v[92:95], v[160:163], v[224:227], v[92:95]
	v_mfma_f32_16x16x32_bf16 v[80:83], v[152:155], v[232:235], v[80:83]
	v_mfma_f32_16x16x32_bf16 v[72:75], v[160:163], v[232:235], v[72:75]
	v_mfma_f32_16x16x32_bf16 v[124:127], v[156:159], v[198:201], v[124:127]
	v_mfma_f32_16x16x32_bf16 v[120:123], v[164:167], v[198:201], v[120:123]
	v_mfma_f32_16x16x32_bf16 v[116:119], v[156:159], v[206:209], v[116:119]
	v_mfma_f32_16x16x32_bf16 v[108:111], v[164:167], v[206:209], v[108:111]
	v_mfma_f32_16x16x32_bf16 v[100:103], v[156:159], v[228:231], v[100:103]
	v_mfma_f32_16x16x32_bf16 v[92:95], v[164:167], v[228:231], v[92:95]
	v_mfma_f32_16x16x32_bf16 v[80:83], v[156:159], v[236:239], v[80:83]
	v_mfma_f32_16x16x32_bf16 v[72:75], v[164:167], v[236:239], v[72:75]
	s_setprio 1
	s_setprio 0
	v_mfma_f32_16x16x32_bf16 v[112:115], v[168:171], v[194:197], v[112:115]
	v_mfma_f32_16x16x32_bf16 v[104:107], v[176:179], v[194:197], v[104:107]
	v_mfma_f32_16x16x32_bf16 v[96:99], v[168:171], v[202:205], v[96:99]
	v_mfma_f32_16x16x32_bf16 v[88:91], v[176:179], v[202:205], v[88:91]
	v_mfma_f32_16x16x32_bf16 v[84:87], v[168:171], v[224:227], v[84:87]
	v_mfma_f32_16x16x32_bf16 v[76:79], v[176:179], v[224:227], v[76:79]
	v_mfma_f32_16x16x32_bf16 v[68:71], v[168:171], v[232:235], v[68:71]
	v_mfma_f32_16x16x32_bf16 v[64:67], v[176:179], v[232:235], v[64:67]
	v_mfma_f32_16x16x32_bf16 v[112:115], v[172:175], v[198:201], v[112:115]
	v_mfma_f32_16x16x32_bf16 v[104:107], v[180:183], v[198:201], v[104:107]
	v_mfma_f32_16x16x32_bf16 v[96:99], v[172:175], v[206:209], v[96:99]
	v_mfma_f32_16x16x32_bf16 v[88:91], v[180:183], v[206:209], v[88:91]
	v_mfma_f32_16x16x32_bf16 v[84:87], v[172:175], v[228:231], v[84:87]
	v_mfma_f32_16x16x32_bf16 v[76:79], v[180:183], v[228:231], v[76:79]
	v_mfma_f32_16x16x32_bf16 v[68:71], v[172:175], v[236:239], v[68:71]
	v_mfma_f32_16x16x32_bf16 v[64:67], v[180:183], v[236:239], v[64:67]
	s_setprio 1
	s_barrier
	s_add_i32 s12, s28, s30
	v_lshl_add_u64 v[216:217], v[210:211], 0, v[132:133]
	s_mov_b32 m0, s12
	ds_read_b128 v[194:197], v149 offset:16384
	ds_read_b128 v[198:201], v149 offset:17408
	ds_read_b128 v[202:205], v149 offset:18432
	ds_read_b128 v[206:209], v149 offset:19456
	ds_read_b128 v[224:227], v149 offset:20480
	ds_read_b128 v[228:231], v149 offset:21504
	ds_read_b128 v[232:235], v149 offset:22528
	ds_read_b128 v[236:239], v149 offset:23552
	global_load_lds_dwordx4 v[216:217], off
	v_lshl_add_u64 v[218:219], v[210:211], 0, v[128:129]
	s_add_i32 m0, s12, 0x2000
	v_lshl_add_u64 v[220:221], v[210:211], 0, s[72:73]
	s_add_i32 s12, s29, s30
	global_load_lds_dwordx4 v[218:219], off
	v_lshl_add_u64 v[240:241], v[220:221], 0, v[132:133]
	s_mov_b32 m0, s12
	v_lshl_add_u64 v[220:221], v[220:221], 0, v[128:129]
	global_load_lds_dwordx4 v[240:241], off
	s_add_i32 m0, s12, 0x2000
	v_lshl_add_u64 v[240:241], s[16:17], 0, v[130:131]
	global_load_lds_dwordx4 v[220:221], off
	v_lshl_add_u64 v[220:221], s[16:17], 0, v[134:135]
	s_mov_b32 m0, s40
	s_nop 0
	global_load_lds_dwordx4 v[220:221], off
	s_mov_b32 m0, s41
	s_nop 0
	global_load_lds_dwordx4 v[240:241], off
	s_waitcnt vmcnt(8)
	s_waitcnt lgkmcnt(0)
	s_barrier
	s_setprio 0
	s_waitcnt lgkmcnt(0)
	v_mfma_f32_16x16x32_bf16 v[60:63], v[152:155], v[194:197], v[60:63]
	v_mfma_f32_16x16x32_bf16 v[56:59], v[160:163], v[194:197], v[56:59]
	v_mfma_f32_16x16x32_bf16 v[52:55], v[152:155], v[202:205], v[52:55]
	v_mfma_f32_16x16x32_bf16 v[44:47], v[160:163], v[202:205], v[44:47]
	v_mfma_f32_16x16x32_bf16 v[36:39], v[152:155], v[224:227], v[36:39]
	v_mfma_f32_16x16x32_bf16 v[28:31], v[160:163], v[224:227], v[28:31]
	v_mfma_f32_16x16x32_bf16 v[20:23], v[152:155], v[232:235], v[20:23]
	v_mfma_f32_16x16x32_bf16 v[12:15], v[160:163], v[232:235], v[12:15]
	v_mfma_f32_16x16x32_bf16 v[60:63], v[156:159], v[198:201], v[60:63]
	v_mfma_f32_16x16x32_bf16 v[56:59], v[164:167], v[198:201], v[56:59]
	v_mfma_f32_16x16x32_bf16 v[52:55], v[156:159], v[206:209], v[52:55]
	v_mfma_f32_16x16x32_bf16 v[44:47], v[164:167], v[206:209], v[44:47]
	v_mfma_f32_16x16x32_bf16 v[36:39], v[156:159], v[228:231], v[36:39]
	v_mfma_f32_16x16x32_bf16 v[28:31], v[164:167], v[228:231], v[28:31]
	v_mfma_f32_16x16x32_bf16 v[20:23], v[156:159], v[236:239], v[20:23]
	v_mfma_f32_16x16x32_bf16 v[12:15], v[164:167], v[236:239], v[12:15]
	s_setprio 1
	s_setprio 0
	v_mfma_f32_16x16x32_bf16 v[48:51], v[168:171], v[194:197], v[48:51]
	v_mfma_f32_16x16x32_bf16 v[40:43], v[176:179], v[194:197], v[40:43]
	v_mfma_f32_16x16x32_bf16 v[32:35], v[168:171], v[202:205], v[32:35]
	v_mfma_f32_16x16x32_bf16 v[24:27], v[176:179], v[202:205], v[24:27]
	v_mfma_f32_16x16x32_bf16 v[16:19], v[168:171], v[224:227], v[16:19]
	v_mfma_f32_16x16x32_bf16 v[8:11], v[176:179], v[224:227], v[8:11]
	v_mfma_f32_16x16x32_bf16 v[4:7], v[168:171], v[232:235], v[4:7]
	v_mfma_f32_16x16x32_bf16 v[0:3], v[176:179], v[232:235], v[0:3]
	v_mfma_f32_16x16x32_bf16 v[48:51], v[172:175], v[198:201], v[48:51]
	v_mfma_f32_16x16x32_bf16 v[40:43], v[180:183], v[198:201], v[40:43]
	v_mfma_f32_16x16x32_bf16 v[32:35], v[172:175], v[206:209], v[32:35]
	v_mfma_f32_16x16x32_bf16 v[24:27], v[180:183], v[206:209], v[24:27]
	v_mfma_f32_16x16x32_bf16 v[16:19], v[172:175], v[228:231], v[16:19]
	v_mfma_f32_16x16x32_bf16 v[8:11], v[180:183], v[228:231], v[8:11]
	v_mfma_f32_16x16x32_bf16 v[4:7], v[172:175], v[236:239], v[4:7]
	v_mfma_f32_16x16x32_bf16 v[0:3], v[180:183], v[236:239], v[0:3]
	s_setprio 1
	s_barrier
	s_add_i32 s28, 0, 0x18000
	s_add_i32 s29, 0, 0x1c000
	v_add_u32_e32 v164, s28, v147
	v_add_u32_e32 v180, s29, v147
	ds_read_b128 v[152:155], v164
	ds_read_b128 v[156:159], v164 offset:1024
	ds_read_b128 v[160:163], v164 offset:2048
	ds_read_b128 v[164:167], v164 offset:3072
	ds_read_b128 v[168:171], v180
	ds_read_b128 v[172:175], v180 offset:1024
	ds_read_b128 v[176:179], v180 offset:2048
	ds_read_b128 v[180:183], v180 offset:3072
	s_add_u32 s12, s16, 0xb0000
	s_addc_u32 s13, s17, 0
	s_mov_b32 m0, s42
	v_lshl_add_u64 v[242:243], s[12:13], 0, v[134:135]
	ds_read_b128 v[194:197], v149 offset:32768
	ds_read_b128 v[198:201], v149 offset:33792
	ds_read_b128 v[202:205], v149 offset:34816
	ds_read_b128 v[206:209], v149 offset:35840
	ds_read_b128 v[224:227], v149 offset:36864
	ds_read_b128 v[228:231], v149 offset:37888
	ds_read_b128 v[232:235], v149 offset:38912
	ds_read_b128 v[236:239], v149 offset:39936
	global_load_lds_dwordx4 v[242:243], off
	v_lshl_add_u64 v[242:243], s[12:13], 0, v[130:131]
	s_mov_b32 m0, s43
	s_nop 0
	global_load_lds_dwordx4 v[242:243], off
	s_waitcnt vmcnt(8)
	s_waitcnt lgkmcnt(0)
	s_barrier
	s_setprio 0
	s_waitcnt lgkmcnt(0)
	v_mfma_f32_16x16x32_bf16 v[124:127], v[152:155], v[194:197], v[124:127]
	v_mfma_f32_16x16x32_bf16 v[120:123], v[160:163], v[194:197], v[120:123]
	v_mfma_f32_16x16x32_bf16 v[116:119], v[152:155], v[202:205], v[116:119]
	v_mfma_f32_16x16x32_bf16 v[108:111], v[160:163], v[202:205], v[108:111]
	v_mfma_f32_16x16x32_bf16 v[100:103], v[152:155], v[224:227], v[100:103]
	v_mfma_f32_16x16x32_bf16 v[92:95], v[160:163], v[224:227], v[92:95]
	v_mfma_f32_16x16x32_bf16 v[80:83], v[152:155], v[232:235], v[80:83]
	v_mfma_f32_16x16x32_bf16 v[72:75], v[160:163], v[232:235], v[72:75]
	v_mfma_f32_16x16x32_bf16 v[124:127], v[156:159], v[198:201], v[124:127]
	v_mfma_f32_16x16x32_bf16 v[120:123], v[164:167], v[198:201], v[120:123]
	v_mfma_f32_16x16x32_bf16 v[116:119], v[156:159], v[206:209], v[116:119]
	v_mfma_f32_16x16x32_bf16 v[108:111], v[164:167], v[206:209], v[108:111]
	v_mfma_f32_16x16x32_bf16 v[100:103], v[156:159], v[228:231], v[100:103]
	v_mfma_f32_16x16x32_bf16 v[92:95], v[164:167], v[228:231], v[92:95]
	v_mfma_f32_16x16x32_bf16 v[80:83], v[156:159], v[236:239], v[80:83]
	v_mfma_f32_16x16x32_bf16 v[72:75], v[164:167], v[236:239], v[72:75]
	s_setprio 1
	s_setprio 0
	v_mfma_f32_16x16x32_bf16 v[112:115], v[168:171], v[194:197], v[112:115]
	v_mfma_f32_16x16x32_bf16 v[104:107], v[176:179], v[194:197], v[104:107]
	v_mfma_f32_16x16x32_bf16 v[96:99], v[168:171], v[202:205], v[96:99]
	v_mfma_f32_16x16x32_bf16 v[88:91], v[176:179], v[202:205], v[88:91]
	v_mfma_f32_16x16x32_bf16 v[84:87], v[168:171], v[224:227], v[84:87]
	v_mfma_f32_16x16x32_bf16 v[76:79], v[176:179], v[224:227], v[76:79]
	v_mfma_f32_16x16x32_bf16 v[68:71], v[168:171], v[232:235], v[68:71]
	v_mfma_f32_16x16x32_bf16 v[64:67], v[176:179], v[232:235], v[64:67]
	v_mfma_f32_16x16x32_bf16 v[112:115], v[172:175], v[198:201], v[112:115]
	v_mfma_f32_16x16x32_bf16 v[104:107], v[180:183], v[198:201], v[104:107]
	v_mfma_f32_16x16x32_bf16 v[96:99], v[172:175], v[206:209], v[96:99]
	v_mfma_f32_16x16x32_bf16 v[88:91], v[180:183], v[206:209], v[88:91]
	v_mfma_f32_16x16x32_bf16 v[84:87], v[172:175], v[228:231], v[84:87]
	v_mfma_f32_16x16x32_bf16 v[76:79], v[180:183], v[228:231], v[76:79]
	v_mfma_f32_16x16x32_bf16 v[68:71], v[172:175], v[236:239], v[68:71]
	v_mfma_f32_16x16x32_bf16 v[64:67], v[180:183], v[236:239], v[64:67]
	s_setprio 1
	s_barrier
	s_add_i32 s12, s28, s30
	v_lshl_add_u64 v[216:217], v[216:217], 0, s[68:69]
	s_mov_b32 m0, s12
	ds_read_b128 v[194:197], v149 offset:49152
	ds_read_b128 v[198:201], v149 offset:50176
	ds_read_b128 v[202:205], v149 offset:51200
	ds_read_b128 v[206:209], v149 offset:52224
	ds_read_b128 v[224:227], v149 offset:53248
	ds_read_b128 v[228:231], v149 offset:54272
	ds_read_b128 v[232:235], v149 offset:55296
	ds_read_b128 v[236:239], v149 offset:56320
	global_load_lds_dwordx4 v[216:217], off
	v_lshl_add_u64 v[216:217], v[218:219], 0, s[68:69]
	s_add_i32 m0, s12, 0x2000
	v_lshl_add_u64 v[210:211], v[210:211], 0, s[74:75]
	s_add_i32 s12, s29, s30
	global_load_lds_dwordx4 v[216:217], off
	v_lshl_add_u64 v[216:217], v[210:211], 0, v[132:133]
	s_mov_b32 m0, s12
	v_lshl_add_u64 v[210:211], v[210:211], 0, v[128:129]
	global_load_lds_dwordx4 v[216:217], off
	s_add_i32 m0, s12, 0x2000
	s_nop 0
	global_load_lds_dwordx4 v[210:211], off
	v_lshl_add_u64 v[210:211], v[220:221], 0, s[68:69]
	s_mov_b32 m0, s44
	s_nop 0
	global_load_lds_dwordx4 v[210:211], off
	v_lshl_add_u64 v[210:211], v[240:241], 0, s[68:69]
	s_mov_b32 m0, s45
	s_nop 0
	global_load_lds_dwordx4 v[210:211], off
	s_waitcnt vmcnt(8)
	s_waitcnt lgkmcnt(0)
	s_barrier
	s_setprio 0
	s_waitcnt lgkmcnt(0)
	v_mfma_f32_16x16x32_bf16 v[60:63], v[152:155], v[194:197], v[60:63]
	v_mfma_f32_16x16x32_bf16 v[56:59], v[160:163], v[194:197], v[56:59]
	v_mfma_f32_16x16x32_bf16 v[52:55], v[152:155], v[202:205], v[52:55]
	v_mfma_f32_16x16x32_bf16 v[44:47], v[160:163], v[202:205], v[44:47]
	v_mfma_f32_16x16x32_bf16 v[36:39], v[152:155], v[224:227], v[36:39]
	v_mfma_f32_16x16x32_bf16 v[28:31], v[160:163], v[224:227], v[28:31]
	v_mfma_f32_16x16x32_bf16 v[20:23], v[152:155], v[232:235], v[20:23]
	v_mfma_f32_16x16x32_bf16 v[12:15], v[160:163], v[232:235], v[12:15]
	v_mfma_f32_16x16x32_bf16 v[60:63], v[156:159], v[198:201], v[60:63]
	v_mfma_f32_16x16x32_bf16 v[56:59], v[164:167], v[198:201], v[56:59]
	v_mfma_f32_16x16x32_bf16 v[52:55], v[156:159], v[206:209], v[52:55]
	v_mfma_f32_16x16x32_bf16 v[44:47], v[164:167], v[206:209], v[44:47]
	v_mfma_f32_16x16x32_bf16 v[36:39], v[156:159], v[228:231], v[36:39]
	v_mfma_f32_16x16x32_bf16 v[28:31], v[164:167], v[228:231], v[28:31]
	v_mfma_f32_16x16x32_bf16 v[20:23], v[156:159], v[236:239], v[20:23]
	v_mfma_f32_16x16x32_bf16 v[12:15], v[164:167], v[236:239], v[12:15]
	s_setprio 1
	s_setprio 0
	v_mfma_f32_16x16x32_bf16 v[48:51], v[168:171], v[194:197], v[48:51]
	v_mfma_f32_16x16x32_bf16 v[40:43], v[176:179], v[194:197], v[40:43]
	v_mfma_f32_16x16x32_bf16 v[32:35], v[168:171], v[202:205], v[32:35]
	v_mfma_f32_16x16x32_bf16 v[24:27], v[176:179], v[202:205], v[24:27]
	v_mfma_f32_16x16x32_bf16 v[16:19], v[168:171], v[224:227], v[16:19]
	v_mfma_f32_16x16x32_bf16 v[8:11], v[176:179], v[224:227], v[8:11]
	v_mfma_f32_16x16x32_bf16 v[4:7], v[168:171], v[232:235], v[4:7]
	v_mfma_f32_16x16x32_bf16 v[0:3], v[176:179], v[232:235], v[0:3]
	v_mfma_f32_16x16x32_bf16 v[48:51], v[172:175], v[198:201], v[48:51]
	v_mfma_f32_16x16x32_bf16 v[40:43], v[180:183], v[198:201], v[40:43]
	v_mfma_f32_16x16x32_bf16 v[32:35], v[172:175], v[206:209], v[32:35]
	v_mfma_f32_16x16x32_bf16 v[24:27], v[180:183], v[206:209], v[24:27]
	v_mfma_f32_16x16x32_bf16 v[16:19], v[172:175], v[228:231], v[16:19]
	v_mfma_f32_16x16x32_bf16 v[8:11], v[180:183], v[228:231], v[8:11]
	v_mfma_f32_16x16x32_bf16 v[4:7], v[172:175], v[236:239], v[4:7]
	v_mfma_f32_16x16x32_bf16 v[0:3], v[180:183], v[236:239], v[0:3]
	s_setprio 1
	s_barrier
	s_add_i32 s59, s59, 2
	v_lshl_add_u64 v[144:145], v[144:145], 0, s[60:61]
	s_cmp_gt_u32 s59, 41
	s_mov_b64 s[12:13], s[14:15]
	s_cbranch_scc0 .LBB0_1491
	s_mov_b64 s[14:15], 0xb0000
	s_and_b64 vcc, exec, s[6:7]
	s_cbranch_vccz .LBB0_1494
	s_barrier

.LBB0_1587:
	s_add_u32 s28, s24, 0xfff80080
	s_addc_u32 s29, s25, -1
	s_add_i32 s48, 0, 0x10000
	s_cmp_eq_u32 s51, 28
	s_cselect_b32 s39, s9, s29
	s_cselect_b32 s38, s11, s28
	s_cselect_b32 s31, s45, s50
	s_cselect_b32 s30, s46, s47
	s_add_i32 s49, 0, 0x14000
	v_add_u32_e32 v154, s48, v139
	v_add_u32_e32 v170, s49, v139
	ds_read_b128 v[142:145], v154
	ds_read_b128 v[146:149], v154 offset:1024
	ds_read_b128 v[150:153], v154 offset:2048
	ds_read_b128 v[154:157], v154 offset:3072
	ds_read_b128 v[158:161], v170
	ds_read_b128 v[162:165], v170 offset:1024
	ds_read_b128 v[166:169], v170 offset:2048
	ds_read_b128 v[170:173], v170 offset:3072
	v_lshl_add_u64 v[182:183], s[24:25], 0, v[134:135]
	s_add_i32 m0, s20, 0xc000
	ds_read_b128 v[174:177], v141
	ds_read_b128 v[178:181], v141 offset:1024
	ds_read_b128 v[194:197], v141 offset:2048
	ds_read_b128 v[198:201], v141 offset:3072
	ds_read_b128 v[202:205], v141 offset:4096
	ds_read_b128 v[206:209], v141 offset:5120
	ds_read_b128 v[224:227], v141 offset:6144
	ds_read_b128 v[228:231], v141 offset:7168
	global_load_lds_dwordx4 v[182:183], off
	v_lshl_add_u64 v[182:183], s[24:25], 0, v[136:137]
	s_add_i32 m0, s20, 0xe000
	s_nop 0
	global_load_lds_dwordx4 v[182:183], off
	s_waitcnt vmcnt(8)
	s_waitcnt lgkmcnt(0)
	s_barrier
	s_setprio 0
	s_waitcnt lgkmcnt(0)
	v_mfma_f32_16x16x32_bf16 v[124:127], v[142:145], v[174:177], v[124:127]
	v_mfma_f32_16x16x32_bf16 v[116:119], v[150:153], v[174:177], v[116:119]
	v_mfma_f32_16x16x32_bf16 v[108:111], v[142:145], v[194:197], v[108:111]
	v_mfma_f32_16x16x32_bf16 v[100:103], v[150:153], v[194:197], v[100:103]
	v_mfma_f32_16x16x32_bf16 v[92:95], v[142:145], v[202:205], v[92:95]
	v_mfma_f32_16x16x32_bf16 v[84:87], v[150:153], v[202:205], v[84:87]
	v_mfma_f32_16x16x32_bf16 v[76:79], v[142:145], v[224:227], v[76:79]
	v_mfma_f32_16x16x32_bf16 v[68:71], v[150:153], v[224:227], v[68:71]
	v_mfma_f32_16x16x32_bf16 v[124:127], v[146:149], v[178:181], v[124:127]
	v_mfma_f32_16x16x32_bf16 v[116:119], v[154:157], v[178:181], v[116:119]
	v_mfma_f32_16x16x32_bf16 v[108:111], v[146:149], v[198:201], v[108:111]
	v_mfma_f32_16x16x32_bf16 v[100:103], v[154:157], v[198:201], v[100:103]
	v_mfma_f32_16x16x32_bf16 v[92:95], v[146:149], v[206:209], v[92:95]
	v_mfma_f32_16x16x32_bf16 v[84:87], v[154:157], v[206:209], v[84:87]
	v_mfma_f32_16x16x32_bf16 v[76:79], v[146:149], v[228:231], v[76:79]
	v_mfma_f32_16x16x32_bf16 v[68:71], v[154:157], v[228:231], v[68:71]
	s_setprio 1
	s_setprio 0
	v_mfma_f32_16x16x32_bf16 v[120:123], v[158:161], v[174:177], v[120:123]
	v_mfma_f32_16x16x32_bf16 v[112:115], v[166:169], v[174:177], v[112:115]
	v_mfma_f32_16x16x32_bf16 v[104:107], v[158:161], v[194:197], v[104:107]
	v_mfma_f32_16x16x32_bf16 v[96:99], v[166:169], v[194:197], v[96:99]
	v_mfma_f32_16x16x32_bf16 v[88:91], v[158:161], v[202:205], v[88:91]
	v_mfma_f32_16x16x32_bf16 v[80:83], v[166:169], v[202:205], v[80:83]
	v_mfma_f32_16x16x32_bf16 v[72:75], v[158:161], v[224:227], v[72:75]
	v_mfma_f32_16x16x32_bf16 v[64:67], v[166:169], v[224:227], v[64:67]
	v_mfma_f32_16x16x32_bf16 v[120:123], v[162:165], v[178:181], v[120:123]
	v_mfma_f32_16x16x32_bf16 v[112:115], v[170:173], v[178:181], v[112:115]
	v_mfma_f32_16x16x32_bf16 v[104:107], v[162:165], v[198:201], v[104:107]
	v_mfma_f32_16x16x32_bf16 v[96:99], v[170:173], v[198:201], v[96:99]
	v_mfma_f32_16x16x32_bf16 v[88:91], v[162:165], v[206:209], v[88:91]
	v_mfma_f32_16x16x32_bf16 v[80:83], v[170:173], v[206:209], v[80:83]
	v_mfma_f32_16x16x32_bf16 v[72:75], v[162:165], v[228:231], v[72:75]
	v_mfma_f32_16x16x32_bf16 v[64:67], v[170:173], v[228:231], v[64:67]
	s_setprio 1
	s_barrier
	s_add_i32 s28, s48, s4
	v_lshl_add_u64 v[182:183], s[30:31], 0, v[184:185]
	s_mov_b32 m0, s28
	ds_read_b128 v[174:177], v141 offset:16384
	ds_read_b128 v[178:181], v141 offset:17408
	ds_read_b128 v[194:197], v141 offset:18432
	ds_read_b128 v[198:201], v141 offset:19456
	ds_read_b128 v[202:205], v141 offset:20480
	ds_read_b128 v[206:209], v141 offset:21504
	ds_read_b128 v[224:227], v141 offset:22528
	ds_read_b128 v[228:231], v141 offset:23552
	global_load_lds_dwordx4 v[182:183], off
	s_add_i32 m0, s28, 0x2000
	s_add_u32 s28, s30, 0x80000
	v_lshl_add_u64 v[210:211], s[30:31], 0, v[128:129]
	s_addc_u32 s29, s31, 0
	s_add_i32 s48, s49, s4
	global_load_lds_dwordx4 v[210:211], off
	v_lshl_add_u64 v[216:217], s[28:29], 0, v[184:185]
	s_mov_b32 m0, s48
	v_lshl_add_u64 v[218:219], s[38:39], 0, v[130:131]
	global_load_lds_dwordx4 v[216:217], off
	v_lshl_add_u64 v[216:217], s[28:29], 0, v[128:129]
	s_add_i32 m0, s48, 0x2000
	s_nop 0
	global_load_lds_dwordx4 v[216:217], off
	v_lshl_add_u64 v[216:217], s[38:39], 0, v[132:133]
	s_mov_b32 m0, s20
	s_nop 0
	global_load_lds_dwordx4 v[216:217], off
	s_mov_b32 m0, s21
	s_nop 0
	global_load_lds_dwordx4 v[218:219], off
	s_waitcnt vmcnt(8)
	s_waitcnt lgkmcnt(0)
	s_barrier
	s_setprio 0
	s_waitcnt lgkmcnt(0)
	v_mfma_f32_16x16x32_bf16 v[60:63], v[142:145], v[174:177], v[60:63]
	v_mfma_f32_16x16x32_bf16 v[52:55], v[150:153], v[174:177], v[52:55]
	v_mfma_f32_16x16x32_bf16 v[44:47], v[142:145], v[194:197], v[44:47]
	v_mfma_f32_16x16x32_bf16 v[36:39], v[150:153], v[194:197], v[36:39]
	v_mfma_f32_16x16x32_bf16 v[28:31], v[142:145], v[202:205], v[28:31]
	v_mfma_f32_16x16x32_bf16 v[20:23], v[150:153], v[202:205], v[20:23]
	v_mfma_f32_16x16x32_bf16 v[12:15], v[142:145], v[224:227], v[12:15]
	v_mfma_f32_16x16x32_bf16 v[4:7], v[150:153], v[224:227], v[4:7]
	v_mfma_f32_16x16x32_bf16 v[60:63], v[146:149], v[178:181], v[60:63]
	v_mfma_f32_16x16x32_bf16 v[52:55], v[154:157], v[178:181], v[52:55]
	v_mfma_f32_16x16x32_bf16 v[44:47], v[146:149], v[198:201], v[44:47]
	v_mfma_f32_16x16x32_bf16 v[36:39], v[154:157], v[198:201], v[36:39]
	v_mfma_f32_16x16x32_bf16 v[28:31], v[146:149], v[206:209], v[28:31]
	v_mfma_f32_16x16x32_bf16 v[20:23], v[154:157], v[206:209], v[20:23]
	v_mfma_f32_16x16x32_bf16 v[12:15], v[146:149], v[228:231], v[12:15]
	v_mfma_f32_16x16x32_bf16 v[4:7], v[154:157], v[228:231], v[4:7]
	s_setprio 1
	s_setprio 0
	v_mfma_f32_16x16x32_bf16 v[56:59], v[158:161], v[174:177], v[56:59]
	v_mfma_f32_16x16x32_bf16 v[48:51], v[166:169], v[174:177], v[48:51]
	v_mfma_f32_16x16x32_bf16 v[40:43], v[158:161], v[194:197], v[40:43]
	v_mfma_f32_16x16x32_bf16 v[32:35], v[166:169], v[194:197], v[32:35]
	v_mfma_f32_16x16x32_bf16 v[24:27], v[158:161], v[202:205], v[24:27]
	v_mfma_f32_16x16x32_bf16 v[16:19], v[166:169], v[202:205], v[16:19]
	v_mfma_f32_16x16x32_bf16 v[8:11], v[158:161], v[224:227], v[8:11]
	v_mfma_f32_16x16x32_bf16 v[0:3], v[166:169], v[224:227], v[0:3]
	v_mfma_f32_16x16x32_bf16 v[56:59], v[162:165], v[178:181], v[56:59]
	v_mfma_f32_16x16x32_bf16 v[48:51], v[170:173], v[178:181], v[48:51]
	v_mfma_f32_16x16x32_bf16 v[40:43], v[162:165], v[198:201], v[40:43]
	v_mfma_f32_16x16x32_bf16 v[32:35], v[170:173], v[198:201], v[32:35]
	v_mfma_f32_16x16x32_bf16 v[24:27], v[162:165], v[206:209], v[24:27]
	v_mfma_f32_16x16x32_bf16 v[16:19], v[170:173], v[206:209], v[16:19]
	v_mfma_f32_16x16x32_bf16 v[8:11], v[162:165], v[228:231], v[8:11]
	v_mfma_f32_16x16x32_bf16 v[0:3], v[170:173], v[228:231], v[0:3]
	s_setprio 1
	s_barrier
	s_add_i32 s48, 0, 0x18000
	s_add_i32 s49, 0, 0x1c000
	v_add_u32_e32 v154, s48, v139
	v_add_u32_e32 v170, s49, v139
	ds_read_b128 v[142:145], v154
	ds_read_b128 v[146:149], v154 offset:1024
	ds_read_b128 v[150:153], v154 offset:2048
	ds_read_b128 v[154:157], v154 offset:3072
	ds_read_b128 v[158:161], v170
	ds_read_b128 v[162:165], v170 offset:1024
	ds_read_b128 v[166:169], v170 offset:2048
	ds_read_b128 v[170:173], v170 offset:3072
	s_add_u32 s28, s38, 0x80000
	s_addc_u32 s29, s39, 0
	s_mov_b32 m0, s26
	v_lshl_add_u64 v[232:233], s[28:29], 0, v[132:133]
	ds_read_b128 v[174:177], v141 offset:32768
	ds_read_b128 v[178:181], v141 offset:33792
	ds_read_b128 v[194:197], v141 offset:34816
	ds_read_b128 v[198:201], v141 offset:35840
	ds_read_b128 v[202:205], v141 offset:36864
	ds_read_b128 v[206:209], v141 offset:37888
	ds_read_b128 v[224:227], v141 offset:38912
	ds_read_b128 v[228:231], v141 offset:39936
	global_load_lds_dwordx4 v[232:233], off
	v_lshl_add_u64 v[232:233], s[28:29], 0, v[130:131]
	s_mov_b32 m0, s27
	s_nop 0
	global_load_lds_dwordx4 v[232:233], off
	s_waitcnt vmcnt(8)
	s_waitcnt lgkmcnt(0)
	s_barrier
	s_setprio 0
	s_waitcnt lgkmcnt(0)
	v_mfma_f32_16x16x32_bf16 v[124:127], v[142:145], v[174:177], v[124:127]
	v_mfma_f32_16x16x32_bf16 v[116:119], v[150:153], v[174:177], v[116:119]
	v_mfma_f32_16x16x32_bf16 v[108:111], v[142:145], v[194:197], v[108:111]
	v_mfma_f32_16x16x32_bf16 v[100:103], v[150:153], v[194:197], v[100:103]
	v_mfma_f32_16x16x32_bf16 v[92:95], v[142:145], v[202:205], v[92:95]
	v_mfma_f32_16x16x32_bf16 v[84:87], v[150:153], v[202:205], v[84:87]
	v_mfma_f32_16x16x32_bf16 v[76:79], v[142:145], v[224:227], v[76:79]
	v_mfma_f32_16x16x32_bf16 v[68:71], v[150:153], v[224:227], v[68:71]
	v_mfma_f32_16x16x32_bf16 v[124:127], v[146:149], v[178:181], v[124:127]
	v_mfma_f32_16x16x32_bf16 v[116:119], v[154:157], v[178:181], v[116:119]
	v_mfma_f32_16x16x32_bf16 v[108:111], v[146:149], v[198:201], v[108:111]
	v_mfma_f32_16x16x32_bf16 v[100:103], v[154:157], v[198:201], v[100:103]
	v_mfma_f32_16x16x32_bf16 v[92:95], v[146:149], v[206:209], v[92:95]
	v_mfma_f32_16x16x32_bf16 v[84:87], v[154:157], v[206:209], v[84:87]
	v_mfma_f32_16x16x32_bf16 v[76:79], v[146:149], v[228:231], v[76:79]
	v_mfma_f32_16x16x32_bf16 v[68:71], v[154:157], v[228:231], v[68:71]
	s_setprio 1
	s_setprio 0
	v_mfma_f32_16x16x32_bf16 v[120:123], v[158:161], v[174:177], v[120:123]
	v_mfma_f32_16x16x32_bf16 v[112:115], v[166:169], v[174:177], v[112:115]
	v_mfma_f32_16x16x32_bf16 v[104:107], v[158:161], v[194:197], v[104:107]
	v_mfma_f32_16x16x32_bf16 v[96:99], v[166:169], v[194:197], v[96:99]
	v_mfma_f32_16x16x32_bf16 v[88:91], v[158:161], v[202:205], v[88:91]
	v_mfma_f32_16x16x32_bf16 v[80:83], v[166:169], v[202:205], v[80:83]
	v_mfma_f32_16x16x32_bf16 v[72:75], v[158:161], v[224:227], v[72:75]
	v_mfma_f32_16x16x32_bf16 v[64:67], v[166:169], v[224:227], v[64:67]
	v_mfma_f32_16x16x32_bf16 v[120:123], v[162:165], v[178:181], v[120:123]
	v_mfma_f32_16x16x32_bf16 v[112:115], v[170:173], v[178:181], v[112:115]
	v_mfma_f32_16x16x32_bf16 v[104:107], v[162:165], v[198:201], v[104:107]
	v_mfma_f32_16x16x32_bf16 v[96:99], v[170:173], v[198:201], v[96:99]
	v_mfma_f32_16x16x32_bf16 v[88:91], v[162:165], v[206:209], v[88:91]
	v_mfma_f32_16x16x32_bf16 v[80:83], v[170:173], v[206:209], v[80:83]
	v_mfma_f32_16x16x32_bf16 v[72:75], v[162:165], v[228:231], v[72:75]
	v_mfma_f32_16x16x32_bf16 v[64:67], v[170:173], v[228:231], v[64:67]
	s_setprio 1
	s_barrier
	s_add_i32 s28, s48, s4
	v_lshl_add_u64 v[182:183], v[182:183], 0, s[68:69]
	s_mov_b32 m0, s28
	ds_read_b128 v[174:177], v141 offset:49152
	ds_read_b128 v[178:181], v141 offset:50176
	ds_read_b128 v[194:197], v141 offset:51200
	ds_read_b128 v[198:201], v141 offset:52224
	ds_read_b128 v[202:205], v141 offset:53248
	ds_read_b128 v[206:209], v141 offset:54272
	ds_read_b128 v[224:227], v141 offset:55296
	ds_read_b128 v[228:231], v141 offset:56320
	global_load_lds_dwordx4 v[182:183], off
	s_add_i32 m0, s28, 0x2000
	s_add_u32 s28, s30, 0x80080
	v_lshl_add_u64 v[182:183], v[210:211], 0, s[68:69]
	s_addc_u32 s29, s31, 0
	s_add_i32 s30, s49, s4
	global_load_lds_dwordx4 v[182:183], off
	v_lshl_add_u64 v[182:183], s[28:29], 0, v[184:185]
	s_mov_b32 m0, s30
	s_nop 0
	global_load_lds_dwordx4 v[182:183], off
	v_lshl_add_u64 v[182:183], s[28:29], 0, v[128:129]
	s_add_i32 m0, s30, 0x2000
	s_nop 0
	global_load_lds_dwordx4 v[182:183], off
	v_lshl_add_u64 v[182:183], v[216:217], 0, s[68:69]
	s_mov_b32 m0, s40
	s_nop 0
	global_load_lds_dwordx4 v[182:183], off
	v_lshl_add_u64 v[182:183], v[218:219], 0, s[68:69]
	s_mov_b32 m0, s41
	s_nop 0
	global_load_lds_dwordx4 v[182:183], off
	s_waitcnt vmcnt(8)
	s_waitcnt lgkmcnt(0)
	s_barrier
	s_setprio 0
	s_waitcnt lgkmcnt(0)
	v_mfma_f32_16x16x32_bf16 v[60:63], v[142:145], v[174:177], v[60:63]
	v_mfma_f32_16x16x32_bf16 v[52:55], v[150:153], v[174:177], v[52:55]
	v_mfma_f32_16x16x32_bf16 v[44:47], v[142:145], v[194:197], v[44:47]
	v_mfma_f32_16x16x32_bf16 v[36:39], v[150:153], v[194:197], v[36:39]
	v_mfma_f32_16x16x32_bf16 v[28:31], v[142:145], v[202:205], v[28:31]
	v_mfma_f32_16x16x32_bf16 v[20:23], v[150:153], v[202:205], v[20:23]
	v_mfma_f32_16x16x32_bf16 v[12:15], v[142:145], v[224:227], v[12:15]
	v_mfma_f32_16x16x32_bf16 v[4:7], v[150:153], v[224:227], v[4:7]
	v_mfma_f32_16x16x32_bf16 v[60:63], v[146:149], v[178:181], v[60:63]
	v_mfma_f32_16x16x32_bf16 v[52:55], v[154:157], v[178:181], v[52:55]
	v_mfma_f32_16x16x32_bf16 v[44:47], v[146:149], v[198:201], v[44:47]
	v_mfma_f32_16x16x32_bf16 v[36:39], v[154:157], v[198:201], v[36:39]
	v_mfma_f32_16x16x32_bf16 v[28:31], v[146:149], v[206:209], v[28:31]
	v_mfma_f32_16x16x32_bf16 v[20:23], v[154:157], v[206:209], v[20:23]
	v_mfma_f32_16x16x32_bf16 v[12:15], v[146:149], v[228:231], v[12:15]
	v_mfma_f32_16x16x32_bf16 v[4:7], v[154:157], v[228:231], v[4:7]
	s_setprio 1
	s_setprio 0
	v_mfma_f32_16x16x32_bf16 v[56:59], v[158:161], v[174:177], v[56:59]
	v_mfma_f32_16x16x32_bf16 v[48:51], v[166:169], v[174:177], v[48:51]
	v_mfma_f32_16x16x32_bf16 v[40:43], v[158:161], v[194:197], v[40:43]
	v_mfma_f32_16x16x32_bf16 v[32:35], v[166:169], v[194:197], v[32:35]
	v_mfma_f32_16x16x32_bf16 v[24:27], v[158:161], v[202:205], v[24:27]
	v_mfma_f32_16x16x32_bf16 v[16:19], v[166:169], v[202:205], v[16:19]
	v_mfma_f32_16x16x32_bf16 v[8:11], v[158:161], v[224:227], v[8:11]
	v_mfma_f32_16x16x32_bf16 v[0:3], v[166:169], v[224:227], v[0:3]
	v_mfma_f32_16x16x32_bf16 v[56:59], v[162:165], v[178:181], v[56:59]
	v_mfma_f32_16x16x32_bf16 v[48:51], v[170:173], v[178:181], v[48:51]
	v_mfma_f32_16x16x32_bf16 v[40:43], v[162:165], v[198:201], v[40:43]
	v_mfma_f32_16x16x32_bf16 v[32:35], v[170:173], v[198:201], v[32:35]
	v_mfma_f32_16x16x32_bf16 v[24:27], v[162:165], v[206:209], v[24:27]
	v_mfma_f32_16x16x32_bf16 v[16:19], v[170:173], v[206:209], v[16:19]
	v_mfma_f32_16x16x32_bf16 v[8:11], v[162:165], v[228:231], v[8:11]
	v_mfma_f32_16x16x32_bf16 v[0:3], v[170:173], v[228:231], v[0:3]
	s_setprio 1
	s_barrier
	s_add_i32 s51, s51, 2
	s_add_u32 s24, s24, 0x100
	s_addc_u32 s25, s25, 0
	s_add_u32 s47, s47, 0x100
	s_addc_u32 s50, s50, 0
	s_cmp_gt_u32 s51, 29
	s_cbranch_scc0 .LBB0_1587
	s_and_b64 vcc, exec, s[6:7]
	s_cbranch_vccz .LBB0_1590
	s_barrier

.LBB0_1661:
	s_add_u32 s24, s18, 0x100
	s_addc_u32 s25, s19, 0
	s_add_i32 s28, 0, 0x10000
	s_cmpk_eq_i32 s61, 0x54
	s_cselect_b32 s39, s51, s25
	s_cselect_b32 s38, s52, s24
	s_cselect_b32 s31, s53, s60
	s_cselect_b32 s30, s58, s59
	s_add_i32 s29, 0, 0x14000
	s_waitcnt vmcnt(0)
	v_add_u32_e32 v84, s28, v163
	v_add_u32_e32 v170, s29, v163
	ds_read_b128 v[64:67], v84
	ds_read_b128 v[68:71], v84 offset:1024
	ds_read_b128 v[80:83], v84 offset:2048
	ds_read_b128 v[84:87], v84 offset:3072
	ds_read_b128 v[154:157], v170
	ds_read_b128 v[158:161], v170 offset:1024
	ds_read_b128 v[166:169], v170 offset:2048
	ds_read_b128 v[170:173], v170 offset:3072
	v_lshl_add_u64 v[182:183], s[18:19], 0, v[150:151]
	s_add_i32 m0, s20, 0xc000
	ds_read_b128 v[174:177], v165
	ds_read_b128 v[178:181], v165 offset:1024
	ds_read_b128 v[194:197], v165 offset:2048
	ds_read_b128 v[198:201], v165 offset:3072
	ds_read_b128 v[202:205], v165 offset:4096
	ds_read_b128 v[206:209], v165 offset:5120
	ds_read_b128 v[224:227], v165 offset:6144
	ds_read_b128 v[228:231], v165 offset:7168
	global_load_lds_dwordx4 v[182:183], off
	v_lshl_add_u64 v[182:183], s[18:19], 0, v[152:153]
	s_add_i32 m0, s20, 0xe000
	s_nop 0
	global_load_lds_dwordx4 v[182:183], off
	s_waitcnt vmcnt(8)
	s_waitcnt lgkmcnt(0)
	s_barrier
	s_setprio 0
	s_waitcnt lgkmcnt(0)
	v_mfma_f32_16x16x32_bf16 v[140:143], v[64:67], v[174:177], v[140:143]
	v_mfma_f32_16x16x32_bf16 v[136:139], v[80:83], v[174:177], v[136:139]
	v_mfma_f32_16x16x32_bf16 v[124:127], v[64:67], v[194:197], v[124:127]
	v_mfma_f32_16x16x32_bf16 v[120:123], v[80:83], v[194:197], v[120:123]
	v_mfma_f32_16x16x32_bf16 v[108:111], v[64:67], v[202:205], v[108:111]
	v_mfma_f32_16x16x32_bf16 v[104:107], v[80:83], v[202:205], v[104:107]
	v_mfma_f32_16x16x32_bf16 v[92:95], v[64:67], v[224:227], v[92:95]
	v_mfma_f32_16x16x32_bf16 v[88:91], v[80:83], v[224:227], v[88:91]
	v_mfma_f32_16x16x32_bf16 v[140:143], v[68:71], v[178:181], v[140:143]
	v_mfma_f32_16x16x32_bf16 v[136:139], v[84:87], v[178:181], v[136:139]
	v_mfma_f32_16x16x32_bf16 v[124:127], v[68:71], v[198:201], v[124:127]
	v_mfma_f32_16x16x32_bf16 v[120:123], v[84:87], v[198:201], v[120:123]
	v_mfma_f32_16x16x32_bf16 v[108:111], v[68:71], v[206:209], v[108:111]
	v_mfma_f32_16x16x32_bf16 v[104:107], v[84:87], v[206:209], v[104:107]
	v_mfma_f32_16x16x32_bf16 v[92:95], v[68:71], v[228:231], v[92:95]
	v_mfma_f32_16x16x32_bf16 v[88:91], v[84:87], v[228:231], v[88:91]
	s_setprio 1
	s_setprio 0
	v_mfma_f32_16x16x32_bf16 v[132:135], v[154:157], v[174:177], v[132:135]
	v_mfma_f32_16x16x32_bf16 v[128:131], v[166:169], v[174:177], v[128:131]
	v_mfma_f32_16x16x32_bf16 v[116:119], v[154:157], v[194:197], v[116:119]
	v_mfma_f32_16x16x32_bf16 v[112:115], v[166:169], v[194:197], v[112:115]
	v_mfma_f32_16x16x32_bf16 v[100:103], v[154:157], v[202:205], v[100:103]
	v_mfma_f32_16x16x32_bf16 v[96:99], v[166:169], v[202:205], v[96:99]
	v_mfma_f32_16x16x32_bf16 v[76:79], v[154:157], v[224:227], v[76:79]
	v_mfma_f32_16x16x32_bf16 v[72:75], v[166:169], v[224:227], v[72:75]
	v_mfma_f32_16x16x32_bf16 v[132:135], v[158:161], v[178:181], v[132:135]
	v_mfma_f32_16x16x32_bf16 v[128:131], v[170:173], v[178:181], v[128:131]
	v_mfma_f32_16x16x32_bf16 v[116:119], v[158:161], v[198:201], v[116:119]
	v_mfma_f32_16x16x32_bf16 v[112:115], v[170:173], v[198:201], v[112:115]
	v_mfma_f32_16x16x32_bf16 v[100:103], v[158:161], v[206:209], v[100:103]
	v_mfma_f32_16x16x32_bf16 v[96:99], v[170:173], v[206:209], v[96:99]
	v_mfma_f32_16x16x32_bf16 v[76:79], v[158:161], v[228:231], v[76:79]
	v_mfma_f32_16x16x32_bf16 v[72:75], v[170:173], v[228:231], v[72:75]
	s_setprio 1
	s_barrier
	s_add_i32 s18, s28, s4
	v_lshl_add_u64 v[182:183], s[30:31], 0, v[184:185]
	s_mov_b32 m0, s18
	ds_read_b128 v[174:177], v165 offset:16384
	ds_read_b128 v[178:181], v165 offset:17408
	ds_read_b128 v[194:197], v165 offset:18432
	ds_read_b128 v[198:201], v165 offset:19456
	ds_read_b128 v[202:205], v165 offset:20480
	ds_read_b128 v[206:209], v165 offset:21504
	ds_read_b128 v[224:227], v165 offset:22528
	ds_read_b128 v[228:231], v165 offset:23552
	global_load_lds_dwordx4 v[182:183], off
	s_add_i32 m0, s18, 0x2000
	s_add_u32 s18, s30, 0x160000
	v_lshl_add_u64 v[210:211], s[30:31], 0, v[144:145]
	s_addc_u32 s19, s31, 0
	s_add_i32 s28, s29, s4
	global_load_lds_dwordx4 v[210:211], off
	v_lshl_add_u64 v[216:217], s[18:19], 0, v[184:185]
	s_mov_b32 m0, s28
	v_lshl_add_u64 v[218:219], s[38:39], 0, v[146:147]
	global_load_lds_dwordx4 v[216:217], off
	v_lshl_add_u64 v[216:217], s[18:19], 0, v[144:145]
	s_add_i32 m0, s28, 0x2000
	s_nop 0
	global_load_lds_dwordx4 v[216:217], off
	v_lshl_add_u64 v[216:217], s[38:39], 0, v[148:149]
	s_mov_b32 m0, s20
	s_nop 0
	global_load_lds_dwordx4 v[216:217], off
	s_mov_b32 m0, s21
	s_nop 0
	global_load_lds_dwordx4 v[218:219], off
	s_waitcnt vmcnt(8)
	s_waitcnt lgkmcnt(0)
	s_barrier
	s_setprio 0
	s_waitcnt lgkmcnt(0)
	v_mfma_f32_16x16x32_bf16 v[60:63], v[64:67], v[174:177], v[60:63]
	v_mfma_f32_16x16x32_bf16 v[56:59], v[80:83], v[174:177], v[56:59]
	v_mfma_f32_16x16x32_bf16 v[44:47], v[64:67], v[194:197], v[44:47]
	v_mfma_f32_16x16x32_bf16 v[40:43], v[80:83], v[194:197], v[40:43]
	v_mfma_f32_16x16x32_bf16 v[28:31], v[64:67], v[202:205], v[28:31]
	v_mfma_f32_16x16x32_bf16 v[24:27], v[80:83], v[202:205], v[24:27]
	v_mfma_f32_16x16x32_bf16 v[12:15], v[64:67], v[224:227], v[12:15]
	v_mfma_f32_16x16x32_bf16 v[8:11], v[80:83], v[224:227], v[8:11]
	v_mfma_f32_16x16x32_bf16 v[60:63], v[68:71], v[178:181], v[60:63]
	v_mfma_f32_16x16x32_bf16 v[56:59], v[84:87], v[178:181], v[56:59]
	v_mfma_f32_16x16x32_bf16 v[44:47], v[68:71], v[198:201], v[44:47]
	v_mfma_f32_16x16x32_bf16 v[40:43], v[84:87], v[198:201], v[40:43]
	v_mfma_f32_16x16x32_bf16 v[28:31], v[68:71], v[206:209], v[28:31]
	v_mfma_f32_16x16x32_bf16 v[24:27], v[84:87], v[206:209], v[24:27]
	v_mfma_f32_16x16x32_bf16 v[12:15], v[68:71], v[228:231], v[12:15]
	v_mfma_f32_16x16x32_bf16 v[8:11], v[84:87], v[228:231], v[8:11]
	s_setprio 1
	s_setprio 0
	v_mfma_f32_16x16x32_bf16 v[52:55], v[154:157], v[174:177], v[52:55]
	v_mfma_f32_16x16x32_bf16 v[48:51], v[166:169], v[174:177], v[48:51]
	v_mfma_f32_16x16x32_bf16 v[36:39], v[154:157], v[194:197], v[36:39]
	v_mfma_f32_16x16x32_bf16 v[32:35], v[166:169], v[194:197], v[32:35]
	v_mfma_f32_16x16x32_bf16 v[20:23], v[154:157], v[202:205], v[20:23]
	v_mfma_f32_16x16x32_bf16 v[16:19], v[166:169], v[202:205], v[16:19]
	v_mfma_f32_16x16x32_bf16 v[4:7], v[154:157], v[224:227], v[4:7]
	v_mfma_f32_16x16x32_bf16 v[0:3], v[166:169], v[224:227], v[0:3]
	v_mfma_f32_16x16x32_bf16 v[52:55], v[158:161], v[178:181], v[52:55]
	v_mfma_f32_16x16x32_bf16 v[48:51], v[170:173], v[178:181], v[48:51]
	v_mfma_f32_16x16x32_bf16 v[36:39], v[158:161], v[198:201], v[36:39]
	v_mfma_f32_16x16x32_bf16 v[32:35], v[170:173], v[198:201], v[32:35]
	v_mfma_f32_16x16x32_bf16 v[20:23], v[158:161], v[206:209], v[20:23]
	v_mfma_f32_16x16x32_bf16 v[16:19], v[170:173], v[206:209], v[16:19]
	v_mfma_f32_16x16x32_bf16 v[4:7], v[158:161], v[228:231], v[4:7]
	v_mfma_f32_16x16x32_bf16 v[0:3], v[170:173], v[228:231], v[0:3]
	s_setprio 1
	s_barrier
	s_add_i32 s28, 0, 0x18000
	s_add_i32 s29, 0, 0x1c000
	v_add_u32_e32 v84, s28, v163
	v_add_u32_e32 v170, s29, v163
	ds_read_b128 v[64:67], v84
	ds_read_b128 v[68:71], v84 offset:1024
	ds_read_b128 v[80:83], v84 offset:2048
	ds_read_b128 v[84:87], v84 offset:3072
	ds_read_b128 v[154:157], v170
	ds_read_b128 v[158:161], v170 offset:1024
	ds_read_b128 v[166:169], v170 offset:2048
	ds_read_b128 v[170:173], v170 offset:3072
	s_add_u32 s18, s38, 0x160000
	s_addc_u32 s19, s39, 0
	s_mov_b32 m0, s26
	v_lshl_add_u64 v[232:233], s[18:19], 0, v[148:149]
	ds_read_b128 v[174:177], v165 offset:32768
	ds_read_b128 v[178:181], v165 offset:33792
	ds_read_b128 v[194:197], v165 offset:34816
	ds_read_b128 v[198:201], v165 offset:35840
	ds_read_b128 v[202:205], v165 offset:36864
	ds_read_b128 v[206:209], v165 offset:37888
	ds_read_b128 v[224:227], v165 offset:38912
	ds_read_b128 v[228:231], v165 offset:39936
	global_load_lds_dwordx4 v[232:233], off
	v_lshl_add_u64 v[232:233], s[18:19], 0, v[146:147]
	s_mov_b32 m0, s27
	s_nop 0
	global_load_lds_dwordx4 v[232:233], off
	s_waitcnt vmcnt(8)
	s_waitcnt lgkmcnt(0)
	s_barrier
	s_setprio 0
	s_waitcnt lgkmcnt(0)
	v_mfma_f32_16x16x32_bf16 v[140:143], v[64:67], v[174:177], v[140:143]
	v_mfma_f32_16x16x32_bf16 v[136:139], v[80:83], v[174:177], v[136:139]
	v_mfma_f32_16x16x32_bf16 v[124:127], v[64:67], v[194:197], v[124:127]
	v_mfma_f32_16x16x32_bf16 v[120:123], v[80:83], v[194:197], v[120:123]
	v_mfma_f32_16x16x32_bf16 v[108:111], v[64:67], v[202:205], v[108:111]
	v_mfma_f32_16x16x32_bf16 v[104:107], v[80:83], v[202:205], v[104:107]
	v_mfma_f32_16x16x32_bf16 v[92:95], v[64:67], v[224:227], v[92:95]
	v_mfma_f32_16x16x32_bf16 v[88:91], v[80:83], v[224:227], v[88:91]
	v_mfma_f32_16x16x32_bf16 v[140:143], v[68:71], v[178:181], v[140:143]
	v_mfma_f32_16x16x32_bf16 v[136:139], v[84:87], v[178:181], v[136:139]
	v_mfma_f32_16x16x32_bf16 v[124:127], v[68:71], v[198:201], v[124:127]
	v_mfma_f32_16x16x32_bf16 v[120:123], v[84:87], v[198:201], v[120:123]
	v_mfma_f32_16x16x32_bf16 v[108:111], v[68:71], v[206:209], v[108:111]
	v_mfma_f32_16x16x32_bf16 v[104:107], v[84:87], v[206:209], v[104:107]
	v_mfma_f32_16x16x32_bf16 v[92:95], v[68:71], v[228:231], v[92:95]
	v_mfma_f32_16x16x32_bf16 v[88:91], v[84:87], v[228:231], v[88:91]
	s_setprio 1
	s_setprio 0
	v_mfma_f32_16x16x32_bf16 v[132:135], v[154:157], v[174:177], v[132:135]
	v_mfma_f32_16x16x32_bf16 v[128:131], v[166:169], v[174:177], v[128:131]
	v_mfma_f32_16x16x32_bf16 v[116:119], v[154:157], v[194:197], v[116:119]
	v_mfma_f32_16x16x32_bf16 v[112:115], v[166:169], v[194:197], v[112:115]
	v_mfma_f32_16x16x32_bf16 v[100:103], v[154:157], v[202:205], v[100:103]
	v_mfma_f32_16x16x32_bf16 v[96:99], v[166:169], v[202:205], v[96:99]
	v_mfma_f32_16x16x32_bf16 v[76:79], v[154:157], v[224:227], v[76:79]
	v_mfma_f32_16x16x32_bf16 v[72:75], v[166:169], v[224:227], v[72:75]
	v_mfma_f32_16x16x32_bf16 v[132:135], v[158:161], v[178:181], v[132:135]
	v_mfma_f32_16x16x32_bf16 v[128:131], v[170:173], v[178:181], v[128:131]
	v_mfma_f32_16x16x32_bf16 v[116:119], v[158:161], v[198:201], v[116:119]
	v_mfma_f32_16x16x32_bf16 v[112:115], v[170:173], v[198:201], v[112:115]
	v_mfma_f32_16x16x32_bf16 v[100:103], v[158:161], v[206:209], v[100:103]
	v_mfma_f32_16x16x32_bf16 v[96:99], v[170:173], v[206:209], v[96:99]
	v_mfma_f32_16x16x32_bf16 v[76:79], v[158:161], v[228:231], v[76:79]
	v_mfma_f32_16x16x32_bf16 v[72:75], v[170:173], v[228:231], v[72:75]
	s_setprio 1
	s_barrier
	s_add_i32 s18, s28, s4
	v_lshl_add_u64 v[182:183], v[182:183], 0, s[68:69]
	s_mov_b32 m0, s18
	ds_read_b128 v[174:177], v165 offset:49152
	ds_read_b128 v[178:181], v165 offset:50176
	ds_read_b128 v[194:197], v165 offset:51200
	ds_read_b128 v[198:201], v165 offset:52224
	ds_read_b128 v[202:205], v165 offset:53248
	ds_read_b128 v[206:209], v165 offset:54272
	ds_read_b128 v[224:227], v165 offset:55296
	ds_read_b128 v[228:231], v165 offset:56320
	global_load_lds_dwordx4 v[182:183], off
	s_add_i32 m0, s18, 0x2000
	s_add_u32 s18, s30, 0x160080
	v_lshl_add_u64 v[182:183], v[210:211], 0, s[68:69]
	s_addc_u32 s19, s31, 0
	s_add_i32 s28, s29, s4
	global_load_lds_dwordx4 v[182:183], off
	v_lshl_add_u64 v[182:183], s[18:19], 0, v[184:185]
	s_mov_b32 m0, s28
	s_nop 0
	global_load_lds_dwordx4 v[182:183], off
	v_lshl_add_u64 v[182:183], s[18:19], 0, v[144:145]
	s_add_i32 m0, s28, 0x2000
	s_nop 0
	global_load_lds_dwordx4 v[182:183], off
	v_lshl_add_u64 v[182:183], v[216:217], 0, s[68:69]
	s_mov_b32 m0, s42
	s_nop 0
	global_load_lds_dwordx4 v[182:183], off
	v_lshl_add_u64 v[182:183], v[218:219], 0, s[68:69]
	s_mov_b32 m0, s43
	s_nop 0
	global_load_lds_dwordx4 v[182:183], off
	s_waitcnt vmcnt(8)
	s_waitcnt lgkmcnt(0)
	s_barrier
	s_setprio 0
	s_waitcnt lgkmcnt(0)
	v_mfma_f32_16x16x32_bf16 v[60:63], v[64:67], v[174:177], v[60:63]
	v_mfma_f32_16x16x32_bf16 v[56:59], v[80:83], v[174:177], v[56:59]
	v_mfma_f32_16x16x32_bf16 v[44:47], v[64:67], v[194:197], v[44:47]
	v_mfma_f32_16x16x32_bf16 v[40:43], v[80:83], v[194:197], v[40:43]
	v_mfma_f32_16x16x32_bf16 v[28:31], v[64:67], v[202:205], v[28:31]
	v_mfma_f32_16x16x32_bf16 v[24:27], v[80:83], v[202:205], v[24:27]
	v_mfma_f32_16x16x32_bf16 v[12:15], v[64:67], v[224:227], v[12:15]
	v_mfma_f32_16x16x32_bf16 v[8:11], v[80:83], v[224:227], v[8:11]
	v_mfma_f32_16x16x32_bf16 v[60:63], v[68:71], v[178:181], v[60:63]
	v_mfma_f32_16x16x32_bf16 v[56:59], v[84:87], v[178:181], v[56:59]
	v_mfma_f32_16x16x32_bf16 v[44:47], v[68:71], v[198:201], v[44:47]
	v_mfma_f32_16x16x32_bf16 v[40:43], v[84:87], v[198:201], v[40:43]
	v_mfma_f32_16x16x32_bf16 v[28:31], v[68:71], v[206:209], v[28:31]
	v_mfma_f32_16x16x32_bf16 v[24:27], v[84:87], v[206:209], v[24:27]
	v_mfma_f32_16x16x32_bf16 v[12:15], v[68:71], v[228:231], v[12:15]
	v_mfma_f32_16x16x32_bf16 v[8:11], v[84:87], v[228:231], v[8:11]
	s_setprio 1
	s_setprio 0
	v_mfma_f32_16x16x32_bf16 v[52:55], v[154:157], v[174:177], v[52:55]
	v_mfma_f32_16x16x32_bf16 v[48:51], v[166:169], v[174:177], v[48:51]
	v_mfma_f32_16x16x32_bf16 v[36:39], v[154:157], v[194:197], v[36:39]
	v_mfma_f32_16x16x32_bf16 v[32:35], v[166:169], v[194:197], v[32:35]
	v_mfma_f32_16x16x32_bf16 v[20:23], v[154:157], v[202:205], v[20:23]
	v_mfma_f32_16x16x32_bf16 v[16:19], v[166:169], v[202:205], v[16:19]
	v_mfma_f32_16x16x32_bf16 v[4:7], v[154:157], v[224:227], v[4:7]
	v_mfma_f32_16x16x32_bf16 v[0:3], v[166:169], v[224:227], v[0:3]
	v_mfma_f32_16x16x32_bf16 v[52:55], v[158:161], v[178:181], v[52:55]
	v_mfma_f32_16x16x32_bf16 v[48:51], v[170:173], v[178:181], v[48:51]
	v_mfma_f32_16x16x32_bf16 v[36:39], v[158:161], v[198:201], v[36:39]
	v_mfma_f32_16x16x32_bf16 v[32:35], v[170:173], v[198:201], v[32:35]
	v_mfma_f32_16x16x32_bf16 v[20:23], v[158:161], v[206:209], v[20:23]
	v_mfma_f32_16x16x32_bf16 v[16:19], v[170:173], v[206:209], v[16:19]
	v_mfma_f32_16x16x32_bf16 v[4:7], v[158:161], v[228:231], v[4:7]
	v_mfma_f32_16x16x32_bf16 v[0:3], v[170:173], v[228:231], v[0:3]
	s_setprio 1
	s_barrier
	s_add_i32 s61, s61, 2
	s_add_u32 s59, s59, 0x100
	s_addc_u32 s60, s60, 0
	s_cmpk_gt_u32 s61, 0x55
	s_mov_b64 s[18:19], s[24:25]
	s_cbranch_scc0 .LBB0_1661
	s_and_b64 vcc, exec, s[8:9]
	s_cbranch_vccz .LBB0_1664
	s_barrier

.LBB0_1741:
	s_add_u32 s38, s36, 0x100
	s_addc_u32 s39, s37, 0
	s_add_i32 s28, 0, 0x10000
	s_cmp_eq_u32 s59, 4
	s_cselect_b32 s43, s11, s39
	s_cselect_b32 s42, s50, s38
	s_cselect_b32 s41, s51, s58
	s_cselect_b32 s40, s52, s53
	s_add_i32 s48, 0, 0x14000
	v_add_u32_e32 v124, s28, v172
	v_add_u32_e32 v170, s48, v172
	ds_read_b128 v[112:115], v124
	ds_read_b128 v[116:119], v124 offset:1024
	ds_read_b128 v[120:123], v124 offset:2048
	ds_read_b128 v[124:127], v124 offset:3072
	ds_read_b128 v[176:179], v170
	ds_read_b128 v[180:183], v170 offset:1024
	ds_read_b128 v[194:197], v170 offset:2048
	ds_read_b128 v[198:201], v170 offset:3072
	v_lshl_add_u64 v[170:171], s[36:37], 0, v[166:167]
	s_add_i32 m0, s20, 0xc000
	ds_read_b128 v[202:205], v174
	ds_read_b128 v[206:209], v174 offset:1024
	ds_read_b128 v[224:227], v174 offset:2048
	ds_read_b128 v[228:231], v174 offset:3072
	ds_read_b128 v[232:235], v174 offset:4096
	ds_read_b128 v[236:239], v174 offset:5120
	ds_read_b128 v[240:243], v174 offset:6144
	ds_read_b128 v[244:247], v174 offset:7168
	global_load_lds_dwordx4 v[170:171], off
	v_lshl_add_u64 v[170:171], s[36:37], 0, v[168:169]
	s_add_i32 m0, s20, 0xe000
	s_nop 0
	global_load_lds_dwordx4 v[170:171], off
	s_waitcnt vmcnt(8)
	s_waitcnt lgkmcnt(0)
	s_barrier
	s_setprio 0
	s_waitcnt lgkmcnt(0)
	v_mfma_f32_16x16x32_bf16 v[140:143], v[112:115], v[202:205], v[140:143]
	v_mfma_f32_16x16x32_bf16 v[136:139], v[120:123], v[202:205], v[136:139]
	v_mfma_f32_16x16x32_bf16 v[108:111], v[112:115], v[224:227], v[108:111]
	v_mfma_f32_16x16x32_bf16 v[104:107], v[120:123], v[224:227], v[104:107]
	v_mfma_f32_16x16x32_bf16 v[92:95], v[112:115], v[232:235], v[92:95]
	v_mfma_f32_16x16x32_bf16 v[88:91], v[120:123], v[232:235], v[88:91]
	v_mfma_f32_16x16x32_bf16 v[76:79], v[112:115], v[240:243], v[76:79]
	v_mfma_f32_16x16x32_bf16 v[72:75], v[120:123], v[240:243], v[72:75]
	v_mfma_f32_16x16x32_bf16 v[140:143], v[116:119], v[206:209], v[140:143]
	v_mfma_f32_16x16x32_bf16 v[136:139], v[124:127], v[206:209], v[136:139]
	v_mfma_f32_16x16x32_bf16 v[108:111], v[116:119], v[228:231], v[108:111]
	v_mfma_f32_16x16x32_bf16 v[104:107], v[124:127], v[228:231], v[104:107]
	v_mfma_f32_16x16x32_bf16 v[92:95], v[116:119], v[236:239], v[92:95]
	v_mfma_f32_16x16x32_bf16 v[88:91], v[124:127], v[236:239], v[88:91]
	v_mfma_f32_16x16x32_bf16 v[76:79], v[116:119], v[244:247], v[76:79]
	v_mfma_f32_16x16x32_bf16 v[72:75], v[124:127], v[244:247], v[72:75]
	s_setprio 1
	s_setprio 0
	v_mfma_f32_16x16x32_bf16 v[132:135], v[176:179], v[202:205], v[132:135]
	v_mfma_f32_16x16x32_bf16 v[128:131], v[194:197], v[202:205], v[128:131]
	v_mfma_f32_16x16x32_bf16 v[100:103], v[176:179], v[224:227], v[100:103]
	v_mfma_f32_16x16x32_bf16 v[96:99], v[194:197], v[224:227], v[96:99]
	v_mfma_f32_16x16x32_bf16 v[84:87], v[176:179], v[232:235], v[84:87]
	v_mfma_f32_16x16x32_bf16 v[80:83], v[194:197], v[232:235], v[80:83]
	v_mfma_f32_16x16x32_bf16 v[68:71], v[176:179], v[240:243], v[68:71]
	v_mfma_f32_16x16x32_bf16 v[64:67], v[194:197], v[240:243], v[64:67]
	v_mfma_f32_16x16x32_bf16 v[132:135], v[180:183], v[206:209], v[132:135]
	v_mfma_f32_16x16x32_bf16 v[128:131], v[198:201], v[206:209], v[128:131]
	v_mfma_f32_16x16x32_bf16 v[100:103], v[180:183], v[228:231], v[100:103]
	v_mfma_f32_16x16x32_bf16 v[96:99], v[198:201], v[228:231], v[96:99]
	v_mfma_f32_16x16x32_bf16 v[84:87], v[180:183], v[236:239], v[84:87]
	v_mfma_f32_16x16x32_bf16 v[80:83], v[198:201], v[236:239], v[80:83]
	v_mfma_f32_16x16x32_bf16 v[68:71], v[180:183], v[244:247], v[68:71]
	v_mfma_f32_16x16x32_bf16 v[64:67], v[198:201], v[244:247], v[64:67]
	s_setprio 1
	s_barrier
	s_add_i32 s28, s28, s4
	v_lshl_add_u64 v[170:171], s[40:41], 0, v[184:185]
	s_mov_b32 m0, s28
	ds_read_b128 v[202:205], v174 offset:16384
	ds_read_b128 v[206:209], v174 offset:17408
	ds_read_b128 v[224:227], v174 offset:18432
	ds_read_b128 v[228:231], v174 offset:19456
	ds_read_b128 v[232:235], v174 offset:20480
	ds_read_b128 v[236:239], v174 offset:21504
	ds_read_b128 v[240:243], v174 offset:22528
	ds_read_b128 v[244:247], v174 offset:23552
	global_load_lds_dwordx4 v[170:171], off
	s_add_i32 m0, s28, 0x2000
	s_add_u32 s28, s40, 0x160000
	v_lshl_add_u64 v[210:211], s[40:41], 0, v[144:145]
	s_addc_u32 s29, s41, 0
	s_add_i32 s36, s48, s4
	global_load_lds_dwordx4 v[210:211], off
	v_lshl_add_u64 v[216:217], s[28:29], 0, v[184:185]
	s_mov_b32 m0, s36
	v_lshl_add_u64 v[218:219], s[42:43], 0, v[146:147]
	global_load_lds_dwordx4 v[216:217], off
	v_lshl_add_u64 v[216:217], s[28:29], 0, v[144:145]
	s_add_i32 m0, s36, 0x2000
	s_nop 0
	global_load_lds_dwordx4 v[216:217], off
	v_lshl_add_u64 v[216:217], s[42:43], 0, v[148:149]
	s_mov_b32 m0, s20
	s_nop 0
	global_load_lds_dwordx4 v[216:217], off
	s_mov_b32 m0, s21
	s_nop 0
	global_load_lds_dwordx4 v[218:219], off
	s_waitcnt vmcnt(8)
	s_waitcnt lgkmcnt(0)
	s_barrier
	s_setprio 0
	s_waitcnt lgkmcnt(0)
	v_mfma_f32_16x16x32_bf16 v[60:63], v[112:115], v[202:205], v[60:63]
	v_mfma_f32_16x16x32_bf16 v[56:59], v[120:123], v[202:205], v[56:59]
	v_mfma_f32_16x16x32_bf16 v[44:47], v[112:115], v[224:227], v[44:47]
	v_mfma_f32_16x16x32_bf16 v[40:43], v[120:123], v[224:227], v[40:43]
	v_mfma_f32_16x16x32_bf16 v[36:39], v[112:115], v[232:235], v[36:39]
	v_mfma_f32_16x16x32_bf16 v[28:31], v[120:123], v[232:235], v[28:31]
	v_mfma_f32_16x16x32_bf16 v[20:23], v[112:115], v[240:243], v[20:23]
	v_mfma_f32_16x16x32_bf16 v[12:15], v[120:123], v[240:243], v[12:15]
	v_mfma_f32_16x16x32_bf16 v[60:63], v[116:119], v[206:209], v[60:63]
	v_mfma_f32_16x16x32_bf16 v[56:59], v[124:127], v[206:209], v[56:59]
	v_mfma_f32_16x16x32_bf16 v[44:47], v[116:119], v[228:231], v[44:47]
	v_mfma_f32_16x16x32_bf16 v[40:43], v[124:127], v[228:231], v[40:43]
	v_mfma_f32_16x16x32_bf16 v[36:39], v[116:119], v[236:239], v[36:39]
	v_mfma_f32_16x16x32_bf16 v[28:31], v[124:127], v[236:239], v[28:31]
	v_mfma_f32_16x16x32_bf16 v[20:23], v[116:119], v[244:247], v[20:23]
	v_mfma_f32_16x16x32_bf16 v[12:15], v[124:127], v[244:247], v[12:15]
	s_setprio 1
	s_setprio 0
	v_mfma_f32_16x16x32_bf16 v[52:55], v[176:179], v[202:205], v[52:55]
	v_mfma_f32_16x16x32_bf16 v[48:51], v[194:197], v[202:205], v[48:51]
	v_mfma_f32_16x16x32_bf16 v[32:35], v[176:179], v[224:227], v[32:35]
	v_mfma_f32_16x16x32_bf16 v[24:27], v[194:197], v[224:227], v[24:27]
	v_mfma_f32_16x16x32_bf16 v[16:19], v[176:179], v[232:235], v[16:19]
	v_mfma_f32_16x16x32_bf16 v[8:11], v[194:197], v[232:235], v[8:11]
	v_mfma_f32_16x16x32_bf16 v[4:7], v[176:179], v[240:243], v[4:7]
	v_mfma_f32_16x16x32_bf16 v[0:3], v[194:197], v[240:243], v[0:3]
	v_mfma_f32_16x16x32_bf16 v[52:55], v[180:183], v[206:209], v[52:55]
	v_mfma_f32_16x16x32_bf16 v[48:51], v[198:201], v[206:209], v[48:51]
	v_mfma_f32_16x16x32_bf16 v[32:35], v[180:183], v[228:231], v[32:35]
	v_mfma_f32_16x16x32_bf16 v[24:27], v[198:201], v[228:231], v[24:27]
	v_mfma_f32_16x16x32_bf16 v[16:19], v[180:183], v[236:239], v[16:19]
	v_mfma_f32_16x16x32_bf16 v[8:11], v[198:201], v[236:239], v[8:11]
	v_mfma_f32_16x16x32_bf16 v[4:7], v[180:183], v[244:247], v[4:7]
	v_mfma_f32_16x16x32_bf16 v[0:3], v[198:201], v[244:247], v[0:3]
	s_setprio 1
	s_barrier
	s_add_i32 s36, 0, 0x18000
	s_add_i32 s37, 0, 0x1c000
	v_add_u32_e32 v124, s36, v172
	v_add_u32_e32 v175, s37, v172
	ds_read_b128 v[112:115], v124
	ds_read_b128 v[116:119], v124 offset:1024
	ds_read_b128 v[120:123], v124 offset:2048
	ds_read_b128 v[124:127], v124 offset:3072
	ds_read_b128 v[176:179], v175
	ds_read_b128 v[180:183], v175 offset:1024
	ds_read_b128 v[194:197], v175 offset:2048
	ds_read_b128 v[198:201], v175 offset:3072
	s_add_u32 s28, s42, 0x160000
	s_addc_u32 s29, s43, 0
	s_mov_b32 m0, s26
	v_lshl_add_u64 v[220:221], s[28:29], 0, v[148:149]
	ds_read_b128 v[202:205], v174 offset:32768
	ds_read_b128 v[206:209], v174 offset:33792
	ds_read_b128 v[224:227], v174 offset:34816
	ds_read_b128 v[228:231], v174 offset:35840
	ds_read_b128 v[232:235], v174 offset:36864
	ds_read_b128 v[236:239], v174 offset:37888
	ds_read_b128 v[240:243], v174 offset:38912
	ds_read_b128 v[244:247], v174 offset:39936
	global_load_lds_dwordx4 v[220:221], off
	v_lshl_add_u64 v[220:221], s[28:29], 0, v[146:147]
	s_mov_b32 m0, s27
	s_nop 0
	global_load_lds_dwordx4 v[220:221], off
	s_waitcnt vmcnt(8)
	s_waitcnt lgkmcnt(0)
	s_barrier
	s_setprio 0
	s_waitcnt lgkmcnt(0)
	v_mfma_f32_16x16x32_bf16 v[140:143], v[112:115], v[202:205], v[140:143]
	v_mfma_f32_16x16x32_bf16 v[136:139], v[120:123], v[202:205], v[136:139]
	v_mfma_f32_16x16x32_bf16 v[108:111], v[112:115], v[224:227], v[108:111]
	v_mfma_f32_16x16x32_bf16 v[104:107], v[120:123], v[224:227], v[104:107]
	v_mfma_f32_16x16x32_bf16 v[92:95], v[112:115], v[232:235], v[92:95]
	v_mfma_f32_16x16x32_bf16 v[88:91], v[120:123], v[232:235], v[88:91]
	v_mfma_f32_16x16x32_bf16 v[76:79], v[112:115], v[240:243], v[76:79]
	v_mfma_f32_16x16x32_bf16 v[72:75], v[120:123], v[240:243], v[72:75]
	v_mfma_f32_16x16x32_bf16 v[140:143], v[116:119], v[206:209], v[140:143]
	v_mfma_f32_16x16x32_bf16 v[136:139], v[124:127], v[206:209], v[136:139]
	v_mfma_f32_16x16x32_bf16 v[108:111], v[116:119], v[228:231], v[108:111]
	v_mfma_f32_16x16x32_bf16 v[104:107], v[124:127], v[228:231], v[104:107]
	v_mfma_f32_16x16x32_bf16 v[92:95], v[116:119], v[236:239], v[92:95]
	v_mfma_f32_16x16x32_bf16 v[88:91], v[124:127], v[236:239], v[88:91]
	v_mfma_f32_16x16x32_bf16 v[76:79], v[116:119], v[244:247], v[76:79]
	v_mfma_f32_16x16x32_bf16 v[72:75], v[124:127], v[244:247], v[72:75]
	s_setprio 1
	s_setprio 0
	v_mfma_f32_16x16x32_bf16 v[132:135], v[176:179], v[202:205], v[132:135]
	v_mfma_f32_16x16x32_bf16 v[128:131], v[194:197], v[202:205], v[128:131]
	v_mfma_f32_16x16x32_bf16 v[100:103], v[176:179], v[224:227], v[100:103]
	v_mfma_f32_16x16x32_bf16 v[96:99], v[194:197], v[224:227], v[96:99]
	v_mfma_f32_16x16x32_bf16 v[84:87], v[176:179], v[232:235], v[84:87]
	v_mfma_f32_16x16x32_bf16 v[80:83], v[194:197], v[232:235], v[80:83]
	v_mfma_f32_16x16x32_bf16 v[68:71], v[176:179], v[240:243], v[68:71]
	v_mfma_f32_16x16x32_bf16 v[64:67], v[194:197], v[240:243], v[64:67]
	v_mfma_f32_16x16x32_bf16 v[132:135], v[180:183], v[206:209], v[132:135]
	v_mfma_f32_16x16x32_bf16 v[128:131], v[198:201], v[206:209], v[128:131]
	v_mfma_f32_16x16x32_bf16 v[100:103], v[180:183], v[228:231], v[100:103]
	v_mfma_f32_16x16x32_bf16 v[96:99], v[198:201], v[228:231], v[96:99]
	v_mfma_f32_16x16x32_bf16 v[84:87], v[180:183], v[236:239], v[84:87]
	v_mfma_f32_16x16x32_bf16 v[80:83], v[198:201], v[236:239], v[80:83]
	v_mfma_f32_16x16x32_bf16 v[68:71], v[180:183], v[244:247], v[68:71]
	v_mfma_f32_16x16x32_bf16 v[64:67], v[198:201], v[244:247], v[64:67]
	s_setprio 1
	s_barrier
	s_add_i32 s28, s36, s4
	v_lshl_add_u64 v[170:171], v[170:171], 0, s[68:69]
	s_mov_b32 m0, s28
	ds_read_b128 v[202:205], v174 offset:49152
	ds_read_b128 v[206:209], v174 offset:50176
	ds_read_b128 v[224:227], v174 offset:51200
	ds_read_b128 v[228:231], v174 offset:52224
	ds_read_b128 v[232:235], v174 offset:53248
	ds_read_b128 v[236:239], v174 offset:54272
	ds_read_b128 v[240:243], v174 offset:55296
	ds_read_b128 v[244:247], v174 offset:56320
	global_load_lds_dwordx4 v[170:171], off
	s_add_i32 m0, s28, 0x2000
	s_add_u32 s28, s40, 0x160080
	v_lshl_add_u64 v[170:171], v[210:211], 0, s[68:69]
	s_addc_u32 s29, s41, 0
	s_add_i32 s36, s37, s4
	global_load_lds_dwordx4 v[170:171], off
	v_lshl_add_u64 v[170:171], s[28:29], 0, v[184:185]
	s_mov_b32 m0, s36
	s_nop 0
	global_load_lds_dwordx4 v[170:171], off
	v_lshl_add_u64 v[170:171], s[28:29], 0, v[144:145]
	s_add_i32 m0, s36, 0x2000
	s_nop 0
	global_load_lds_dwordx4 v[170:171], off
	v_lshl_add_u64 v[170:171], v[216:217], 0, s[68:69]
	s_mov_b32 m0, s44
	s_nop 0
	global_load_lds_dwordx4 v[170:171], off
	v_lshl_add_u64 v[170:171], v[218:219], 0, s[68:69]
	s_mov_b32 m0, s45
	s_nop 0
	global_load_lds_dwordx4 v[170:171], off
	s_waitcnt vmcnt(8)
	s_waitcnt lgkmcnt(0)
	s_barrier
	s_setprio 0
	s_waitcnt lgkmcnt(0)
	v_mfma_f32_16x16x32_bf16 v[60:63], v[112:115], v[202:205], v[60:63]
	v_mfma_f32_16x16x32_bf16 v[56:59], v[120:123], v[202:205], v[56:59]
	v_mfma_f32_16x16x32_bf16 v[44:47], v[112:115], v[224:227], v[44:47]
	v_mfma_f32_16x16x32_bf16 v[40:43], v[120:123], v[224:227], v[40:43]
	v_mfma_f32_16x16x32_bf16 v[36:39], v[112:115], v[232:235], v[36:39]
	v_mfma_f32_16x16x32_bf16 v[28:31], v[120:123], v[232:235], v[28:31]
	v_mfma_f32_16x16x32_bf16 v[20:23], v[112:115], v[240:243], v[20:23]
	v_mfma_f32_16x16x32_bf16 v[12:15], v[120:123], v[240:243], v[12:15]
	v_mfma_f32_16x16x32_bf16 v[60:63], v[116:119], v[206:209], v[60:63]
	v_mfma_f32_16x16x32_bf16 v[56:59], v[124:127], v[206:209], v[56:59]
	v_mfma_f32_16x16x32_bf16 v[44:47], v[116:119], v[228:231], v[44:47]
	v_mfma_f32_16x16x32_bf16 v[40:43], v[124:127], v[228:231], v[40:43]
	v_mfma_f32_16x16x32_bf16 v[36:39], v[116:119], v[236:239], v[36:39]
	v_mfma_f32_16x16x32_bf16 v[28:31], v[124:127], v[236:239], v[28:31]
	v_mfma_f32_16x16x32_bf16 v[20:23], v[116:119], v[244:247], v[20:23]
	v_mfma_f32_16x16x32_bf16 v[12:15], v[124:127], v[244:247], v[12:15]
	s_setprio 1
	s_setprio 0
	v_mfma_f32_16x16x32_bf16 v[52:55], v[176:179], v[202:205], v[52:55]
	v_mfma_f32_16x16x32_bf16 v[48:51], v[194:197], v[202:205], v[48:51]
	v_mfma_f32_16x16x32_bf16 v[32:35], v[176:179], v[224:227], v[32:35]
	v_mfma_f32_16x16x32_bf16 v[24:27], v[194:197], v[224:227], v[24:27]
	v_mfma_f32_16x16x32_bf16 v[16:19], v[176:179], v[232:235], v[16:19]
	v_mfma_f32_16x16x32_bf16 v[8:11], v[194:197], v[232:235], v[8:11]
	v_mfma_f32_16x16x32_bf16 v[4:7], v[176:179], v[240:243], v[4:7]
	v_mfma_f32_16x16x32_bf16 v[0:3], v[194:197], v[240:243], v[0:3]
	v_mfma_f32_16x16x32_bf16 v[52:55], v[180:183], v[206:209], v[52:55]
	v_mfma_f32_16x16x32_bf16 v[48:51], v[198:201], v[206:209], v[48:51]
	v_mfma_f32_16x16x32_bf16 v[32:35], v[180:183], v[228:231], v[32:35]
	v_mfma_f32_16x16x32_bf16 v[24:27], v[198:201], v[228:231], v[24:27]
	v_mfma_f32_16x16x32_bf16 v[16:19], v[180:183], v[236:239], v[16:19]
	v_mfma_f32_16x16x32_bf16 v[8:11], v[198:201], v[236:239], v[8:11]
	v_mfma_f32_16x16x32_bf16 v[4:7], v[180:183], v[244:247], v[4:7]
	v_mfma_f32_16x16x32_bf16 v[0:3], v[198:201], v[244:247], v[0:3]
	s_setprio 1
	s_barrier
	s_add_i32 s59, s59, 2
	s_add_u32 s53, s53, 0x100
	s_addc_u32 s58, s58, 0
	s_cmp_gt_u32 s59, 5
	s_mov_b64 s[36:37], s[38:39]
	s_cbranch_scc0 .LBB0_1741
	s_and_b64 vcc, exec, s[8:9]
	s_cbranch_vccz .LBB0_1744
	s_barrier
